# chunk-state units (SSD, mLSTM): transposed MFMA accumulators so f32 state tiles leave as 16-byte stores (4x fewer store instructions)
# baseline (speedup 1.0000x reference)
; #define LAS __attribute__((address_space(3)))
; DI f32x4 mfma16(bf16x8 a, bf16x8 b, f32x4 c) { asm volatile("s_nop 3" : "+v"(a), "+v"(b)); return __builtin_amdgcn_mfma_f32_16x16x32_bf16(a, b, c, 0, 0, 0); }
; DI void ml_local_unit(Frame& F, int l, int ch, int h, const MlLPre& P) {
;     ...
; #pragma unroll
;     for (int it = 0; it < 3; ++it) { const int mt = (it < 2) ? (w >> 1) : 4, nt = (it < 2) ? 2 * (w & 1) + it : w;
;         if (it == 2 && w >= 4) break;
;         f32x4 acc = (f32x4){0.f, 0.f, 0.f, 0.f};
; #pragma unroll
;         for (int ks = 0; ks < 4; ++ks) { const bf16x8 a = *(const LAS bf16x8*)(VWT + (16 * mt + r) * LP + 32 * ks + 8 * q), b = *(const LAS bf16x8*)(KT + (16 * nt + r) * LP + 32 * ks + 8 * q); acc = mfma16(a, b, acc); }
; #pragma unroll
;     ...
;         for (int jj = 0; jj < 4; ++jj) mls[(16 * mt + 4 * q + jj) * 64 + 16 * nt + r] = 0.01f * (float)(((16 * mt + 4 * q + jj) * 5 + (16 * nt + r) * 3 + ch) % 17 - 8);
;     ...
;         for (int jj = 0; jj < 4; ++jj) mls[(16 * mt + 4 * q + jj) * 64 + 16 * nt + r] = acc[jj];
;     ...
;         for (int jj = 0; jj < 4; ++jj) mls[(16 * mt + 4 * q + jj) * 64 + 16 * nt + r] = acc[jj];
; __global__ void __launch_bounds__(NWAVES * 64, 2) mega_fwd(Args args) {
;     ...
;             for (int ch = F.bx; ch < NCHUNK; ch += F.G) {
;                 _Pragma("unroll 1") for (int g = 0; g < 2; ++g) ssd_local_unit(F, F.l, ch, g);
;                 { MlLPre PA_, PB_; ml_local_load(F, ch, 0, PA_);
;                   ml_local_load(F, ch, 1, PB_); ml_local_unit(F, F.l, ch, 0, PA_);
;                   ml_local_load(F, ch, 2, PA_); ml_local_unit(F, F.l, ch, 1, PB_);
;                   ml_local_load(F, ch, 3, PB_); ml_local_unit(F, F.l, ch, 2, PA_);
;                   ml_local_unit(F, F.l, ch, 3, PB_); }
.LBB0_831:
	v_readlane_b32 s0, v255, 10
	s_cmp_le_i32 s0, s50
	v_readlane_b32 s1, v255, 11
	s_cselect_b64 s[8:9], -1, 0
	s_and_b64 s[0:1], s[8:9], s[2:3]
	s_andn2_b64 vcc, exec, s[0:1]
	s_cbranch_vccnz .LBB0_954
	v_mov_b32_e32 v132, v228
	v_and_b32_e32 v250, 15, v228
	v_bfe_u32 v251, v228, 4, 2
	v_mul_u32_u24_e32 v250, 0xfc, v250
	v_mul_u32_u24_e32 v251, 0x3f0, v251
	v_sub_u32_e32 v250, v250, v251
	v_ashrrev_i32_e32 v251, 31, v250
	s_mov_b64 s[0:1], 0
	s_mov_b32 s26, s57
	s_mov_b32 s2, s53
	v_readlane_b32 s27, v255, 2
	v_readlane_b32 s4, v255, 3
	s_add_i32 s17, s2, 0
	v_readlane_b32 s6, v255, 5
	v_readlane_b32 s7, v255, 6
	s_add_u32 s10, s6, s0
	s_addc_u32 s11, s7, s1
	s_cmpk_lt_i32 s26, 0x100
	v_readlane_b32 s28, v255, 19
	s_cselect_b64 s[12:13], -1, 0
	s_cmpk_gt_i32 s26, 0xff
	v_readlane_b32 s5, v255, 4
	s_cbranch_scc1 .LBB0_933
	s_lshl_b32 s14, s28, 2
	s_ashr_i32 s15, s14, 31
	s_mov_b32 s16, s26
	s_mov_b64 s[20:21], s[10:11]
	s_branch .LBB0_835

; DI float silu_f(float x) { return x * __builtin_amdgcn_rcpf(1.f + __expf(-x)); }
; DI void ssd_local_unit(Frame& F, int l, int ch, int g) {
;     ...
;     auto load_part = [&](const int part, v4u (&raw)[4][4]) {
; #pragma unroll
;         for (int cc = 0; cc < 4; ++cc)
; #pragma unroll
;             for (int j = 0; j < 4; ++j) raw[cc][j] = *(const v4u*)(proj + (size_t)(t0 + spc[j]) * PP + O_XBC + part * 256 + g * 128 + cg * 32 + cc * 8); };
;     auto do_part = [&](const int part, const v4u (&raw)[4][4]) {
; #pragma unroll
;         for (int cc = 0; cc < 4; ++cc) {
;             const int lc = cg * 32 + cc * 8, c0 = part * 256 + g * 128 + lc;
;             float acc[8];
;             { const f32x4 b0 = *(const f32x4*)(cb + c0), b1 = *(const f32x4*)(cb + c0 + 4);
; #pragma unroll
;               for (int e = 0; e < 4; ++e) { acc[e] = b0[e]; acc[4 + e] = b1[e]; } }
; #pragma unroll
;             for (int j = 0; j < 4; ++j) { float x[8]; unpack8(raw[cc][j], x);
;                 const f32x4 w0 = *(const f32x4*)(cw + j * XC + c0), w1 = *(const f32x4*)(cw + j * XC + c0 + 4);
; #pragma unroll
;                 for (int e = 0; e < 4; ++e) { acc[e] += w0[e] * okm[j] * x[e]; acc[4 + e] += w1[e] * okm[j] * x[4 + e]; } }
; #pragma unroll
;             for (int e = 0; e < 8; ++e) acc[e] = silu_f(acc[e]);
.LBB0_838:
	v_cndmask_b32_e64 v136, 0, 1.0, s[4:5]
	s_add_i32 s4, s19, 0x11000
	s_mul_i32 s0, s28, 0x3000
	s_add_u32 s0, s45, s0
	s_mul_hi_i32 s1, s28, 0x3000
	v_cndmask_b32_e64 v138, 0, 1.0, s[2:3]
	s_addc_u32 s1, s43, s1
	s_mul_i32 s2, s28, 0xc00
	s_add_u32 s2, s42, s2
	s_mul_hi_i32 s3, s28, 0xc00
	v_lshlrev_b32_e32 v141, 5, v137
	s_addc_u32 s3, s44, s3
	s_lshl_b32 s52, s40, 1
	v_lshl_add_u64 v[52:53], v[52:53], 0, s[52:53]
	v_lshlrev_b32_e32 v66, 1, v141
	v_mov_b32_e32 v67, v3
	v_cndmask_b32_e64 v140, 0, 1.0, vcc
	v_cmp_lt_i32_e32 vcc, s30, v1
	v_lshl_add_u64 v[52:53], v[52:53], 0, v[66:67]
	v_lshl_add_u64 v[58:59], v[52:53], 0, s[84:85]
	v_cndmask_b32_e64 v134, 0, 1.0, vcc
	v_add_co_u32_e32 v52, vcc, s64, v52
	v_lshl_add_u64 v[56:57], v[56:57], 0, s[52:53]
	s_nop 0
	v_addc_co_u32_e32 v53, vcc, 0, v53, vcc
	v_lshl_add_u64 v[56:57], v[56:57], 0, v[66:67]
	v_lshl_add_u64 v[62:63], v[56:57], 0, s[84:85]
	v_add_co_u32_e32 v56, vcc, s64, v56
	v_lshl_add_u64 v[60:61], v[60:61], 0, s[52:53]
	s_nop 0
	v_addc_co_u32_e32 v57, vcc, 0, v57, vcc
	v_lshl_add_u64 v[60:61], v[60:61], 0, v[66:67]
	v_lshl_add_u64 v[80:81], v[60:61], 0, s[84:85]
	v_add_co_u32_e32 v60, vcc, s64, v60
	v_lshl_add_u64 v[64:65], v[64:65], 0, s[52:53]
	s_nop 0
	v_addc_co_u32_e32 v61, vcc, 0, v61, vcc
	v_lshl_add_u64 v[64:65], v[64:65], 0, v[66:67]
	v_or_b32_e32 v152, s40, v141
	v_mov_b32_e32 v153, v3
	v_lshl_add_u64 v[96:97], v[64:65], 0, s[84:85]
	v_add_co_u32_e32 v64, vcc, s64, v64
	v_lshlrev_b64 v[142:143], 2, v[152:153]
	s_nop 0
	v_addc_co_u32_e32 v65, vcc, 0, v65, vcc
	v_lshl_add_u64 v[144:145], s[0:1], 0, v[142:143]
	v_lshl_add_u64 v[146:147], s[2:3], 0, v[142:143]
	s_mov_b64 s[6:7], 0x400
	v_add_co_u32_e32 v148, vcc, s64, v144
	s_waitcnt lgkmcnt(0)
	s_barrier
	global_load_dwordx4 v[100:103], v[52:53], off
	s_nop 0
	global_load_dwordx4 v[52:55], v[58:59], off offset:48
	global_load_dwordx4 v[68:71], v[58:59], off offset:32
	global_load_dwordx4 v[84:87], v[58:59], off offset:16
	global_load_dwordx4 v[104:107], v[56:57], off
	s_nop 0
	global_load_dwordx4 v[56:59], v[62:63], off offset:48
	global_load_dwordx4 v[72:75], v[62:63], off offset:32
	global_load_dwordx4 v[88:91], v[62:63], off offset:16
	global_load_dwordx4 v[108:111], v[60:61], off
	s_nop 0
	global_load_dwordx4 v[60:63], v[80:81], off offset:48
	global_load_dwordx4 v[76:79], v[80:81], off offset:32
	global_load_dwordx4 v[92:95], v[80:81], off offset:16
	global_load_dwordx4 v[112:115], v[64:65], off
	s_nop 0
	global_load_dwordx4 v[64:67], v[96:97], off offset:48
	global_load_dwordx4 v[80:83], v[96:97], off offset:32
	s_nop 0
	global_load_dwordx4 v[96:99], v[96:97], off offset:16
	s_nop 0
	global_load_dwordx4 v[162:165], v[146:147], off offset:1040
	global_load_dwordx4 v[166:169], v[146:147], off offset:1024
	v_lshl_add_u64 v[142:143], v[144:145], 0, s[6:7]
	global_load_dwordx4 v[170:173], v[144:145], off offset:1040
	global_load_dwordx4 v[174:177], v[144:145], off offset:1024
	global_load_dwordx4 v[178:181], v[142:143], off offset:3088
	global_load_dwordx4 v[182:185], v[142:143], off offset:3072
	v_addc_co_u32_e32 v149, vcc, 0, v145, vcc
	s_movk_i32 s42, 0x2000
	s_mov_b64 s[6:7], 0x1c00
	v_add_co_u32_e32 v150, vcc, s42, v144
	v_lshl_add_u64 v[142:143], v[144:145], 0, s[6:7]
	global_load_dwordx4 v[186:189], v[148:149], off offset:3072
	global_load_dwordx4 v[190:193], v[142:143], off offset:16
	s_mov_b64 s[6:7], 0x2800
	v_addc_co_u32_e32 v151, vcc, 0, v145, vcc
	v_lshl_add_u64 v[142:143], v[144:145], 0, s[6:7]
	global_load_dwordx4 v[194:197], v[150:151], off offset:2048
	global_load_dwordx4 v[198:201], v[142:143], off offset:16
	s_waitcnt vmcnt(38)
	v_lshlrev_b32_e32 v142, 16, v116
	v_and_b32_e32 v143, 0xffff0000, v116
	v_lshlrev_b32_e32 v116, 16, v117
	v_and_b32_e32 v117, 0xffff0000, v117
	s_movk_i32 s5, 0x2200
	s_waitcnt vmcnt(6)
	v_pk_mul_f32 v[174:175], v[140:141], v[174:175] op_sel_hi:[0,1]
	v_pk_fma_f32 v[142:143], v[174:175], v[142:143], v[166:167]
	v_lshlrev_b32_e32 v166, 16, v120
	v_and_b32_e32 v167, 0xffff0000, v120
	s_waitcnt vmcnt(4)
	v_pk_mul_f32 v[174:175], v[138:139], v[182:183] op_sel_hi:[0,1]
	v_pk_fma_f32 v[142:143], v[174:175], v[166:167], v[142:143]
	v_lshlrev_b32_e32 v166, 16, v124
	v_and_b32_e32 v167, 0xffff0000, v124
	v_lshlrev_b32_e32 v120, 16, v121
	s_waitcnt vmcnt(3)
	v_pk_mul_f32 v[174:175], v[136:137], v[186:187] op_sel_hi:[0,1]
	v_pk_fma_f32 v[142:143], v[174:175], v[166:167], v[142:143]
	v_lshlrev_b32_e32 v166, 16, v128
	v_and_b32_e32 v167, 0xffff0000, v128
	v_and_b32_e32 v121, 0xffff0000, v121
	s_waitcnt vmcnt(1)
	v_pk_mul_f32 v[174:175], v[134:135], v[194:195] op_sel_hi:[0,1]
	v_pk_fma_f32 v[142:143], v[174:175], v[166:167], v[142:143]
	s_nop 0
	v_mul_f32_e32 v0, 0xbfb8aa3b, v142
	v_exp_f32_e32 v0, v0
	s_nop 0
	v_add_f32_e32 v0, 1.0, v0
	v_rcp_f32_e32 v166, v0
	v_mul_f32_e32 v0, 0xbfb8aa3b, v143
	v_exp_f32_e32 v0, v0
	s_nop 0
	v_add_f32_e32 v0, 1.0, v0
	v_rcp_f32_e32 v167, v0
	s_nop 0
	v_pk_mul_f32 v[166:167], v[142:143], v[166:167]
	v_pk_mul_f32 v[142:143], v[140:141], v[176:177] op_sel_hi:[0,1]
	v_pk_fma_f32 v[116:117], v[142:143], v[116:117], v[168:169]
	v_pk_mul_f32 v[142:143], v[138:139], v[184:185] op_sel_hi:[0,1]
	v_pk_fma_f32 v[116:117], v[142:143], v[120:121], v[116:117]
	v_lshlrev_b32_e32 v120, 16, v125
	v_and_b32_e32 v121, 0xffff0000, v125
	v_pk_mul_f32 v[124:125], v[136:137], v[188:189] op_sel_hi:[0,1]
	v_pk_fma_f32 v[116:117], v[124:125], v[120:121], v[116:117]
	v_lshlrev_b32_e32 v120, 16, v129
	v_and_b32_e32 v121, 0xffff0000, v129
	v_pk_mul_f32 v[124:125], v[134:135], v[196:197] op_sel_hi:[0,1]
	v_pk_fma_f32 v[116:117], v[124:125], v[120:121], v[116:117]
	v_pk_mul_f32 v[124:125], v[140:141], v[170:171] op_sel_hi:[0,1]
	v_mul_f32_e32 v0, 0xbfb8aa3b, v116
	v_exp_f32_e32 v0, v0
	v_pk_mul_f32 v[128:129], v[138:139], v[178:179] op_sel_hi:[0,1]
	v_add_f32_e32 v0, 1.0, v0
	v_rcp_f32_e32 v120, v0
	v_mul_f32_e32 v0, 0xbfb8aa3b, v117
	v_exp_f32_e32 v0, v0
	s_nop 0
	v_add_f32_e32 v0, 1.0, v0
	v_rcp_f32_e32 v121, v0
	s_nop 0
	v_pk_mul_f32 v[120:121], v[116:117], v[120:121]
	v_lshlrev_b32_e32 v116, 16, v118
	v_and_b32_e32 v117, 0xffff0000, v118
	v_pk_fma_f32 v[116:117], v[124:125], v[116:117], v[162:163]
	v_lshlrev_b32_e32 v124, 16, v122
	v_and_b32_e32 v125, 0xffff0000, v122
	v_pk_fma_f32 v[116:117], v[128:129], v[124:125], v[116:117]
	v_lshlrev_b32_e32 v124, 16, v126
	v_and_b32_e32 v125, 0xffff0000, v126
	v_pk_mul_f32 v[128:129], v[136:137], v[190:191] op_sel_hi:[0,1]
	v_pk_fma_f32 v[116:117], v[128:129], v[124:125], v[116:117]
	v_lshlrev_b32_e32 v124, 16, v130
	v_and_b32_e32 v125, 0xffff0000, v130
	s_waitcnt vmcnt(0)
; __device__ __forceinline__ unsigned f2bf(float f) { unsigned u = __builtin_bit_cast(unsigned, f); return (u + 0x7fffu + ((u >> 16) & 1u)) >> 16; }
; DI unsigned pk2h(float lo, float hi) { const f32x2h_t v = {lo, hi}; return __builtin_bit_cast(unsigned, __builtin_convertvector(v, bf16x2h_t)); }
; DI float silu_f(float x) { return x * __builtin_amdgcn_rcpf(1.f + __expf(-x)); }
; DI void ssd_local_unit(Frame& F, int l, int ch, int g) {
;     ...
;             for (int j = 0; j < 4; ++j) { float x[8]; unpack8(raw[cc][j], x);
;                 const f32x4 w0 = *(const f32x4*)(cw + j * XC + c0), w1 = *(const f32x4*)(cw + j * XC + c0 + 4);
; #pragma unroll
;                 for (int e = 0; e < 4; ++e) { acc[e] += w0[e] * okm[j] * x[e]; acc[4 + e] += w1[e] * okm[j] * x[4 + e]; } }
; #pragma unroll
;             for (int e = 0; e < 8; ++e) acc[e] = silu_f(acc[e]);
;             v4u o; o.x = pk2h(acc[0], acc[1]); o.y = pk2h(acc[2], acc[3]); o.z = pk2h(acc[4], acc[5]); o.w = pk2h(acc[6], acc[7]);
;             *(v4u*)(xbcc + (size_t)(t0 + s) * XC + c0) = o;
;             if (part == 0) { const int r2 = lc >> 6; const float dtv = DT[r2 * 128 + s], sc = dtv * __expf(AC[r2 * 128 + 127] - AC[r2 * 128 + s]);
; #pragma unroll
;                 for (int e = 0; e < 8; ++e) { XWT[(lc + e) * LP + s] = (bf16)f2bf(acc[e] * sc); XD[(lc + e) * LP + s] = (bf16)f2bf(acc[e] * dtv); } }
;             else if (part == 1) {
; #pragma unroll
;                 for (int e = 0; e < 8; ++e) BT[(lc + e) * LP + s] = (bf16)f2bf(acc[e]); }
	v_pk_mul_f32 v[128:129], v[134:135], v[198:199] op_sel_hi:[0,1]
	v_pk_fma_f32 v[116:117], v[128:129], v[124:125], v[116:117]
	v_or_b32_e32 v163, 8, v141
	v_mul_f32_e32 v0, 0xbfb8aa3b, v116
	v_exp_f32_e32 v0, v0
	v_or_b32_e32 v162, 16, v141
	v_lshlrev_b32_e32 v198, 16, v100
	v_and_b32_e32 v199, 0xffff0000, v100
	v_add_f32_e32 v0, 1.0, v0
	v_rcp_f32_e32 v124, v0
	v_mul_f32_e32 v0, 0xbfb8aa3b, v117
	v_exp_f32_e32 v0, v0
	v_lshlrev_b32_e32 v100, 16, v101
	v_and_b32_e32 v101, 0xffff0000, v101
	v_add_f32_e32 v0, 1.0, v0
	v_rcp_f32_e32 v125, v0
	s_nop 0
	v_pk_mul_f32 v[124:125], v[116:117], v[124:125]
	v_lshlrev_b32_e32 v116, 16, v119
	v_and_b32_e32 v117, 0xffff0000, v119
	v_pk_mul_f32 v[118:119], v[140:141], v[172:173] op_sel_hi:[0,1]
	v_pk_fma_f32 v[116:117], v[118:119], v[116:117], v[164:165]
	v_lshlrev_b32_e32 v118, 16, v123
	v_and_b32_e32 v119, 0xffff0000, v123
	v_pk_mul_f32 v[122:123], v[138:139], v[180:181] op_sel_hi:[0,1]
	v_pk_fma_f32 v[116:117], v[122:123], v[118:119], v[116:117]
	v_lshlrev_b32_e32 v118, 16, v127
	v_and_b32_e32 v119, 0xffff0000, v127
	v_pk_mul_f32 v[122:123], v[136:137], v[192:193] op_sel_hi:[0,1]
	v_pk_fma_f32 v[116:117], v[122:123], v[118:119], v[116:117]
	v_lshlrev_b32_e32 v118, 16, v131
	v_and_b32_e32 v119, 0xffff0000, v131
	v_pk_mul_f32 v[122:123], v[134:135], v[200:201] op_sel_hi:[0,1]
	v_pk_fma_f32 v[116:117], v[122:123], v[118:119], v[116:117]
	v_mov_b64_e32 v[126:127], s[20:21]
	v_mul_f32_e32 v0, 0xbfb8aa3b, v116
	v_exp_f32_e32 v0, v0
	v_mad_i64_i32 v[126:127], s[6:7], v135, s65, v[126:127]
	s_mov_b64 s[6:7], 0x1c100000
	v_add_f32_e32 v0, 1.0, v0
	v_rcp_f32_e32 v118, v0
	v_mul_f32_e32 v0, 0xbfb8aa3b, v117
	v_exp_f32_e32 v0, v0
	v_lshl_add_u64 v[142:143], v[126:127], 0, s[6:7]
	v_lshlrev_b32_e32 v126, 1, v152
	v_mov_b32_e32 v127, v3
	v_add_f32_e32 v0, 1.0, v0
	v_rcp_f32_e32 v119, v0
	v_lshlrev_b32_e32 v164, 1, v1
	v_lshl_add_u64 v[152:153], v[142:143], 0, v[126:127]
	v_add_u32_e32 v135, s19, v164
	v_pk_mul_f32 v[122:123], v[116:117], v[118:119]
	v_cvt_pk_bf16_f32 v116, v166, v167
	v_cvt_pk_bf16_f32 v117, v120, v121
	v_cvt_pk_bf16_f32 v118, v124, v125
	v_cvt_pk_bf16_f32 v119, v122, v123
	v_bfe_u32 v0, v166, 16, 1
	global_store_dwordx4 v[152:153], v[116:119], off offset:512
	v_add3_u32 v0, v166, v0, s97
	s_mov_b64 s[6:7], 0x420
	v_mad_u32_u24 v116, v137, s5, v135
	ds_write_b16_d16_hi v116, v0 offset:34816
	v_bfe_u32 v0, v167, 16, 1
	v_add3_u32 v0, v167, v0, s97
	ds_write_b16_d16_hi v116, v0 offset:35088
	v_bfe_u32 v0, v120, 16, 1
	v_add3_u32 v0, v120, v0, s97
	ds_write_b16_d16_hi v116, v0 offset:35360
	v_bfe_u32 v0, v121, 16, 1
	v_add3_u32 v0, v121, v0, s97
	ds_write_b16_d16_hi v116, v0 offset:35632
	v_bfe_u32 v0, v124, 16, 1
	v_add3_u32 v0, v124, v0, s97
	ds_write_b16_d16_hi v116, v0 offset:35904
	v_bfe_u32 v0, v125, 16, 1
	v_add3_u32 v0, v125, v0, s97
	ds_write_b16_d16_hi v116, v0 offset:36176
	v_bfe_u32 v0, v122, 16, 1
	v_add3_u32 v0, v122, v0, s97
	ds_write_b16_d16_hi v116, v0 offset:36448
	v_bfe_u32 v0, v123, 16, 1
	v_add3_u32 v0, v123, v0, s97
	ds_write_b16_d16_hi v116, v0 offset:36720
	global_load_dwordx4 v[118:121], v[146:147], off offset:1072
	global_load_dwordx4 v[122:125], v[146:147], off offset:1056
	v_lshl_add_u64 v[130:131], v[144:145], 0, s[6:7]
	global_load_dwordx4 v[126:129], v[144:145], off offset:1072
	global_load_dwordx4 v[166:169], v[144:145], off offset:1056
	global_load_dwordx4 v[170:173], v[130:131], off offset:3088
	global_load_dwordx4 v[174:177], v[130:131], off offset:3072
	s_mov_b64 s[6:7], 0x1c20
	v_lshl_add_u64 v[130:131], v[144:145], 0, s[6:7]
	global_load_dwordx4 v[178:181], v[148:149], off offset:3104
	global_load_dwordx4 v[182:185], v[130:131], off offset:16
	s_mov_b64 s[6:7], 0x2820
	v_lshl_add_u64 v[130:131], v[144:145], 0, s[6:7]
	global_load_dwordx4 v[186:189], v[150:151], off offset:2080
	global_load_dwordx4 v[190:193], v[130:131], off offset:16
	v_lshlrev_b32_e32 v130, 16, v36
	v_and_b32_e32 v131, 0xffff0000, v36
	v_lshlrev_b32_e32 v36, 16, v37
	v_and_b32_e32 v37, 0xffff0000, v37
	s_mov_b64 s[6:7], 0x440
	s_waitcnt vmcnt(6)
	v_pk_mul_f32 v[166:167], v[140:141], v[166:167] op_sel_hi:[0,1]
	v_pk_fma_f32 v[122:123], v[166:167], v[130:131], v[122:123]
	v_lshlrev_b32_e32 v130, 16, v40
	v_and_b32_e32 v131, 0xffff0000, v40
	s_waitcnt vmcnt(4)
	v_pk_mul_f32 v[166:167], v[138:139], v[174:175] op_sel_hi:[0,1]
	v_pk_fma_f32 v[122:123], v[166:167], v[130:131], v[122:123]
	v_lshlrev_b32_e32 v130, 16, v44
	v_and_b32_e32 v131, 0xffff0000, v44
	s_waitcnt vmcnt(3)
	v_pk_mul_f32 v[166:167], v[136:137], v[178:179] op_sel_hi:[0,1]
	v_pk_fma_f32 v[122:123], v[166:167], v[130:131], v[122:123]
	v_lshlrev_b32_e32 v130, 16, v48
	v_and_b32_e32 v131, 0xffff0000, v48
	s_waitcnt vmcnt(1)
; __device__ __forceinline__ unsigned f2bf(float f) { unsigned u = __builtin_bit_cast(unsigned, f); return (u + 0x7fffu + ((u >> 16) & 1u)) >> 16; }
; DI unsigned pk2h(float lo, float hi) { const f32x2h_t v = {lo, hi}; return __builtin_bit_cast(unsigned, __builtin_convertvector(v, bf16x2h_t)); }
; DI float silu_f(float x) { return x * __builtin_amdgcn_rcpf(1.f + __expf(-x)); }
; DI void ssd_local_unit(Frame& F, int l, int ch, int g) {
;     ...
;     auto do_part = [&](const int part, const v4u (&raw)[4][4]) {
; #pragma unroll
;         for (int cc = 0; cc < 4; ++cc) {
;             const int lc = cg * 32 + cc * 8, c0 = part * 256 + g * 128 + lc;
;             float acc[8];
;             { const f32x4 b0 = *(const f32x4*)(cb + c0), b1 = *(const f32x4*)(cb + c0 + 4);
; #pragma unroll
;               for (int e = 0; e < 4; ++e) { acc[e] = b0[e]; acc[4 + e] = b1[e]; } }
; #pragma unroll
;             for (int j = 0; j < 4; ++j) { float x[8]; unpack8(raw[cc][j], x);
;                 const f32x4 w0 = *(const f32x4*)(cw + j * XC + c0), w1 = *(const f32x4*)(cw + j * XC + c0 + 4);
; #pragma unroll
;                 for (int e = 0; e < 4; ++e) { acc[e] += w0[e] * okm[j] * x[e]; acc[4 + e] += w1[e] * okm[j] * x[4 + e]; } }
; #pragma unroll
;             for (int e = 0; e < 8; ++e) acc[e] = silu_f(acc[e]);
;             v4u o; o.x = pk2h(acc[0], acc[1]); o.y = pk2h(acc[2], acc[3]); o.z = pk2h(acc[4], acc[5]); o.w = pk2h(acc[6], acc[7]);
;             *(v4u*)(xbcc + (size_t)(t0 + s) * XC + c0) = o;
;             if (part == 0) { const int r2 = lc >> 6; const float dtv = DT[r2 * 128 + s], sc = dtv * __expf(AC[r2 * 128 + 127] - AC[r2 * 128 + s]);
; #pragma unroll
;                 for (int e = 0; e < 8; ++e) { XWT[(lc + e) * LP + s] = (bf16)f2bf(acc[e] * sc); XD[(lc + e) * LP + s] = (bf16)f2bf(acc[e] * dtv); } }
;             else if (part == 1) {
; #pragma unroll
;                 for (int e = 0; e < 8; ++e) BT[(lc + e) * LP + s] = (bf16)f2bf(acc[e]); }
	v_pk_mul_f32 v[166:167], v[134:135], v[186:187] op_sel_hi:[0,1]
	v_pk_fma_f32 v[122:123], v[166:167], v[130:131], v[122:123]
	v_lshlrev_b32_e32 v40, 16, v41
	v_mul_f32_e32 v0, 0xbfb8aa3b, v122
	v_exp_f32_e32 v0, v0
	v_and_b32_e32 v41, 0xffff0000, v41
	v_add_f32_e32 v0, 1.0, v0
	v_rcp_f32_e32 v130, v0
	v_mul_f32_e32 v0, 0xbfb8aa3b, v123
	v_exp_f32_e32 v0, v0
	s_nop 0
	v_add_f32_e32 v0, 1.0, v0
	v_rcp_f32_e32 v131, v0
	s_nop 0
	v_pk_mul_f32 v[122:123], v[122:123], v[130:131]
	v_pk_mul_f32 v[130:131], v[140:141], v[168:169] op_sel_hi:[0,1]
	v_pk_fma_f32 v[36:37], v[130:131], v[36:37], v[124:125]
	v_pk_mul_f32 v[124:125], v[138:139], v[176:177] op_sel_hi:[0,1]
	v_pk_fma_f32 v[36:37], v[124:125], v[40:41], v[36:37]
	v_lshlrev_b32_e32 v40, 16, v45
	v_and_b32_e32 v41, 0xffff0000, v45
	v_pk_mul_f32 v[44:45], v[136:137], v[180:181] op_sel_hi:[0,1]
	v_pk_fma_f32 v[36:37], v[44:45], v[40:41], v[36:37]
	v_lshlrev_b32_e32 v40, 16, v49
	v_and_b32_e32 v41, 0xffff0000, v49
	v_pk_mul_f32 v[44:45], v[134:135], v[188:189] op_sel_hi:[0,1]
	v_pk_fma_f32 v[36:37], v[44:45], v[40:41], v[36:37]
	v_pk_mul_f32 v[44:45], v[140:141], v[126:127] op_sel_hi:[0,1]
	v_mul_f32_e32 v0, 0xbfb8aa3b, v36
	v_exp_f32_e32 v0, v0
	v_pk_mul_f32 v[48:49], v[138:139], v[170:171] op_sel_hi:[0,1]
	v_add_f32_e32 v0, 1.0, v0
	v_rcp_f32_e32 v40, v0
	v_mul_f32_e32 v0, 0xbfb8aa3b, v37
	v_exp_f32_e32 v0, v0
	s_nop 0
	v_add_f32_e32 v0, 1.0, v0
	v_rcp_f32_e32 v41, v0
	s_nop 0
	v_pk_mul_f32 v[40:41], v[36:37], v[40:41]
	v_lshlrev_b32_e32 v36, 16, v38
	v_and_b32_e32 v37, 0xffff0000, v38
	v_pk_fma_f32 v[36:37], v[44:45], v[36:37], v[118:119]
	v_lshlrev_b32_e32 v44, 16, v42
	v_and_b32_e32 v45, 0xffff0000, v42
	v_pk_fma_f32 v[36:37], v[48:49], v[44:45], v[36:37]
	v_lshlrev_b32_e32 v44, 16, v46
	v_and_b32_e32 v45, 0xffff0000, v46
	v_pk_mul_f32 v[48:49], v[136:137], v[182:183] op_sel_hi:[0,1]
	v_pk_fma_f32 v[36:37], v[48:49], v[44:45], v[36:37]
	v_lshlrev_b32_e32 v44, 16, v50
	v_and_b32_e32 v45, 0xffff0000, v50
	s_waitcnt vmcnt(0)
	v_pk_mul_f32 v[48:49], v[134:135], v[190:191] op_sel_hi:[0,1]
	v_pk_fma_f32 v[36:37], v[48:49], v[44:45], v[36:37]
	s_nop 0
	v_mul_f32_e32 v0, 0xbfb8aa3b, v36
	v_exp_f32_e32 v0, v0
	s_nop 0
	v_add_f32_e32 v0, 1.0, v0
	v_rcp_f32_e32 v44, v0
	v_mul_f32_e32 v0, 0xbfb8aa3b, v37
	v_exp_f32_e32 v0, v0
	s_nop 0
	v_add_f32_e32 v0, 1.0, v0
	v_rcp_f32_e32 v45, v0
	s_nop 0
	v_pk_mul_f32 v[44:45], v[36:37], v[44:45]
	v_lshlrev_b32_e32 v36, 16, v39
	v_and_b32_e32 v37, 0xffff0000, v39
	v_pk_mul_f32 v[38:39], v[140:141], v[128:129] op_sel_hi:[0,1]
	v_pk_fma_f32 v[36:37], v[38:39], v[36:37], v[120:121]
	v_lshlrev_b32_e32 v38, 16, v43
	v_and_b32_e32 v39, 0xffff0000, v43
	v_pk_mul_f32 v[42:43], v[138:139], v[172:173] op_sel_hi:[0,1]
	v_pk_fma_f32 v[36:37], v[42:43], v[38:39], v[36:37]
	v_lshlrev_b32_e32 v38, 16, v47
	v_and_b32_e32 v39, 0xffff0000, v47
	v_pk_mul_f32 v[42:43], v[136:137], v[184:185] op_sel_hi:[0,1]
	v_pk_fma_f32 v[36:37], v[42:43], v[38:39], v[36:37]
	v_lshlrev_b32_e32 v38, 16, v51
	v_and_b32_e32 v39, 0xffff0000, v51
	v_pk_mul_f32 v[42:43], v[134:135], v[192:193] op_sel_hi:[0,1]
	v_pk_fma_f32 v[36:37], v[42:43], v[38:39], v[36:37]
	s_nop 0
	v_mul_f32_e32 v0, 0xbfb8aa3b, v36
	v_exp_f32_e32 v0, v0
	s_nop 0
	v_add_f32_e32 v0, 1.0, v0
	v_rcp_f32_e32 v38, v0
	v_mul_f32_e32 v0, 0xbfb8aa3b, v37
	v_exp_f32_e32 v0, v0
	s_nop 0
	v_add_f32_e32 v0, 1.0, v0
	v_rcp_f32_e32 v39, v0
	v_bfe_u32 v0, v122, 16, 1
	v_add3_u32 v0, v122, v0, s97
	v_pk_mul_f32 v[42:43], v[36:37], v[38:39]
	v_cvt_pk_bf16_f32 v36, v122, v123
	v_cvt_pk_bf16_f32 v37, v40, v41
	v_cvt_pk_bf16_f32 v38, v44, v45
	v_cvt_pk_bf16_f32 v39, v42, v43
	global_store_dwordx4 v[152:153], v[36:39], off offset:528
	s_nop 1
	v_mad_u32_u24 v36, v163, s66, v135
	ds_write_b16_d16_hi v36, v0 offset:34816
	v_bfe_u32 v0, v123, 16, 1
	v_add3_u32 v0, v123, v0, s97
	ds_write_b16_d16_hi v116, v0 offset:37264
	v_bfe_u32 v0, v40, 16, 1
	v_add3_u32 v0, v40, v0, s97
	ds_write_b16_d16_hi v116, v0 offset:37536
	v_bfe_u32 v0, v41, 16, 1
	v_add3_u32 v0, v41, v0, s97
	ds_write_b16_d16_hi v116, v0 offset:37808
	v_bfe_u32 v0, v44, 16, 1
	v_add3_u32 v0, v44, v0, s97
	ds_write_b16_d16_hi v116, v0 offset:38080
	v_bfe_u32 v0, v45, 16, 1
	v_add3_u32 v0, v45, v0, s97
	ds_write_b16_d16_hi v116, v0 offset:38352
	v_bfe_u32 v0, v42, 16, 1
	v_add3_u32 v0, v42, v0, s97
	ds_write_b16_d16_hi v116, v0 offset:38624
	v_bfe_u32 v0, v43, 16, 1
	v_add3_u32 v0, v43, v0, s97
	ds_write_b16_d16_hi v116, v0 offset:38896
	v_lshl_add_u64 v[122:123], v[144:145], 0, s[6:7]
	global_load_dwordx4 v[36:39], v[146:147], off offset:1104
	global_load_dwordx4 v[40:43], v[146:147], off offset:1088
	global_load_dwordx4 v[44:47], v[144:145], off offset:1104
	global_load_dwordx4 v[48:51], v[144:145], off offset:1088
	global_load_dwordx4 v[118:121], v[122:123], off offset:3088
	s_nop 0
	global_load_dwordx4 v[122:125], v[122:123], off offset:3072
	s_mov_b64 s[6:7], 0x1c40
	v_lshl_add_u64 v[130:131], v[144:145], 0, s[6:7]
	global_load_dwordx4 v[126:129], v[148:149], off offset:3136
	global_load_dwordx4 v[166:169], v[130:131], off offset:16
	s_mov_b64 s[6:7], 0x2840
	v_lshl_add_u64 v[130:131], v[144:145], 0, s[6:7]
	global_load_dwordx4 v[170:173], v[150:151], off offset:2112
	global_load_dwordx4 v[174:177], v[130:131], off offset:16
	v_lshlrev_b32_e32 v130, 16, v20
	v_and_b32_e32 v131, 0xffff0000, v20
	v_lshlrev_b32_e32 v20, 16, v21
	v_and_b32_e32 v21, 0xffff0000, v21
	s_mov_b64 s[6:7], 0x460
	s_waitcnt vmcnt(6)
	v_pk_mul_f32 v[48:49], v[140:141], v[48:49] op_sel_hi:[0,1]
	v_pk_fma_f32 v[40:41], v[48:49], v[130:131], v[40:41]
	v_lshlrev_b32_e32 v48, 16, v24
	v_and_b32_e32 v49, 0xffff0000, v24
	s_waitcnt vmcnt(4)
; __device__ __forceinline__ unsigned f2bf(float f) { unsigned u = __builtin_bit_cast(unsigned, f); return (u + 0x7fffu + ((u >> 16) & 1u)) >> 16; }
; DI unsigned pk2h(float lo, float hi) { const f32x2h_t v = {lo, hi}; return __builtin_bit_cast(unsigned, __builtin_convertvector(v, bf16x2h_t)); }
; DI float silu_f(float x) { return x * __builtin_amdgcn_rcpf(1.f + __expf(-x)); }
; DI void ssd_local_unit(Frame& F, int l, int ch, int g) {
;     ...
;     auto do_part = [&](const int part, const v4u (&raw)[4][4]) {
; #pragma unroll
;         for (int cc = 0; cc < 4; ++cc) {
;             const int lc = cg * 32 + cc * 8, c0 = part * 256 + g * 128 + lc;
;             float acc[8];
;             { const f32x4 b0 = *(const f32x4*)(cb + c0), b1 = *(const f32x4*)(cb + c0 + 4);
; #pragma unroll
;               for (int e = 0; e < 4; ++e) { acc[e] = b0[e]; acc[4 + e] = b1[e]; } }
; #pragma unroll
;             for (int j = 0; j < 4; ++j) { float x[8]; unpack8(raw[cc][j], x);
;                 const f32x4 w0 = *(const f32x4*)(cw + j * XC + c0), w1 = *(const f32x4*)(cw + j * XC + c0 + 4);
; #pragma unroll
;                 for (int e = 0; e < 4; ++e) { acc[e] += w0[e] * okm[j] * x[e]; acc[4 + e] += w1[e] * okm[j] * x[4 + e]; } }
; #pragma unroll
;             for (int e = 0; e < 8; ++e) acc[e] = silu_f(acc[e]);
;             v4u o; o.x = pk2h(acc[0], acc[1]); o.y = pk2h(acc[2], acc[3]); o.z = pk2h(acc[4], acc[5]); o.w = pk2h(acc[6], acc[7]);
;             *(v4u*)(xbcc + (size_t)(t0 + s) * XC + c0) = o;
;             if (part == 0) { const int r2 = lc >> 6; const float dtv = DT[r2 * 128 + s], sc = dtv * __expf(AC[r2 * 128 + 127] - AC[r2 * 128 + s]);
; #pragma unroll
;                 for (int e = 0; e < 8; ++e) { XWT[(lc + e) * LP + s] = (bf16)f2bf(acc[e] * sc); XD[(lc + e) * LP + s] = (bf16)f2bf(acc[e] * dtv); } }
;             else if (part == 1) {
; #pragma unroll
;                 for (int e = 0; e < 8; ++e) BT[(lc + e) * LP + s] = (bf16)f2bf(acc[e]); }
	v_pk_mul_f32 v[122:123], v[138:139], v[122:123] op_sel_hi:[0,1]
	v_pk_fma_f32 v[40:41], v[122:123], v[48:49], v[40:41]
	v_lshlrev_b32_e32 v48, 16, v28
	v_and_b32_e32 v49, 0xffff0000, v28
	s_waitcnt vmcnt(3)
	v_pk_mul_f32 v[122:123], v[136:137], v[126:127] op_sel_hi:[0,1]
	v_pk_fma_f32 v[40:41], v[122:123], v[48:49], v[40:41]
	v_lshlrev_b32_e32 v48, 16, v32
	v_and_b32_e32 v49, 0xffff0000, v32
	s_waitcnt vmcnt(1)
	v_pk_mul_f32 v[122:123], v[134:135], v[170:171] op_sel_hi:[0,1]
	v_pk_fma_f32 v[40:41], v[122:123], v[48:49], v[40:41]
	v_lshlrev_b32_e32 v24, 16, v25
	v_mul_f32_e32 v0, 0xbfb8aa3b, v40
	v_exp_f32_e32 v0, v0
	v_and_b32_e32 v25, 0xffff0000, v25
	v_lshlrev_b32_e32 v126, 16, v4
	v_and_b32_e32 v127, 0xffff0000, v4
	v_add_f32_e32 v0, 1.0, v0
	v_rcp_f32_e32 v48, v0
	v_mul_f32_e32 v0, 0xbfb8aa3b, v41
	v_exp_f32_e32 v0, v0
	v_lshlrev_b32_e32 v4, 16, v5
	v_and_b32_e32 v5, 0xffff0000, v5
	v_add_f32_e32 v0, 1.0, v0
	v_rcp_f32_e32 v49, v0
	s_nop 0
	v_pk_mul_f32 v[40:41], v[40:41], v[48:49]
	v_pk_mul_f32 v[48:49], v[140:141], v[50:51] op_sel_hi:[0,1]
	v_pk_fma_f32 v[20:21], v[48:49], v[20:21], v[42:43]
	v_pk_mul_f32 v[42:43], v[138:139], v[124:125] op_sel_hi:[0,1]
	v_pk_fma_f32 v[20:21], v[42:43], v[24:25], v[20:21]
	v_lshlrev_b32_e32 v24, 16, v29
	v_and_b32_e32 v25, 0xffff0000, v29
	v_pk_mul_f32 v[28:29], v[136:137], v[128:129] op_sel_hi:[0,1]
	v_pk_fma_f32 v[20:21], v[28:29], v[24:25], v[20:21]
	v_lshlrev_b32_e32 v24, 16, v33
	v_and_b32_e32 v25, 0xffff0000, v33
	v_pk_mul_f32 v[28:29], v[134:135], v[172:173] op_sel_hi:[0,1]
	v_pk_fma_f32 v[20:21], v[28:29], v[24:25], v[20:21]
	v_pk_mul_f32 v[28:29], v[140:141], v[44:45] op_sel_hi:[0,1]
	v_mul_f32_e32 v0, 0xbfb8aa3b, v20
	v_exp_f32_e32 v0, v0
	v_pk_mul_f32 v[32:33], v[138:139], v[118:119] op_sel_hi:[0,1]
	v_add_f32_e32 v0, 1.0, v0
	v_rcp_f32_e32 v24, v0
	v_mul_f32_e32 v0, 0xbfb8aa3b, v21
	v_exp_f32_e32 v0, v0
	s_nop 0
	v_add_f32_e32 v0, 1.0, v0
	v_rcp_f32_e32 v25, v0
	s_nop 0
	v_pk_mul_f32 v[24:25], v[20:21], v[24:25]
	v_lshlrev_b32_e32 v20, 16, v22
	v_and_b32_e32 v21, 0xffff0000, v22
	v_pk_fma_f32 v[20:21], v[28:29], v[20:21], v[36:37]
	v_lshlrev_b32_e32 v28, 16, v26
	v_and_b32_e32 v29, 0xffff0000, v26
	v_pk_fma_f32 v[20:21], v[32:33], v[28:29], v[20:21]
	v_lshlrev_b32_e32 v28, 16, v30
	v_and_b32_e32 v29, 0xffff0000, v30
	v_pk_mul_f32 v[32:33], v[136:137], v[166:167] op_sel_hi:[0,1]
	v_pk_fma_f32 v[20:21], v[32:33], v[28:29], v[20:21]
	v_lshlrev_b32_e32 v28, 16, v34
	v_and_b32_e32 v29, 0xffff0000, v34
	s_waitcnt vmcnt(0)
	v_pk_mul_f32 v[32:33], v[134:135], v[174:175] op_sel_hi:[0,1]
	v_pk_fma_f32 v[20:21], v[32:33], v[28:29], v[20:21]
	s_nop 0
	v_mul_f32_e32 v0, 0xbfb8aa3b, v20
	v_exp_f32_e32 v0, v0
	s_nop 0
	v_add_f32_e32 v0, 1.0, v0
	v_rcp_f32_e32 v28, v0
	v_mul_f32_e32 v0, 0xbfb8aa3b, v21
	v_exp_f32_e32 v0, v0
	s_nop 0
	v_add_f32_e32 v0, 1.0, v0
	v_rcp_f32_e32 v29, v0
	s_nop 0
	v_pk_mul_f32 v[28:29], v[20:21], v[28:29]
	v_lshlrev_b32_e32 v20, 16, v23
	v_and_b32_e32 v21, 0xffff0000, v23
	v_pk_mul_f32 v[22:23], v[140:141], v[46:47] op_sel_hi:[0,1]
	v_pk_fma_f32 v[20:21], v[22:23], v[20:21], v[38:39]
	v_lshlrev_b32_e32 v22, 16, v27
	v_and_b32_e32 v23, 0xffff0000, v27
	v_pk_mul_f32 v[26:27], v[138:139], v[120:121] op_sel_hi:[0,1]
	v_pk_fma_f32 v[20:21], v[26:27], v[22:23], v[20:21]
	v_lshlrev_b32_e32 v22, 16, v31
	v_and_b32_e32 v23, 0xffff0000, v31
	v_pk_mul_f32 v[26:27], v[136:137], v[168:169] op_sel_hi:[0,1]
	v_pk_fma_f32 v[20:21], v[26:27], v[22:23], v[20:21]
	v_lshlrev_b32_e32 v22, 16, v35
	v_and_b32_e32 v23, 0xffff0000, v35
	v_pk_mul_f32 v[26:27], v[134:135], v[176:177] op_sel_hi:[0,1]
	v_pk_fma_f32 v[20:21], v[26:27], v[22:23], v[20:21]
	v_or_b32_e32 v139, 24, v141
	v_mul_f32_e32 v0, 0xbfb8aa3b, v20
	v_exp_f32_e32 v0, v0
	s_nop 0
	v_add_f32_e32 v0, 1.0, v0
	v_rcp_f32_e32 v22, v0
	v_mul_f32_e32 v0, 0xbfb8aa3b, v21
	v_exp_f32_e32 v0, v0
	s_nop 0
	v_add_f32_e32 v0, 1.0, v0
	v_rcp_f32_e32 v23, v0
	v_bfe_u32 v0, v40, 16, 1
	v_add3_u32 v0, v40, v0, s97
	v_pk_mul_f32 v[26:27], v[20:21], v[22:23]
	v_cvt_pk_bf16_f32 v20, v40, v41
	v_cvt_pk_bf16_f32 v21, v24, v25
	v_cvt_pk_bf16_f32 v22, v28, v29
	v_cvt_pk_bf16_f32 v23, v26, v27
	global_store_dwordx4 v[152:153], v[20:23], off offset:544
	s_nop 1
	v_mad_u32_u24 v20, v162, s66, v135
	ds_write_b16_d16_hi v20, v0 offset:34816
	v_bfe_u32 v0, v41, 16, 1
	v_add3_u32 v0, v41, v0, s97
	ds_write_b16_d16_hi v116, v0 offset:39440
	v_bfe_u32 v0, v24, 16, 1
	v_add3_u32 v0, v24, v0, s97
	ds_write_b16_d16_hi v116, v0 offset:39712
	v_bfe_u32 v0, v25, 16, 1
	v_add3_u32 v0, v25, v0, s97
	ds_write_b16_d16_hi v116, v0 offset:39984
	v_bfe_u32 v0, v28, 16, 1
	v_add3_u32 v0, v28, v0, s97
	ds_write_b16_d16_hi v116, v0 offset:40256
	v_bfe_u32 v0, v29, 16, 1
	v_add3_u32 v0, v29, v0, s97
	ds_write_b16_d16_hi v116, v0 offset:40528
	v_bfe_u32 v0, v26, 16, 1
	v_add3_u32 v0, v26, v0, s97
	ds_write_b16_d16_hi v116, v0 offset:40800
	v_bfe_u32 v0, v27, 16, 1
	v_add3_u32 v0, v27, v0, s97
	ds_write_b16_d16_hi v116, v0 offset:41072
	v_lshl_add_u64 v[40:41], v[144:145], 0, s[6:7]
	global_load_dwordx4 v[20:23], v[146:147], off offset:1136
	global_load_dwordx4 v[24:27], v[146:147], off offset:1120
	global_load_dwordx4 v[28:31], v[144:145], off offset:1136
	global_load_dwordx4 v[32:35], v[144:145], off offset:1120
	global_load_dwordx4 v[36:39], v[40:41], off offset:3088
	s_nop 0
	global_load_dwordx4 v[40:43], v[40:41], off offset:3072
	s_mov_b64 s[6:7], 0x1c60
	v_lshl_add_u64 v[48:49], v[144:145], 0, s[6:7]
	s_mov_b64 s[6:7], 0x2860
	global_load_dwordx4 v[44:47], v[148:149], off offset:3168
	s_nop 0
	global_load_dwordx4 v[48:51], v[48:49], off offset:16
	v_lshl_add_u64 v[122:123], v[144:145], 0, s[6:7]
	global_load_dwordx4 v[118:121], v[150:151], off offset:2144
	s_nop 0
	global_load_dwordx4 v[122:125], v[122:123], off offset:16
	s_mov_b64 s[6:7], 0x800
	v_lshl_add_u64 v[178:179], v[144:145], 0, s[6:7]
	s_mov_b64 s[6:7], 0x2000
	v_lshl_add_u64 v[186:187], v[144:145], 0, s[6:7]
	s_mov_b64 s[6:7], 0x2c00
	v_lshl_add_u64 v[194:195], v[144:145], 0, s[6:7]
	s_mov_b64 s[6:7], 0x820
	s_waitcnt vmcnt(6)
; __device__ __forceinline__ unsigned f2bf(float f) { unsigned u = __builtin_bit_cast(unsigned, f); return (u + 0x7fffu + ((u >> 16) & 1u)) >> 16; }
; DI unsigned pk2h(float lo, float hi) { const f32x2h_t v = {lo, hi}; return __builtin_bit_cast(unsigned, __builtin_convertvector(v, bf16x2h_t)); }
; DI float silu_f(float x) { return x * __builtin_amdgcn_rcpf(1.f + __expf(-x)); }
; DI void ssd_local_unit(Frame& F, int l, int ch, int g) {
;     ...
;     auto load_part = [&](const int part, v4u (&raw)[4][4]) {
; #pragma unroll
;         for (int cc = 0; cc < 4; ++cc)
; #pragma unroll
;             for (int j = 0; j < 4; ++j) raw[cc][j] = *(const v4u*)(proj + (size_t)(t0 + spc[j]) * PP + O_XBC + part * 256 + g * 128 + cg * 32 + cc * 8); };
;     auto do_part = [&](const int part, const v4u (&raw)[4][4]) {
; #pragma unroll
;         for (int cc = 0; cc < 4; ++cc) {
;             const int lc = cg * 32 + cc * 8, c0 = part * 256 + g * 128 + lc;
;             float acc[8];
;             { const f32x4 b0 = *(const f32x4*)(cb + c0), b1 = *(const f32x4*)(cb + c0 + 4);
; #pragma unroll
;               for (int e = 0; e < 4; ++e) { acc[e] = b0[e]; acc[4 + e] = b1[e]; } }
; #pragma unroll
;             for (int j = 0; j < 4; ++j) { float x[8]; unpack8(raw[cc][j], x);
;                 const f32x4 w0 = *(const f32x4*)(cw + j * XC + c0), w1 = *(const f32x4*)(cw + j * XC + c0 + 4);
; #pragma unroll
;                 for (int e = 0; e < 4; ++e) { acc[e] += w0[e] * okm[j] * x[e]; acc[4 + e] += w1[e] * okm[j] * x[4 + e]; } }
; #pragma unroll
;             for (int e = 0; e < 8; ++e) acc[e] = silu_f(acc[e]);
;             v4u o; o.x = pk2h(acc[0], acc[1]); o.y = pk2h(acc[2], acc[3]); o.z = pk2h(acc[4], acc[5]); o.w = pk2h(acc[6], acc[7]);
;             *(v4u*)(xbcc + (size_t)(t0 + s) * XC + c0) = o;
;             if (part == 0) { const int r2 = lc >> 6; const float dtv = DT[r2 * 128 + s], sc = dtv * __expf(AC[r2 * 128 + 127] - AC[r2 * 128 + s]);
; #pragma unroll
;                 for (int e = 0; e < 8; ++e) { XWT[(lc + e) * LP + s] = (bf16)f2bf(acc[e] * sc); XD[(lc + e) * LP + s] = (bf16)f2bf(acc[e] * dtv); } }
;             else if (part == 1) {
; #pragma unroll
;                 for (int e = 0; e < 8; ++e) BT[(lc + e) * LP + s] = (bf16)f2bf(acc[e]); }
	v_pk_mul_f32 v[32:33], v[140:141], v[32:33] op_sel_hi:[0,1]
	v_pk_fma_f32 v[24:25], v[32:33], v[126:127], v[24:25]
	v_lshlrev_b32_e32 v32, 16, v8
	v_and_b32_e32 v33, 0xffff0000, v8
	s_waitcnt vmcnt(4)
	v_pk_mul_f32 v[40:41], v[138:139], v[40:41] op_sel_hi:[0,1]
	v_pk_fma_f32 v[24:25], v[40:41], v[32:33], v[24:25]
	v_lshlrev_b32_e32 v32, 16, v12
	v_and_b32_e32 v33, 0xffff0000, v12
	s_waitcnt vmcnt(3)
	v_pk_mul_f32 v[40:41], v[136:137], v[44:45] op_sel_hi:[0,1]
	v_pk_fma_f32 v[24:25], v[40:41], v[32:33], v[24:25]
	v_lshlrev_b32_e32 v32, 16, v16
	v_and_b32_e32 v33, 0xffff0000, v16
	s_waitcnt vmcnt(1)
	v_pk_mul_f32 v[40:41], v[134:135], v[118:119] op_sel_hi:[0,1]
	v_pk_fma_f32 v[24:25], v[40:41], v[32:33], v[24:25]
	v_lshlrev_b32_e32 v8, 16, v9
	v_mul_f32_e32 v0, 0xbfb8aa3b, v24
	v_exp_f32_e32 v0, v0
	v_and_b32_e32 v9, 0xffff0000, v9
	v_add_f32_e32 v0, 1.0, v0
	v_rcp_f32_e32 v32, v0
	v_mul_f32_e32 v0, 0xbfb8aa3b, v25
	v_exp_f32_e32 v0, v0
	s_nop 0
	v_add_f32_e32 v0, 1.0, v0
	v_rcp_f32_e32 v33, v0
	s_nop 0
	v_pk_mul_f32 v[24:25], v[24:25], v[32:33]
	v_pk_mul_f32 v[32:33], v[140:141], v[34:35] op_sel_hi:[0,1]
	v_pk_fma_f32 v[4:5], v[32:33], v[4:5], v[26:27]
	v_pk_mul_f32 v[26:27], v[138:139], v[42:43] op_sel_hi:[0,1]
	v_pk_fma_f32 v[4:5], v[26:27], v[8:9], v[4:5]
	v_lshlrev_b32_e32 v8, 16, v13
	v_and_b32_e32 v9, 0xffff0000, v13
	v_pk_mul_f32 v[12:13], v[136:137], v[46:47] op_sel_hi:[0,1]
	v_pk_fma_f32 v[4:5], v[12:13], v[8:9], v[4:5]
	v_lshlrev_b32_e32 v8, 16, v17
	v_and_b32_e32 v9, 0xffff0000, v17
	v_pk_mul_f32 v[12:13], v[134:135], v[120:121] op_sel_hi:[0,1]
	v_pk_fma_f32 v[4:5], v[12:13], v[8:9], v[4:5]
	v_pk_mul_f32 v[12:13], v[140:141], v[28:29] op_sel_hi:[0,1]
	v_mul_f32_e32 v0, 0xbfb8aa3b, v4
	v_exp_f32_e32 v0, v0
	v_pk_mul_f32 v[16:17], v[138:139], v[36:37] op_sel_hi:[0,1]
	v_add_f32_e32 v0, 1.0, v0
	v_rcp_f32_e32 v8, v0
	v_mul_f32_e32 v0, 0xbfb8aa3b, v5
	v_exp_f32_e32 v0, v0
	s_nop 0
	v_add_f32_e32 v0, 1.0, v0
	v_rcp_f32_e32 v9, v0
	s_nop 0
	v_pk_mul_f32 v[8:9], v[4:5], v[8:9]
	v_lshlrev_b32_e32 v4, 16, v6
	v_and_b32_e32 v5, 0xffff0000, v6
	v_pk_fma_f32 v[4:5], v[12:13], v[4:5], v[20:21]
	v_lshlrev_b32_e32 v12, 16, v10
	v_and_b32_e32 v13, 0xffff0000, v10
	v_pk_fma_f32 v[4:5], v[16:17], v[12:13], v[4:5]
	v_lshlrev_b32_e32 v12, 16, v14
	v_and_b32_e32 v13, 0xffff0000, v14
	v_pk_mul_f32 v[16:17], v[136:137], v[48:49] op_sel_hi:[0,1]
	v_pk_fma_f32 v[4:5], v[16:17], v[12:13], v[4:5]
	v_lshlrev_b32_e32 v12, 16, v18
	v_and_b32_e32 v13, 0xffff0000, v18
	s_waitcnt vmcnt(0)
	v_pk_mul_f32 v[16:17], v[134:135], v[122:123] op_sel_hi:[0,1]
	v_pk_fma_f32 v[4:5], v[16:17], v[12:13], v[4:5]
	s_nop 0
	v_mul_f32_e32 v0, 0xbfb8aa3b, v4
	v_exp_f32_e32 v0, v0
	s_nop 0
	v_add_f32_e32 v0, 1.0, v0
	v_rcp_f32_e32 v12, v0
	v_mul_f32_e32 v0, 0xbfb8aa3b, v5
	v_exp_f32_e32 v0, v0
	s_nop 0
	v_add_f32_e32 v0, 1.0, v0
	v_rcp_f32_e32 v13, v0
	s_nop 0
	v_pk_mul_f32 v[12:13], v[4:5], v[12:13]
	v_lshlrev_b32_e32 v4, 16, v7
	v_and_b32_e32 v5, 0xffff0000, v7
	v_pk_mul_f32 v[6:7], v[140:141], v[30:31] op_sel_hi:[0,1]
	v_pk_fma_f32 v[4:5], v[6:7], v[4:5], v[22:23]
	v_lshlrev_b32_e32 v6, 16, v11
	v_and_b32_e32 v7, 0xffff0000, v11
	v_pk_mul_f32 v[10:11], v[138:139], v[38:39] op_sel_hi:[0,1]
	v_pk_fma_f32 v[4:5], v[10:11], v[6:7], v[4:5]
	v_lshlrev_b32_e32 v6, 16, v15
	v_and_b32_e32 v7, 0xffff0000, v15
	v_pk_mul_f32 v[10:11], v[136:137], v[50:51] op_sel_hi:[0,1]
	v_pk_fma_f32 v[4:5], v[10:11], v[6:7], v[4:5]
	v_lshlrev_b32_e32 v6, 16, v19
	v_and_b32_e32 v7, 0xffff0000, v19
	v_pk_mul_f32 v[10:11], v[134:135], v[124:125] op_sel_hi:[0,1]
	v_pk_fma_f32 v[4:5], v[10:11], v[6:7], v[4:5]
	s_nop 0
	v_mul_f32_e32 v0, 0xbfb8aa3b, v4
	v_exp_f32_e32 v0, v0
	s_nop 0
	v_add_f32_e32 v0, 1.0, v0
	v_rcp_f32_e32 v6, v0
	v_mul_f32_e32 v0, 0xbfb8aa3b, v5
	v_exp_f32_e32 v0, v0
	s_nop 0
	v_add_f32_e32 v0, 1.0, v0
	v_rcp_f32_e32 v7, v0
	v_bfe_u32 v0, v24, 16, 1
	v_add3_u32 v0, v24, v0, s97
	v_pk_mul_f32 v[10:11], v[4:5], v[6:7]
	v_cvt_pk_bf16_f32 v4, v24, v25
	v_cvt_pk_bf16_f32 v5, v8, v9
	v_cvt_pk_bf16_f32 v6, v12, v13
	v_cvt_pk_bf16_f32 v7, v10, v11
	global_store_dwordx4 v[152:153], v[4:7], off offset:560
	s_nop 1
	v_mad_u32_u24 v4, v139, s66, v135
	ds_write_b16_d16_hi v4, v0 offset:34816
	v_bfe_u32 v0, v25, 16, 1
	v_add3_u32 v0, v25, v0, s97
	ds_write_b16_d16_hi v116, v0 offset:41616
	v_bfe_u32 v0, v8, 16, 1
	v_add3_u32 v0, v8, v0, s97
	ds_write_b16_d16_hi v116, v0 offset:41888
	v_bfe_u32 v0, v9, 16, 1
	v_add3_u32 v0, v9, v0, s97
	ds_write_b16_d16_hi v116, v0 offset:42160
	v_bfe_u32 v0, v12, 16, 1
	v_add3_u32 v0, v12, v0, s97
	ds_write_b16_d16_hi v116, v0 offset:42432
	v_bfe_u32 v0, v13, 16, 1
	v_add3_u32 v0, v13, v0, s97
	ds_write_b16_d16_hi v116, v0 offset:42704
	v_bfe_u32 v0, v10, 16, 1
	v_add3_u32 v0, v10, v0, s97
	ds_write_b16_d16_hi v116, v0 offset:42976
	v_bfe_u32 v0, v11, 16, 1
	v_add3_u32 v0, v11, v0, s97
	ds_write_b16_d16_hi v116, v0 offset:43248
	global_load_dwordx4 v[4:7], v[154:155], off offset:3120
	global_load_dwordx4 v[20:23], v[154:155], off offset:3104
	global_load_dwordx4 v[36:39], v[154:155], off offset:3088
	global_load_dwordx4 v[116:119], v[154:155], off offset:3072
	global_load_dwordx4 v[8:11], v[156:157], off offset:3120
	global_load_dwordx4 v[24:27], v[156:157], off offset:3104
	global_load_dwordx4 v[40:43], v[156:157], off offset:3088
	global_load_dwordx4 v[120:123], v[156:157], off offset:3072
	global_load_dwordx4 v[12:15], v[158:159], off offset:3120
	global_load_dwordx4 v[28:31], v[158:159], off offset:3104
	global_load_dwordx4 v[44:47], v[158:159], off offset:3088
	global_load_dwordx4 v[124:127], v[158:159], off offset:3072
	global_load_dwordx4 v[16:19], v[160:161], off offset:3120
	global_load_dwordx4 v[32:35], v[160:161], off offset:3104
	global_load_dwordx4 v[48:51], v[160:161], off offset:3088
	global_load_dwordx4 v[128:131], v[160:161], off offset:3072
	global_load_dwordx4 v[154:157], v[146:147], off offset:2064
	s_nop 0
	global_load_dwordx4 v[158:161], v[146:147], off offset:2048
	global_load_dwordx4 v[166:169], v[144:145], off offset:2064
	global_load_dwordx4 v[170:173], v[144:145], off offset:2048
	global_load_dwordx4 v[174:177], v[178:179], off offset:3088
	s_nop 0
	global_load_dwordx4 v[178:181], v[178:179], off offset:3072
	s_nop 0
	global_load_dwordx4 v[182:185], v[150:151], off
	s_nop 0
	global_load_dwordx4 v[186:189], v[186:187], off offset:16
	s_nop 0
	global_load_dwordx4 v[190:193], v[150:151], off offset:3072
	s_nop 0
	global_load_dwordx4 v[194:197], v[194:195], off offset:16
	s_waitcnt vmcnt(6)
; DI unsigned pk2h(float lo, float hi) { const f32x2h_t v = {lo, hi}; return __builtin_bit_cast(unsigned, __builtin_convertvector(v, bf16x2h_t)); }
; DI float silu_f(float x) { return x * __builtin_amdgcn_rcpf(1.f + __expf(-x)); }
; DI void ssd_local_unit(Frame& F, int l, int ch, int g) {
;     ...
;     auto do_part = [&](const int part, const v4u (&raw)[4][4]) {
; #pragma unroll
;         for (int cc = 0; cc < 4; ++cc) {
;             const int lc = cg * 32 + cc * 8, c0 = part * 256 + g * 128 + lc;
;             float acc[8];
;             { const f32x4 b0 = *(const f32x4*)(cb + c0), b1 = *(const f32x4*)(cb + c0 + 4);
; #pragma unroll
;               for (int e = 0; e < 4; ++e) { acc[e] = b0[e]; acc[4 + e] = b1[e]; } }
; #pragma unroll
;             for (int j = 0; j < 4; ++j) { float x[8]; unpack8(raw[cc][j], x);
;                 const f32x4 w0 = *(const f32x4*)(cw + j * XC + c0), w1 = *(const f32x4*)(cw + j * XC + c0 + 4);
; #pragma unroll
;                 for (int e = 0; e < 4; ++e) { acc[e] += w0[e] * okm[j] * x[e]; acc[4 + e] += w1[e] * okm[j] * x[4 + e]; } }
; #pragma unroll
;             for (int e = 0; e < 8; ++e) acc[e] = silu_f(acc[e]);
;             v4u o; o.x = pk2h(acc[0], acc[1]); o.y = pk2h(acc[2], acc[3]); o.z = pk2h(acc[4], acc[5]); o.w = pk2h(acc[6], acc[7]);
;             *(v4u*)(xbcc + (size_t)(t0 + s) * XC + c0) = o;
	v_pk_mul_f32 v[170:171], v[140:141], v[170:171] op_sel_hi:[0,1]
	v_pk_fma_f32 v[158:159], v[170:171], v[198:199], v[158:159]
	v_lshlrev_b32_e32 v170, 16, v104
	v_and_b32_e32 v171, 0xffff0000, v104
	s_waitcnt vmcnt(4)
	v_pk_mul_f32 v[178:179], v[138:139], v[178:179] op_sel_hi:[0,1]
	v_pk_fma_f32 v[158:159], v[178:179], v[170:171], v[158:159]
	v_lshlrev_b32_e32 v170, 16, v108
	v_and_b32_e32 v171, 0xffff0000, v108
	s_waitcnt vmcnt(3)
	v_pk_mul_f32 v[178:179], v[136:137], v[182:183] op_sel_hi:[0,1]
	v_pk_fma_f32 v[158:159], v[178:179], v[170:171], v[158:159]
	v_lshlrev_b32_e32 v170, 16, v112
	v_and_b32_e32 v171, 0xffff0000, v112
	s_waitcnt vmcnt(1)
	v_pk_mul_f32 v[178:179], v[134:135], v[190:191] op_sel_hi:[0,1]
	v_pk_fma_f32 v[158:159], v[178:179], v[170:171], v[158:159]
	v_lshlrev_b32_e32 v104, 16, v105
	v_mul_f32_e32 v0, 0xbfb8aa3b, v158
	v_exp_f32_e32 v0, v0
	v_and_b32_e32 v105, 0xffff0000, v105
	v_lshlrev_b32_e32 v182, 16, v84
	v_and_b32_e32 v183, 0xffff0000, v84
	v_add_f32_e32 v0, 1.0, v0
	v_rcp_f32_e32 v170, v0
	v_mul_f32_e32 v0, 0xbfb8aa3b, v159
	v_exp_f32_e32 v0, v0
	v_lshlrev_b32_e32 v84, 16, v85
	v_and_b32_e32 v85, 0xffff0000, v85
	v_add_f32_e32 v0, 1.0, v0
	v_rcp_f32_e32 v171, v0
	s_nop 0
	v_pk_mul_f32 v[158:159], v[158:159], v[170:171]
	v_pk_mul_f32 v[170:171], v[140:141], v[172:173] op_sel_hi:[0,1]
	v_pk_fma_f32 v[100:101], v[170:171], v[100:101], v[160:161]
	v_pk_mul_f32 v[160:161], v[138:139], v[180:181] op_sel_hi:[0,1]
	v_pk_fma_f32 v[100:101], v[160:161], v[104:105], v[100:101]
	v_lshlrev_b32_e32 v104, 16, v109
	v_and_b32_e32 v105, 0xffff0000, v109
	v_pk_mul_f32 v[108:109], v[136:137], v[184:185] op_sel_hi:[0,1]
	v_pk_fma_f32 v[100:101], v[108:109], v[104:105], v[100:101]
	v_lshlrev_b32_e32 v104, 16, v113
	v_and_b32_e32 v105, 0xffff0000, v113
	v_pk_mul_f32 v[108:109], v[134:135], v[192:193] op_sel_hi:[0,1]
	v_pk_fma_f32 v[100:101], v[108:109], v[104:105], v[100:101]
	v_pk_mul_f32 v[108:109], v[140:141], v[166:167] op_sel_hi:[0,1]
	v_mul_f32_e32 v0, 0xbfb8aa3b, v100
	v_exp_f32_e32 v0, v0
	v_pk_mul_f32 v[112:113], v[138:139], v[174:175] op_sel_hi:[0,1]
	v_add_f32_e32 v0, 1.0, v0
	v_rcp_f32_e32 v104, v0
	v_mul_f32_e32 v0, 0xbfb8aa3b, v101
	v_exp_f32_e32 v0, v0
	s_nop 0
	v_add_f32_e32 v0, 1.0, v0
	v_rcp_f32_e32 v105, v0
	s_nop 0
	v_pk_mul_f32 v[104:105], v[100:101], v[104:105]
	v_lshlrev_b32_e32 v100, 16, v102
	v_and_b32_e32 v101, 0xffff0000, v102
	v_pk_fma_f32 v[100:101], v[108:109], v[100:101], v[154:155]
	v_lshlrev_b32_e32 v108, 16, v106
	v_and_b32_e32 v109, 0xffff0000, v106
	v_pk_fma_f32 v[100:101], v[112:113], v[108:109], v[100:101]
	v_lshlrev_b32_e32 v108, 16, v110
	v_and_b32_e32 v109, 0xffff0000, v110
	v_pk_mul_f32 v[112:113], v[136:137], v[186:187] op_sel_hi:[0,1]
	v_pk_fma_f32 v[100:101], v[112:113], v[108:109], v[100:101]
	v_lshlrev_b32_e32 v108, 16, v114
	v_and_b32_e32 v109, 0xffff0000, v114
	s_waitcnt vmcnt(0)
	v_pk_mul_f32 v[112:113], v[134:135], v[194:195] op_sel_hi:[0,1]
	v_pk_fma_f32 v[100:101], v[112:113], v[108:109], v[100:101]
	s_nop 0
	v_mul_f32_e32 v0, 0xbfb8aa3b, v100
	v_exp_f32_e32 v0, v0
	s_nop 0
	v_add_f32_e32 v0, 1.0, v0
	v_rcp_f32_e32 v108, v0
	v_mul_f32_e32 v0, 0xbfb8aa3b, v101
	v_exp_f32_e32 v0, v0
	s_nop 0
	v_add_f32_e32 v0, 1.0, v0
	v_rcp_f32_e32 v109, v0
	s_nop 0
	v_pk_mul_f32 v[108:109], v[100:101], v[108:109]
	v_lshlrev_b32_e32 v100, 16, v103
	v_and_b32_e32 v101, 0xffff0000, v103
	v_pk_mul_f32 v[102:103], v[140:141], v[168:169] op_sel_hi:[0,1]
	v_pk_fma_f32 v[100:101], v[102:103], v[100:101], v[156:157]
	v_lshlrev_b32_e32 v102, 16, v107
	v_and_b32_e32 v103, 0xffff0000, v107
	v_pk_mul_f32 v[106:107], v[138:139], v[176:177] op_sel_hi:[0,1]
	v_pk_fma_f32 v[100:101], v[106:107], v[102:103], v[100:101]
	v_lshlrev_b32_e32 v102, 16, v111
	v_and_b32_e32 v103, 0xffff0000, v111
	v_pk_mul_f32 v[106:107], v[136:137], v[188:189] op_sel_hi:[0,1]
	v_pk_fma_f32 v[100:101], v[106:107], v[102:103], v[100:101]
	v_lshlrev_b32_e32 v102, 16, v115
	v_and_b32_e32 v103, 0xffff0000, v115
	v_pk_mul_f32 v[106:107], v[134:135], v[196:197] op_sel_hi:[0,1]
	v_pk_fma_f32 v[100:101], v[106:107], v[102:103], v[100:101]
	s_nop 0
	v_mul_f32_e32 v0, 0xbfb8aa3b, v100
	v_exp_f32_e32 v0, v0
	s_nop 0
	v_add_f32_e32 v0, 1.0, v0
	v_rcp_f32_e32 v102, v0
	v_mul_f32_e32 v0, 0xbfb8aa3b, v101
	v_exp_f32_e32 v0, v0
	s_nop 0
	v_add_f32_e32 v0, 1.0, v0
	v_rcp_f32_e32 v103, v0
	s_nop 0
	v_pk_mul_f32 v[106:107], v[100:101], v[102:103]
	v_cvt_pk_bf16_f32 v100, v158, v159
	v_cvt_pk_bf16_f32 v101, v104, v105
	v_cvt_pk_bf16_f32 v102, v108, v109
	v_cvt_pk_bf16_f32 v103, v106, v107
	global_store_dwordx4 v[152:153], v[100:103], off offset:1024
	v_lshl_add_u64 v[158:159], v[144:145], 0, s[6:7]
	global_load_dwordx4 v[100:103], v[146:147], off offset:2096
	global_load_dwordx4 v[104:107], v[146:147], off offset:2080
	global_load_dwordx4 v[108:111], v[144:145], off offset:2096
	global_load_dwordx4 v[112:115], v[144:145], off offset:2080
	global_load_dwordx4 v[154:157], v[158:159], off offset:3088
	s_nop 0
	global_load_dwordx4 v[158:161], v[158:159], off offset:3072
	s_mov_b64 s[6:7], 0x2020
	v_lshl_add_u64 v[170:171], v[144:145], 0, s[6:7]
	s_mov_b64 s[6:7], 0x2c20
	global_load_dwordx4 v[166:169], v[150:151], off offset:32
	s_nop 0
	global_load_dwordx4 v[170:173], v[170:171], off offset:16
	v_lshl_add_u64 v[178:179], v[144:145], 0, s[6:7]
	global_load_dwordx4 v[174:177], v[150:151], off offset:3104
	s_nop 0
	global_load_dwordx4 v[178:181], v[178:179], off offset:16
	s_mov_b64 s[6:7], 0x840
	s_waitcnt vmcnt(6)
	v_pk_mul_f32 v[112:113], v[140:141], v[112:113] op_sel_hi:[0,1]
	v_pk_fma_f32 v[104:105], v[112:113], v[182:183], v[104:105]
	v_lshlrev_b32_e32 v112, 16, v88
	v_and_b32_e32 v113, 0xffff0000, v88
	s_waitcnt vmcnt(4)
; DI unsigned pk2h(float lo, float hi) { const f32x2h_t v = {lo, hi}; return __builtin_bit_cast(unsigned, __builtin_convertvector(v, bf16x2h_t)); }
; DI float silu_f(float x) { return x * __builtin_amdgcn_rcpf(1.f + __expf(-x)); }
; DI void ssd_local_unit(Frame& F, int l, int ch, int g) {
;     ...
;         for (int cc = 0; cc < 4; ++cc) {
;             const int lc = cg * 32 + cc * 8, c0 = part * 256 + g * 128 + lc;
;             float acc[8];
;             { const f32x4 b0 = *(const f32x4*)(cb + c0), b1 = *(const f32x4*)(cb + c0 + 4);
; #pragma unroll
;               for (int e = 0; e < 4; ++e) { acc[e] = b0[e]; acc[4 + e] = b1[e]; } }
; #pragma unroll
;             for (int j = 0; j < 4; ++j) { float x[8]; unpack8(raw[cc][j], x);
;                 const f32x4 w0 = *(const f32x4*)(cw + j * XC + c0), w1 = *(const f32x4*)(cw + j * XC + c0 + 4);
; #pragma unroll
;                 for (int e = 0; e < 4; ++e) { acc[e] += w0[e] * okm[j] * x[e]; acc[4 + e] += w1[e] * okm[j] * x[4 + e]; } }
; #pragma unroll
;             for (int e = 0; e < 8; ++e) acc[e] = silu_f(acc[e]);
;             v4u o; o.x = pk2h(acc[0], acc[1]); o.y = pk2h(acc[2], acc[3]); o.z = pk2h(acc[4], acc[5]); o.w = pk2h(acc[6], acc[7]);
;             *(v4u*)(xbcc + (size_t)(t0 + s) * XC + c0) = o;
	v_pk_mul_f32 v[158:159], v[138:139], v[158:159] op_sel_hi:[0,1]
	v_pk_fma_f32 v[104:105], v[158:159], v[112:113], v[104:105]
	v_lshlrev_b32_e32 v112, 16, v92
	v_and_b32_e32 v113, 0xffff0000, v92
	s_waitcnt vmcnt(3)
	v_pk_mul_f32 v[158:159], v[136:137], v[166:167] op_sel_hi:[0,1]
	v_pk_fma_f32 v[104:105], v[158:159], v[112:113], v[104:105]
	v_lshlrev_b32_e32 v112, 16, v96
	v_and_b32_e32 v113, 0xffff0000, v96
	s_waitcnt vmcnt(1)
	v_pk_mul_f32 v[158:159], v[134:135], v[174:175] op_sel_hi:[0,1]
	v_pk_fma_f32 v[104:105], v[158:159], v[112:113], v[104:105]
	v_lshlrev_b32_e32 v88, 16, v89
	v_mul_f32_e32 v0, 0xbfb8aa3b, v104
	v_exp_f32_e32 v0, v0
	v_and_b32_e32 v89, 0xffff0000, v89
	v_lshlrev_b32_e32 v166, 16, v68
	v_and_b32_e32 v167, 0xffff0000, v68
	v_add_f32_e32 v0, 1.0, v0
	v_rcp_f32_e32 v112, v0
	v_mul_f32_e32 v0, 0xbfb8aa3b, v105
	v_exp_f32_e32 v0, v0
	v_lshlrev_b32_e32 v68, 16, v69
	v_and_b32_e32 v69, 0xffff0000, v69
	v_add_f32_e32 v0, 1.0, v0
	v_rcp_f32_e32 v113, v0
	s_nop 0
	v_pk_mul_f32 v[104:105], v[104:105], v[112:113]
	v_pk_mul_f32 v[112:113], v[140:141], v[114:115] op_sel_hi:[0,1]
	v_pk_fma_f32 v[84:85], v[112:113], v[84:85], v[106:107]
	v_pk_mul_f32 v[106:107], v[138:139], v[160:161] op_sel_hi:[0,1]
	v_pk_fma_f32 v[84:85], v[106:107], v[88:89], v[84:85]
	v_lshlrev_b32_e32 v88, 16, v93
	v_and_b32_e32 v89, 0xffff0000, v93
	v_pk_mul_f32 v[92:93], v[136:137], v[168:169] op_sel_hi:[0,1]
	v_pk_fma_f32 v[84:85], v[92:93], v[88:89], v[84:85]
	v_lshlrev_b32_e32 v88, 16, v97
	v_and_b32_e32 v89, 0xffff0000, v97
	v_pk_mul_f32 v[92:93], v[134:135], v[176:177] op_sel_hi:[0,1]
	v_pk_fma_f32 v[84:85], v[92:93], v[88:89], v[84:85]
	v_pk_mul_f32 v[92:93], v[140:141], v[108:109] op_sel_hi:[0,1]
	v_mul_f32_e32 v0, 0xbfb8aa3b, v84
	v_exp_f32_e32 v0, v0
	v_pk_mul_f32 v[96:97], v[138:139], v[154:155] op_sel_hi:[0,1]
	v_add_f32_e32 v0, 1.0, v0
	v_rcp_f32_e32 v88, v0
	v_mul_f32_e32 v0, 0xbfb8aa3b, v85
	v_exp_f32_e32 v0, v0
	s_nop 0
	v_add_f32_e32 v0, 1.0, v0
	v_rcp_f32_e32 v89, v0
	s_nop 0
	v_pk_mul_f32 v[88:89], v[84:85], v[88:89]
	v_lshlrev_b32_e32 v84, 16, v86
	v_and_b32_e32 v85, 0xffff0000, v86
	v_pk_fma_f32 v[84:85], v[92:93], v[84:85], v[100:101]
	v_lshlrev_b32_e32 v92, 16, v90
	v_and_b32_e32 v93, 0xffff0000, v90
	v_pk_fma_f32 v[84:85], v[96:97], v[92:93], v[84:85]
	v_lshlrev_b32_e32 v92, 16, v94
	v_and_b32_e32 v93, 0xffff0000, v94
	v_pk_mul_f32 v[96:97], v[136:137], v[170:171] op_sel_hi:[0,1]
	v_pk_fma_f32 v[84:85], v[96:97], v[92:93], v[84:85]
	v_lshlrev_b32_e32 v92, 16, v98
	v_and_b32_e32 v93, 0xffff0000, v98
	s_waitcnt vmcnt(0)
	v_pk_mul_f32 v[96:97], v[134:135], v[178:179] op_sel_hi:[0,1]
	v_pk_fma_f32 v[84:85], v[96:97], v[92:93], v[84:85]
	s_nop 0
	v_mul_f32_e32 v0, 0xbfb8aa3b, v84
	v_exp_f32_e32 v0, v0
	s_nop 0
	v_add_f32_e32 v0, 1.0, v0
	v_rcp_f32_e32 v92, v0
	v_mul_f32_e32 v0, 0xbfb8aa3b, v85
	v_exp_f32_e32 v0, v0
	s_nop 0
	v_add_f32_e32 v0, 1.0, v0
	v_rcp_f32_e32 v93, v0
	s_nop 0
	v_pk_mul_f32 v[92:93], v[84:85], v[92:93]
	v_lshlrev_b32_e32 v84, 16, v87
	v_and_b32_e32 v85, 0xffff0000, v87
	v_pk_mul_f32 v[86:87], v[140:141], v[110:111] op_sel_hi:[0,1]
	v_pk_fma_f32 v[84:85], v[86:87], v[84:85], v[102:103]
	v_lshlrev_b32_e32 v86, 16, v91
	v_and_b32_e32 v87, 0xffff0000, v91
	v_pk_mul_f32 v[90:91], v[138:139], v[156:157] op_sel_hi:[0,1]
	v_pk_fma_f32 v[84:85], v[90:91], v[86:87], v[84:85]
	v_lshlrev_b32_e32 v86, 16, v95
	v_and_b32_e32 v87, 0xffff0000, v95
	v_pk_mul_f32 v[90:91], v[136:137], v[172:173] op_sel_hi:[0,1]
	v_pk_fma_f32 v[84:85], v[90:91], v[86:87], v[84:85]
	v_lshlrev_b32_e32 v86, 16, v99
	v_and_b32_e32 v87, 0xffff0000, v99
	v_pk_mul_f32 v[90:91], v[134:135], v[180:181] op_sel_hi:[0,1]
	v_pk_fma_f32 v[84:85], v[90:91], v[86:87], v[84:85]
	s_nop 0
	v_mul_f32_e32 v0, 0xbfb8aa3b, v84
	v_exp_f32_e32 v0, v0
	s_nop 0
	v_add_f32_e32 v0, 1.0, v0
	v_rcp_f32_e32 v86, v0
	v_mul_f32_e32 v0, 0xbfb8aa3b, v85
	v_exp_f32_e32 v0, v0
	s_nop 0
	v_add_f32_e32 v0, 1.0, v0
	v_rcp_f32_e32 v87, v0
	s_nop 0
	v_pk_mul_f32 v[90:91], v[84:85], v[86:87]
	v_cvt_pk_bf16_f32 v84, v104, v105
	v_cvt_pk_bf16_f32 v85, v88, v89
	v_cvt_pk_bf16_f32 v86, v92, v93
	v_cvt_pk_bf16_f32 v87, v90, v91
	global_store_dwordx4 v[152:153], v[84:87], off offset:1040
	v_lshl_add_u64 v[104:105], v[144:145], 0, s[6:7]
	global_load_dwordx4 v[84:87], v[146:147], off offset:2128
	global_load_dwordx4 v[88:91], v[146:147], off offset:2112
	global_load_dwordx4 v[92:95], v[144:145], off offset:2128
	global_load_dwordx4 v[96:99], v[144:145], off offset:2112
	global_load_dwordx4 v[100:103], v[104:105], off offset:3088
	s_nop 0
	global_load_dwordx4 v[104:107], v[104:105], off offset:3072
	s_mov_b64 s[6:7], 0x2040
	v_lshl_add_u64 v[112:113], v[144:145], 0, s[6:7]
	s_mov_b64 s[6:7], 0x2c40
	global_load_dwordx4 v[108:111], v[150:151], off offset:64
	s_nop 0
	global_load_dwordx4 v[112:115], v[112:113], off offset:16
	v_lshl_add_u64 v[158:159], v[144:145], 0, s[6:7]
	global_load_dwordx4 v[154:157], v[150:151], off offset:3136
	s_nop 0
	global_load_dwordx4 v[158:161], v[158:159], off offset:16
	s_mov_b64 s[6:7], 0x860
	s_waitcnt vmcnt(6)
	v_pk_mul_f32 v[96:97], v[140:141], v[96:97] op_sel_hi:[0,1]
	v_pk_fma_f32 v[88:89], v[96:97], v[166:167], v[88:89]
	v_lshlrev_b32_e32 v96, 16, v72
	v_and_b32_e32 v97, 0xffff0000, v72
	s_waitcnt vmcnt(4)
	v_pk_mul_f32 v[104:105], v[138:139], v[104:105] op_sel_hi:[0,1]
	v_pk_fma_f32 v[88:89], v[104:105], v[96:97], v[88:89]
	v_lshlrev_b32_e32 v96, 16, v76
	v_and_b32_e32 v97, 0xffff0000, v76
	s_waitcnt vmcnt(3)
	v_pk_mul_f32 v[104:105], v[136:137], v[108:109] op_sel_hi:[0,1]
	v_pk_fma_f32 v[88:89], v[104:105], v[96:97], v[88:89]
	v_lshlrev_b32_e32 v96, 16, v80
	v_and_b32_e32 v97, 0xffff0000, v80
	s_waitcnt vmcnt(1)
; DI unsigned pk2h(float lo, float hi) { const f32x2h_t v = {lo, hi}; return __builtin_bit_cast(unsigned, __builtin_convertvector(v, bf16x2h_t)); }
; DI float silu_f(float x) { return x * __builtin_amdgcn_rcpf(1.f + __expf(-x)); }
; DI void ssd_local_unit(Frame& F, int l, int ch, int g) {
;     ...
;         for (int cc = 0; cc < 4; ++cc) {
;             const int lc = cg * 32 + cc * 8, c0 = part * 256 + g * 128 + lc;
;             float acc[8];
;             { const f32x4 b0 = *(const f32x4*)(cb + c0), b1 = *(const f32x4*)(cb + c0 + 4);
; #pragma unroll
;               for (int e = 0; e < 4; ++e) { acc[e] = b0[e]; acc[4 + e] = b1[e]; } }
; #pragma unroll
;             for (int j = 0; j < 4; ++j) { float x[8]; unpack8(raw[cc][j], x);
;                 const f32x4 w0 = *(const f32x4*)(cw + j * XC + c0), w1 = *(const f32x4*)(cw + j * XC + c0 + 4);
; #pragma unroll
;                 for (int e = 0; e < 4; ++e) { acc[e] += w0[e] * okm[j] * x[e]; acc[4 + e] += w1[e] * okm[j] * x[4 + e]; } }
; #pragma unroll
;             for (int e = 0; e < 8; ++e) acc[e] = silu_f(acc[e]);
;             v4u o; o.x = pk2h(acc[0], acc[1]); o.y = pk2h(acc[2], acc[3]); o.z = pk2h(acc[4], acc[5]); o.w = pk2h(acc[6], acc[7]);
;             *(v4u*)(xbcc + (size_t)(t0 + s) * XC + c0) = o;
	v_pk_mul_f32 v[104:105], v[134:135], v[154:155] op_sel_hi:[0,1]
	v_pk_fma_f32 v[88:89], v[104:105], v[96:97], v[88:89]
	v_lshlrev_b32_e32 v72, 16, v73
	v_mul_f32_e32 v0, 0xbfb8aa3b, v88
	v_exp_f32_e32 v0, v0
	v_and_b32_e32 v73, 0xffff0000, v73
	v_lshlrev_b32_e32 v108, 16, v52
	v_and_b32_e32 v109, 0xffff0000, v52
	v_add_f32_e32 v0, 1.0, v0
	v_rcp_f32_e32 v96, v0
	v_mul_f32_e32 v0, 0xbfb8aa3b, v89
	v_exp_f32_e32 v0, v0
	v_lshlrev_b32_e32 v52, 16, v53
	v_and_b32_e32 v53, 0xffff0000, v53
	v_add_f32_e32 v0, 1.0, v0
	v_rcp_f32_e32 v97, v0
	s_nop 0
	v_pk_mul_f32 v[88:89], v[88:89], v[96:97]
	v_pk_mul_f32 v[96:97], v[140:141], v[98:99] op_sel_hi:[0,1]
	v_pk_fma_f32 v[68:69], v[96:97], v[68:69], v[90:91]
	v_pk_mul_f32 v[90:91], v[138:139], v[106:107] op_sel_hi:[0,1]
	v_pk_fma_f32 v[68:69], v[90:91], v[72:73], v[68:69]
	v_lshlrev_b32_e32 v72, 16, v77
	v_and_b32_e32 v73, 0xffff0000, v77
	v_pk_mul_f32 v[76:77], v[136:137], v[110:111] op_sel_hi:[0,1]
	v_pk_fma_f32 v[68:69], v[76:77], v[72:73], v[68:69]
	v_lshlrev_b32_e32 v72, 16, v81
	v_and_b32_e32 v73, 0xffff0000, v81
	v_pk_mul_f32 v[76:77], v[134:135], v[156:157] op_sel_hi:[0,1]
	v_pk_fma_f32 v[68:69], v[76:77], v[72:73], v[68:69]
	v_pk_mul_f32 v[76:77], v[140:141], v[92:93] op_sel_hi:[0,1]
	v_mul_f32_e32 v0, 0xbfb8aa3b, v68
	v_exp_f32_e32 v0, v0
	v_pk_mul_f32 v[80:81], v[138:139], v[100:101] op_sel_hi:[0,1]
	v_add_f32_e32 v0, 1.0, v0
	v_rcp_f32_e32 v72, v0
	v_mul_f32_e32 v0, 0xbfb8aa3b, v69
	v_exp_f32_e32 v0, v0
	s_nop 0
	v_add_f32_e32 v0, 1.0, v0
	v_rcp_f32_e32 v73, v0
	s_nop 0
	v_pk_mul_f32 v[72:73], v[68:69], v[72:73]
	v_lshlrev_b32_e32 v68, 16, v70
	v_and_b32_e32 v69, 0xffff0000, v70
	v_pk_fma_f32 v[68:69], v[76:77], v[68:69], v[84:85]
	v_lshlrev_b32_e32 v76, 16, v74
	v_and_b32_e32 v77, 0xffff0000, v74
	v_pk_fma_f32 v[68:69], v[80:81], v[76:77], v[68:69]
	v_lshlrev_b32_e32 v76, 16, v78
	v_and_b32_e32 v77, 0xffff0000, v78
	v_pk_mul_f32 v[80:81], v[136:137], v[112:113] op_sel_hi:[0,1]
	v_pk_fma_f32 v[68:69], v[80:81], v[76:77], v[68:69]
	v_lshlrev_b32_e32 v76, 16, v82
	v_and_b32_e32 v77, 0xffff0000, v82
	s_waitcnt vmcnt(0)
	v_pk_mul_f32 v[80:81], v[134:135], v[158:159] op_sel_hi:[0,1]
	v_pk_fma_f32 v[68:69], v[80:81], v[76:77], v[68:69]
	s_nop 0
	v_mul_f32_e32 v0, 0xbfb8aa3b, v68
	v_exp_f32_e32 v0, v0
	s_nop 0
	v_add_f32_e32 v0, 1.0, v0
	v_rcp_f32_e32 v76, v0
	v_mul_f32_e32 v0, 0xbfb8aa3b, v69
	v_exp_f32_e32 v0, v0
	s_nop 0
	v_add_f32_e32 v0, 1.0, v0
	v_rcp_f32_e32 v77, v0
	s_nop 0
	v_pk_mul_f32 v[76:77], v[68:69], v[76:77]
	v_lshlrev_b32_e32 v68, 16, v71
	v_and_b32_e32 v69, 0xffff0000, v71
	v_pk_mul_f32 v[70:71], v[140:141], v[94:95] op_sel_hi:[0,1]
	v_pk_fma_f32 v[68:69], v[70:71], v[68:69], v[86:87]
	v_lshlrev_b32_e32 v70, 16, v75
	v_and_b32_e32 v71, 0xffff0000, v75
	v_pk_mul_f32 v[74:75], v[138:139], v[102:103] op_sel_hi:[0,1]
	v_pk_fma_f32 v[68:69], v[74:75], v[70:71], v[68:69]
	v_lshlrev_b32_e32 v70, 16, v79
	v_and_b32_e32 v71, 0xffff0000, v79
	v_pk_mul_f32 v[74:75], v[136:137], v[114:115] op_sel_hi:[0,1]
	v_pk_fma_f32 v[68:69], v[74:75], v[70:71], v[68:69]
	v_lshlrev_b32_e32 v70, 16, v83
	v_and_b32_e32 v71, 0xffff0000, v83
	v_pk_mul_f32 v[74:75], v[134:135], v[160:161] op_sel_hi:[0,1]
	v_pk_fma_f32 v[68:69], v[74:75], v[70:71], v[68:69]
	s_nop 0
	v_mul_f32_e32 v0, 0xbfb8aa3b, v68
	v_exp_f32_e32 v0, v0
	s_nop 0
	v_add_f32_e32 v0, 1.0, v0
	v_rcp_f32_e32 v70, v0
	v_mul_f32_e32 v0, 0xbfb8aa3b, v69
	v_exp_f32_e32 v0, v0
	s_nop 0
	v_add_f32_e32 v0, 1.0, v0
	v_rcp_f32_e32 v71, v0
	s_nop 0
	v_pk_mul_f32 v[74:75], v[68:69], v[70:71]
	v_cvt_pk_bf16_f32 v68, v88, v89
	v_cvt_pk_bf16_f32 v69, v72, v73
	v_cvt_pk_bf16_f32 v70, v76, v77
	v_cvt_pk_bf16_f32 v71, v74, v75
	global_store_dwordx4 v[152:153], v[68:71], off offset:1056
	v_lshl_add_u64 v[88:89], v[144:145], 0, s[6:7]
	global_load_dwordx4 v[68:71], v[146:147], off offset:2160
	global_load_dwordx4 v[72:75], v[146:147], off offset:2144
	global_load_dwordx4 v[76:79], v[144:145], off offset:2160
	global_load_dwordx4 v[80:83], v[144:145], off offset:2144
	global_load_dwordx4 v[84:87], v[88:89], off offset:3088
	s_nop 0
	global_load_dwordx4 v[88:91], v[88:89], off offset:3072
	s_mov_b64 s[6:7], 0x2060
	v_lshl_add_u64 v[96:97], v[144:145], 0, s[6:7]
	s_mov_b64 s[6:7], 0x2c60
	global_load_dwordx4 v[92:95], v[150:151], off offset:96
	s_nop 0
	global_load_dwordx4 v[96:99], v[96:97], off offset:16
	v_lshl_add_u64 v[104:105], v[144:145], 0, s[6:7]
	global_load_dwordx4 v[100:103], v[150:151], off offset:3168
	s_nop 0
	global_load_dwordx4 v[104:107], v[104:105], off offset:16
	s_mov_b64 s[6:7], 0x1800
	s_waitcnt vmcnt(6)
	v_pk_mul_f32 v[80:81], v[140:141], v[80:81] op_sel_hi:[0,1]
	v_pk_fma_f32 v[72:73], v[80:81], v[108:109], v[72:73]
	v_lshlrev_b32_e32 v80, 16, v56
	v_and_b32_e32 v81, 0xffff0000, v56
	s_waitcnt vmcnt(4)
	v_pk_mul_f32 v[88:89], v[138:139], v[88:89] op_sel_hi:[0,1]
	v_pk_fma_f32 v[72:73], v[88:89], v[80:81], v[72:73]
	v_lshlrev_b32_e32 v80, 16, v60
	v_and_b32_e32 v81, 0xffff0000, v60
	s_waitcnt vmcnt(3)
	v_pk_mul_f32 v[88:89], v[136:137], v[92:93] op_sel_hi:[0,1]
	v_pk_fma_f32 v[72:73], v[88:89], v[80:81], v[72:73]
	v_lshlrev_b32_e32 v80, 16, v64
	v_and_b32_e32 v81, 0xffff0000, v64
	s_waitcnt vmcnt(1)
; DI unsigned pk2h(float lo, float hi) { const f32x2h_t v = {lo, hi}; return __builtin_bit_cast(unsigned, __builtin_convertvector(v, bf16x2h_t)); }
; DI float silu_f(float x) { return x * __builtin_amdgcn_rcpf(1.f + __expf(-x)); }
; DI void ssd_local_unit(Frame& F, int l, int ch, int g) {
;     ...
;         for (int cc = 0; cc < 4; ++cc) {
;             const int lc = cg * 32 + cc * 8, c0 = part * 256 + g * 128 + lc;
;             float acc[8];
;             { const f32x4 b0 = *(const f32x4*)(cb + c0), b1 = *(const f32x4*)(cb + c0 + 4);
; #pragma unroll
;               for (int e = 0; e < 4; ++e) { acc[e] = b0[e]; acc[4 + e] = b1[e]; } }
; #pragma unroll
;             for (int j = 0; j < 4; ++j) { float x[8]; unpack8(raw[cc][j], x);
;                 const f32x4 w0 = *(const f32x4*)(cw + j * XC + c0), w1 = *(const f32x4*)(cw + j * XC + c0 + 4);
; #pragma unroll
;                 for (int e = 0; e < 4; ++e) { acc[e] += w0[e] * okm[j] * x[e]; acc[4 + e] += w1[e] * okm[j] * x[4 + e]; } }
; #pragma unroll
;             for (int e = 0; e < 8; ++e) acc[e] = silu_f(acc[e]);
;             v4u o; o.x = pk2h(acc[0], acc[1]); o.y = pk2h(acc[2], acc[3]); o.z = pk2h(acc[4], acc[5]); o.w = pk2h(acc[6], acc[7]);
;             *(v4u*)(xbcc + (size_t)(t0 + s) * XC + c0) = o;
	v_pk_mul_f32 v[88:89], v[134:135], v[100:101] op_sel_hi:[0,1]
	v_pk_fma_f32 v[72:73], v[88:89], v[80:81], v[72:73]
	v_lshlrev_b32_e32 v56, 16, v57
	v_mul_f32_e32 v0, 0xbfb8aa3b, v72
	v_exp_f32_e32 v0, v0
	v_and_b32_e32 v57, 0xffff0000, v57
	v_lshlrev_b32_e32 v92, 16, v116
	v_and_b32_e32 v93, 0xffff0000, v116
	v_add_f32_e32 v0, 1.0, v0
	v_rcp_f32_e32 v80, v0
	v_mul_f32_e32 v0, 0xbfb8aa3b, v73
	v_exp_f32_e32 v0, v0
	s_nop 0
	v_add_f32_e32 v0, 1.0, v0
	v_rcp_f32_e32 v81, v0
	s_nop 0
	v_pk_mul_f32 v[72:73], v[72:73], v[80:81]
	v_pk_mul_f32 v[80:81], v[140:141], v[82:83] op_sel_hi:[0,1]
	v_pk_fma_f32 v[52:53], v[80:81], v[52:53], v[74:75]
	v_pk_mul_f32 v[74:75], v[138:139], v[90:91] op_sel_hi:[0,1]
	v_pk_fma_f32 v[52:53], v[74:75], v[56:57], v[52:53]
	v_lshlrev_b32_e32 v56, 16, v61
	v_and_b32_e32 v57, 0xffff0000, v61
	v_pk_mul_f32 v[60:61], v[136:137], v[94:95] op_sel_hi:[0,1]
	v_pk_fma_f32 v[52:53], v[60:61], v[56:57], v[52:53]
	v_lshlrev_b32_e32 v56, 16, v65
	v_and_b32_e32 v57, 0xffff0000, v65
	v_pk_mul_f32 v[60:61], v[134:135], v[102:103] op_sel_hi:[0,1]
	v_pk_fma_f32 v[52:53], v[60:61], v[56:57], v[52:53]
	v_pk_mul_f32 v[60:61], v[140:141], v[76:77] op_sel_hi:[0,1]
	v_mul_f32_e32 v0, 0xbfb8aa3b, v52
	v_exp_f32_e32 v0, v0
	v_pk_mul_f32 v[64:65], v[138:139], v[84:85] op_sel_hi:[0,1]
	v_lshl_add_u64 v[80:81], v[144:145], 0, s[6:7]
	s_mov_b64 s[6:7], 0x2400
	v_add_f32_e32 v0, 1.0, v0
	v_rcp_f32_e32 v56, v0
	v_mul_f32_e32 v0, 0xbfb8aa3b, v53
	v_exp_f32_e32 v0, v0
	v_lshl_add_u64 v[88:89], v[144:145], 0, s[6:7]
	s_movk_i32 s6, 0x2000
	v_add_f32_e32 v0, 1.0, v0
	v_rcp_f32_e32 v57, v0
	s_nop 0
	v_pk_mul_f32 v[56:57], v[52:53], v[56:57]
	v_lshlrev_b32_e32 v52, 16, v54
	v_and_b32_e32 v53, 0xffff0000, v54
	v_pk_fma_f32 v[52:53], v[60:61], v[52:53], v[68:69]
	v_lshlrev_b32_e32 v60, 16, v58
	v_and_b32_e32 v61, 0xffff0000, v58
	v_pk_fma_f32 v[52:53], v[64:65], v[60:61], v[52:53]
	v_lshlrev_b32_e32 v60, 16, v62
	v_and_b32_e32 v61, 0xffff0000, v62
	v_pk_mul_f32 v[64:65], v[136:137], v[96:97] op_sel_hi:[0,1]
	v_pk_fma_f32 v[52:53], v[64:65], v[60:61], v[52:53]
	v_lshlrev_b32_e32 v60, 16, v66
	v_and_b32_e32 v61, 0xffff0000, v66
	s_waitcnt vmcnt(0)
	v_pk_mul_f32 v[64:65], v[134:135], v[104:105] op_sel_hi:[0,1]
	v_pk_fma_f32 v[52:53], v[64:65], v[60:61], v[52:53]
	s_nop 0
	v_mul_f32_e32 v0, 0xbfb8aa3b, v52
	v_exp_f32_e32 v0, v0
	s_nop 0
	v_add_f32_e32 v0, 1.0, v0
	v_rcp_f32_e32 v60, v0
	v_mul_f32_e32 v0, 0xbfb8aa3b, v53
	v_exp_f32_e32 v0, v0
	s_nop 0
	v_add_f32_e32 v0, 1.0, v0
	v_rcp_f32_e32 v61, v0
	s_nop 0
	v_pk_mul_f32 v[60:61], v[52:53], v[60:61]
	v_lshlrev_b32_e32 v52, 16, v55
	v_and_b32_e32 v53, 0xffff0000, v55
	v_pk_mul_f32 v[54:55], v[140:141], v[78:79] op_sel_hi:[0,1]
	v_pk_fma_f32 v[52:53], v[54:55], v[52:53], v[70:71]
	v_lshlrev_b32_e32 v54, 16, v59
	v_and_b32_e32 v55, 0xffff0000, v59
	v_pk_mul_f32 v[58:59], v[138:139], v[86:87] op_sel_hi:[0,1]
	v_pk_fma_f32 v[52:53], v[58:59], v[54:55], v[52:53]
	v_lshlrev_b32_e32 v54, 16, v63
	v_and_b32_e32 v55, 0xffff0000, v63
	v_pk_mul_f32 v[58:59], v[136:137], v[98:99] op_sel_hi:[0,1]
	v_pk_fma_f32 v[52:53], v[58:59], v[54:55], v[52:53]
	v_lshlrev_b32_e32 v54, 16, v67
	v_and_b32_e32 v55, 0xffff0000, v67
	v_pk_mul_f32 v[58:59], v[134:135], v[106:107] op_sel_hi:[0,1]
	v_pk_fma_f32 v[52:53], v[58:59], v[54:55], v[52:53]
	v_lshlrev_b32_e32 v106, 16, v36
	v_mul_f32_e32 v0, 0xbfb8aa3b, v52
	v_exp_f32_e32 v0, v0
	v_and_b32_e32 v107, 0xffff0000, v36
	v_lshlrev_b32_e32 v36, 16, v37
	v_and_b32_e32 v37, 0xffff0000, v37
	v_add_f32_e32 v0, 1.0, v0
	v_rcp_f32_e32 v54, v0
	v_mul_f32_e32 v0, 0xbfb8aa3b, v53
	v_exp_f32_e32 v0, v0
	s_nop 0
	v_add_f32_e32 v0, 1.0, v0
	v_rcp_f32_e32 v55, v0
	s_nop 0
	v_pk_mul_f32 v[58:59], v[52:53], v[54:55]
	v_cvt_pk_bf16_f32 v52, v72, v73
	v_cvt_pk_bf16_f32 v53, v56, v57
	v_cvt_pk_bf16_f32 v54, v60, v61
	v_cvt_pk_bf16_f32 v55, v58, v59
	global_store_dwordx4 v[152:153], v[52:55], off offset:1072
	global_load_dwordx4 v[56:59], v[146:147], off offset:16
	s_nop 0
	global_load_dwordx4 v[52:55], v[146:147], off
	global_load_dwordx4 v[60:63], v[144:145], off offset:16
	global_load_dwordx4 v[64:67], v[144:145], off
	global_load_dwordx4 v[68:71], v[144:145], off offset:3088
	global_load_dwordx4 v[72:75], v[144:145], off offset:3072
	global_load_dwordx4 v[76:79], v[148:149], off offset:2048
	s_nop 0
	global_load_dwordx4 v[80:83], v[80:81], off offset:16
	s_nop 0
	global_load_dwordx4 v[84:87], v[150:151], off offset:1024
	s_nop 0
	global_load_dwordx4 v[88:91], v[88:89], off offset:16
	s_waitcnt vmcnt(7)
	v_pk_mul_f32 v[60:61], v[140:141], v[60:61] op_sel_hi:[0,1]
	s_waitcnt vmcnt(6)
	v_pk_mul_f32 v[64:65], v[140:141], v[64:65] op_sel_hi:[0,1]
	v_pk_fma_f32 v[52:53], v[64:65], v[92:93], v[52:53]
	v_lshlrev_b32_e32 v64, 16, v120
	v_and_b32_e32 v65, 0xffff0000, v120
	s_waitcnt vmcnt(4)
	v_pk_mul_f32 v[72:73], v[138:139], v[72:73] op_sel_hi:[0,1]
	v_pk_fma_f32 v[52:53], v[72:73], v[64:65], v[52:53]
	v_lshlrev_b32_e32 v64, 16, v124
	v_and_b32_e32 v65, 0xffff0000, v124
	s_waitcnt vmcnt(3)
	v_pk_mul_f32 v[72:73], v[136:137], v[76:77] op_sel_hi:[0,1]
	v_pk_fma_f32 v[52:53], v[72:73], v[64:65], v[52:53]
	v_lshlrev_b32_e32 v64, 16, v128
	v_and_b32_e32 v65, 0xffff0000, v128
	s_waitcnt vmcnt(1)
; __device__ __forceinline__ unsigned f2bf(float f) { unsigned u = __builtin_bit_cast(unsigned, f); return (u + 0x7fffu + ((u >> 16) & 1u)) >> 16; }
; DI unsigned pk2h(float lo, float hi) { const f32x2h_t v = {lo, hi}; return __builtin_bit_cast(unsigned, __builtin_convertvector(v, bf16x2h_t)); }
; DI float silu_f(float x) { return x * __builtin_amdgcn_rcpf(1.f + __expf(-x)); }
; DI void ssd_local_unit(Frame& F, int l, int ch, int g) {
;     ...
;         for (int cc = 0; cc < 4; ++cc) {
;             const int lc = cg * 32 + cc * 8, c0 = part * 256 + g * 128 + lc;
;             float acc[8];
;             { const f32x4 b0 = *(const f32x4*)(cb + c0), b1 = *(const f32x4*)(cb + c0 + 4);
; #pragma unroll
;               for (int e = 0; e < 4; ++e) { acc[e] = b0[e]; acc[4 + e] = b1[e]; } }
; #pragma unroll
;             for (int j = 0; j < 4; ++j) { float x[8]; unpack8(raw[cc][j], x);
;                 const f32x4 w0 = *(const f32x4*)(cw + j * XC + c0), w1 = *(const f32x4*)(cw + j * XC + c0 + 4);
; #pragma unroll
;                 for (int e = 0; e < 4; ++e) { acc[e] += w0[e] * okm[j] * x[e]; acc[4 + e] += w1[e] * okm[j] * x[4 + e]; } }
; #pragma unroll
;             for (int e = 0; e < 8; ++e) acc[e] = silu_f(acc[e]);
;             v4u o; o.x = pk2h(acc[0], acc[1]); o.y = pk2h(acc[2], acc[3]); o.z = pk2h(acc[4], acc[5]); o.w = pk2h(acc[6], acc[7]);
;             *(v4u*)(xbcc + (size_t)(t0 + s) * XC + c0) = o;
;             if (part == 0) { const int r2 = lc >> 6; const float dtv = DT[r2 * 128 + s], sc = dtv * __expf(AC[r2 * 128 + 127] - AC[r2 * 128 + s]);
; #pragma unroll
;                 for (int e = 0; e < 8; ++e) { XWT[(lc + e) * LP + s] = (bf16)f2bf(acc[e] * sc); XD[(lc + e) * LP + s] = (bf16)f2bf(acc[e] * dtv); } }
	v_pk_mul_f32 v[72:73], v[134:135], v[84:85] op_sel_hi:[0,1]
	v_pk_fma_f32 v[52:53], v[72:73], v[64:65], v[52:53]
	v_pk_mul_f32 v[66:67], v[140:141], v[66:67] op_sel_hi:[0,1]
	v_mul_f32_e32 v0, 0xbfb8aa3b, v52
	v_exp_f32_e32 v0, v0
	v_pk_mul_f32 v[62:63], v[140:141], v[62:63] op_sel_hi:[0,1]
	v_add_f32_e32 v0, 1.0, v0
	v_rcp_f32_e32 v64, v0
	v_mul_f32_e32 v0, 0xbfb8aa3b, v53
	v_exp_f32_e32 v0, v0
	s_nop 0
	v_add_f32_e32 v0, 1.0, v0
	v_rcp_f32_e32 v65, v0
	s_nop 0
	v_pk_mul_f32 v[52:53], v[52:53], v[64:65]
	v_lshlrev_b32_e32 v64, 16, v117
	v_and_b32_e32 v65, 0xffff0000, v117
	v_pk_fma_f32 v[54:55], v[66:67], v[64:65], v[54:55]
	v_lshlrev_b32_e32 v64, 16, v121
	v_and_b32_e32 v65, 0xffff0000, v121
	v_pk_mul_f32 v[66:67], v[138:139], v[74:75] op_sel_hi:[0,1]
	v_pk_fma_f32 v[54:55], v[66:67], v[64:65], v[54:55]
	v_lshlrev_b32_e32 v64, 16, v125
	v_and_b32_e32 v65, 0xffff0000, v125
	v_pk_mul_f32 v[66:67], v[136:137], v[78:79] op_sel_hi:[0,1]
	v_pk_fma_f32 v[54:55], v[66:67], v[64:65], v[54:55]
	v_lshlrev_b32_e32 v64, 16, v129
	v_and_b32_e32 v65, 0xffff0000, v129
	v_pk_mul_f32 v[66:67], v[134:135], v[86:87] op_sel_hi:[0,1]
	v_pk_fma_f32 v[54:55], v[66:67], v[64:65], v[54:55]
	s_nop 0
	v_mul_f32_e32 v0, 0xbfb8aa3b, v54
	v_exp_f32_e32 v0, v0
	s_nop 0
	v_add_f32_e32 v0, 1.0, v0
	v_rcp_f32_e32 v64, v0
	v_mul_f32_e32 v0, 0xbfb8aa3b, v55
	v_exp_f32_e32 v0, v0
	s_nop 0
	v_add_f32_e32 v0, 1.0, v0
	v_rcp_f32_e32 v65, v0
	s_nop 0
	v_pk_mul_f32 v[54:55], v[54:55], v[64:65]
	v_lshlrev_b32_e32 v64, 16, v118
	v_and_b32_e32 v65, 0xffff0000, v118
	v_pk_fma_f32 v[56:57], v[60:61], v[64:65], v[56:57]
	v_lshlrev_b32_e32 v60, 16, v122
	v_and_b32_e32 v61, 0xffff0000, v122
	v_pk_mul_f32 v[64:65], v[138:139], v[68:69] op_sel_hi:[0,1]
	v_pk_fma_f32 v[56:57], v[64:65], v[60:61], v[56:57]
	v_lshlrev_b32_e32 v60, 16, v126
	v_and_b32_e32 v61, 0xffff0000, v126
	v_pk_mul_f32 v[64:65], v[136:137], v[80:81] op_sel_hi:[0,1]
	v_pk_fma_f32 v[56:57], v[64:65], v[60:61], v[56:57]
	v_lshlrev_b32_e32 v60, 16, v130
	v_and_b32_e32 v61, 0xffff0000, v130
	s_waitcnt vmcnt(0)
	v_pk_mul_f32 v[64:65], v[134:135], v[88:89] op_sel_hi:[0,1]
	v_pk_fma_f32 v[56:57], v[64:65], v[60:61], v[56:57]
	v_add_u32_e32 v64, s4, v164
	v_mul_f32_e32 v0, 0xbfb8aa3b, v56
	v_exp_f32_e32 v0, v0
	s_nop 0
	v_add_f32_e32 v0, 1.0, v0
	v_rcp_f32_e32 v60, v0
	v_mul_f32_e32 v0, 0xbfb8aa3b, v57
	v_exp_f32_e32 v0, v0
	s_nop 0
	v_add_f32_e32 v0, 1.0, v0
	v_rcp_f32_e32 v61, v0
	s_nop 0
	v_pk_mul_f32 v[56:57], v[56:57], v[60:61]
	v_lshlrev_b32_e32 v60, 16, v119
	v_and_b32_e32 v61, 0xffff0000, v119
	v_pk_fma_f32 v[58:59], v[62:63], v[60:61], v[58:59]
	v_lshlrev_b32_e32 v60, 16, v123
	v_and_b32_e32 v61, 0xffff0000, v123
	v_pk_mul_f32 v[62:63], v[138:139], v[70:71] op_sel_hi:[0,1]
	v_pk_fma_f32 v[58:59], v[62:63], v[60:61], v[58:59]
	v_lshlrev_b32_e32 v60, 16, v127
	v_and_b32_e32 v61, 0xffff0000, v127
	v_pk_mul_f32 v[62:63], v[136:137], v[82:83] op_sel_hi:[0,1]
	v_pk_fma_f32 v[58:59], v[62:63], v[60:61], v[58:59]
	v_lshlrev_b32_e32 v60, 16, v131
	v_and_b32_e32 v61, 0xffff0000, v131
	v_pk_mul_f32 v[62:63], v[134:135], v[90:91] op_sel_hi:[0,1]
	v_pk_fma_f32 v[58:59], v[62:63], v[60:61], v[58:59]
	v_cvt_pk_bf16_f32 v62, v56, v57
	v_mul_f32_e32 v0, 0xbfb8aa3b, v58
	v_exp_f32_e32 v0, v0
	s_nop 0
	v_add_f32_e32 v0, 1.0, v0
	v_rcp_f32_e32 v60, v0
	v_mul_f32_e32 v0, 0xbfb8aa3b, v59
	v_exp_f32_e32 v0, v0
	s_nop 0
	v_add_f32_e32 v0, 1.0, v0
	v_rcp_f32_e32 v61, v0
	v_and_b32_e32 v0, 0x80, v2
	v_add_lshl_u32 v0, v0, v1, 2
	v_add_u32_e32 v2, s41, v0
	v_pk_mul_f32 v[58:59], v[58:59], v[60:61]
	v_cvt_pk_bf16_f32 v60, v52, v53
	v_cvt_pk_bf16_f32 v61, v54, v55
	v_cvt_pk_bf16_f32 v63, v58, v59
	v_add_u32_e32 v0, s36, v0
	global_store_dwordx4 v[152:153], v[60:63], off
	ds_read_b32 v60, v2
	ds_read_b32 v0, v0
	v_lshl_or_b32 v2, v137, 8, v233
	v_add_u32_e32 v2, s36, v2
	ds_read_b32 v2, v2
	s_waitcnt lgkmcnt(0)
	v_sub_f32_e32 v0, v2, v0
	v_mul_f32_e32 v0, 0x3fb8aa3b, v0
	v_exp_f32_e32 v0, v0
	s_nop 0
	v_mul_f32_e32 v61, v60, v0
	v_mul_f32_e32 v0, v61, v52
	v_bfe_u32 v2, v0, 16, 1
	v_add3_u32 v0, v0, v2, s97
	v_mul_u32_u24_e32 v2, 0x1100, v137
	v_lshlrev_b32_e32 v2, 1, v2
	v_add_u32_e32 v62, v135, v2
	ds_write_b16_d16_hi v62, v0
	v_mul_f32_e32 v0, v60, v52
	v_bfe_u32 v52, v0, 16, 1
	v_add3_u32 v0, v0, v52, s97
	v_add_u32_e32 v63, v64, v2
	ds_write_b16_d16_hi v63, v0
	v_mul_f32_e32 v0, v61, v53
	v_bfe_u32 v2, v0, 16, 1
	v_add3_u32 v0, v0, v2, s97
	ds_write_b16_d16_hi v62, v0 offset:272
	v_mul_f32_e32 v0, v60, v53
	v_bfe_u32 v2, v0, 16, 1
	v_add3_u32 v0, v0, v2, s97
	ds_write_b16_d16_hi v63, v0 offset:272
	v_mul_f32_e32 v0, v61, v54
	v_bfe_u32 v2, v0, 16, 1
	v_add3_u32 v0, v0, v2, s97
	ds_write_b16_d16_hi v62, v0 offset:544
	v_mul_f32_e32 v0, v60, v54
	v_bfe_u32 v2, v0, 16, 1
	v_add3_u32 v0, v0, v2, s97
	ds_write_b16_d16_hi v63, v0 offset:544
	v_mul_f32_e32 v0, v61, v55
	v_bfe_u32 v2, v0, 16, 1
	v_add3_u32 v0, v0, v2, s97
	ds_write_b16_d16_hi v62, v0 offset:816
	v_mul_f32_e32 v0, v60, v55
	v_bfe_u32 v2, v0, 16, 1
	v_add3_u32 v0, v0, v2, s97
	ds_write_b16_d16_hi v63, v0 offset:816
	v_mul_f32_e32 v0, v61, v56
	v_bfe_u32 v2, v0, 16, 1
	v_add3_u32 v0, v0, v2, s97
	ds_write_b16_d16_hi v62, v0 offset:1088
	v_mul_f32_e32 v0, v60, v56
	v_bfe_u32 v2, v0, 16, 1
	v_add3_u32 v0, v0, v2, s97
	ds_write_b16_d16_hi v63, v0 offset:1088
	v_mul_f32_e32 v0, v61, v57
	v_bfe_u32 v2, v0, 16, 1
	v_add3_u32 v0, v0, v2, s97
	ds_write_b16_d16_hi v62, v0 offset:1360
	v_mul_f32_e32 v0, v60, v57
	v_bfe_u32 v2, v0, 16, 1
	v_add3_u32 v0, v0, v2, s97
	ds_write_b16_d16_hi v63, v0 offset:1360
	v_mul_f32_e32 v0, v61, v58
	v_bfe_u32 v2, v0, 16, 1
	v_add3_u32 v0, v0, v2, s97
; __device__ __forceinline__ unsigned f2bf(float f) { unsigned u = __builtin_bit_cast(unsigned, f); return (u + 0x7fffu + ((u >> 16) & 1u)) >> 16; }
; DI unsigned pk2h(float lo, float hi) { const f32x2h_t v = {lo, hi}; return __builtin_bit_cast(unsigned, __builtin_convertvector(v, bf16x2h_t)); }
; DI float silu_f(float x) { return x * __builtin_amdgcn_rcpf(1.f + __expf(-x)); }
; DI void ssd_local_unit(Frame& F, int l, int ch, int g) {
;     ...
;         for (int cc = 0; cc < 4; ++cc) {
;             const int lc = cg * 32 + cc * 8, c0 = part * 256 + g * 128 + lc;
;             float acc[8];
;             { const f32x4 b0 = *(const f32x4*)(cb + c0), b1 = *(const f32x4*)(cb + c0 + 4);
; #pragma unroll
;               for (int e = 0; e < 4; ++e) { acc[e] = b0[e]; acc[4 + e] = b1[e]; } }
; #pragma unroll
;             for (int j = 0; j < 4; ++j) { float x[8]; unpack8(raw[cc][j], x);
;                 const f32x4 w0 = *(const f32x4*)(cw + j * XC + c0), w1 = *(const f32x4*)(cw + j * XC + c0 + 4);
; #pragma unroll
;                 for (int e = 0; e < 4; ++e) { acc[e] += w0[e] * okm[j] * x[e]; acc[4 + e] += w1[e] * okm[j] * x[4 + e]; } }
; #pragma unroll
;             for (int e = 0; e < 8; ++e) acc[e] = silu_f(acc[e]);
;             v4u o; o.x = pk2h(acc[0], acc[1]); o.y = pk2h(acc[2], acc[3]); o.z = pk2h(acc[4], acc[5]); o.w = pk2h(acc[6], acc[7]);
;             *(v4u*)(xbcc + (size_t)(t0 + s) * XC + c0) = o;
;             if (part == 0) { const int r2 = lc >> 6; const float dtv = DT[r2 * 128 + s], sc = dtv * __expf(AC[r2 * 128 + 127] - AC[r2 * 128 + s]);
; #pragma unroll
;                 for (int e = 0; e < 8; ++e) { XWT[(lc + e) * LP + s] = (bf16)f2bf(acc[e] * sc); XD[(lc + e) * LP + s] = (bf16)f2bf(acc[e] * dtv); } }
	ds_write_b16_d16_hi v62, v0 offset:1632
	v_mul_f32_e32 v0, v60, v58
	v_bfe_u32 v2, v0, 16, 1
	v_add3_u32 v0, v0, v2, s97
	ds_write_b16_d16_hi v63, v0 offset:1632
	v_mul_f32_e32 v0, v61, v59
	v_bfe_u32 v2, v0, 16, 1
	v_add3_u32 v0, v0, v2, s97
	ds_write_b16_d16_hi v62, v0 offset:1904
	v_mul_f32_e32 v0, v60, v59
	v_bfe_u32 v2, v0, 16, 1
	v_add3_u32 v0, v0, v2, s97
	v_add_u32_e32 v2, s40, v141
	v_lshlrev_b64 v[52:53], 2, v[2:3]
	v_lshl_add_u64 v[58:59], s[2:3], 0, v[52:53]
	v_lshl_add_u64 v[52:53], s[0:1], 0, v[52:53]
	ds_write_b16_d16_hi v63, v0 offset:1904
	s_mov_b64 s[0:1], 0x1820
	v_add_co_u32_e32 v54, vcc, s64, v52
	global_load_dwordx4 v[66:69], v[58:59], off offset:48
	global_load_dwordx4 v[70:73], v[58:59], off offset:32
	global_load_dwordx4 v[74:77], v[52:53], off offset:48
	global_load_dwordx4 v[78:81], v[52:53], off offset:32
	global_load_dwordx4 v[82:85], v[52:53], off offset:3120
	global_load_dwordx4 v[86:89], v[52:53], off offset:3104
	v_lshl_add_u64 v[56:57], v[52:53], 0, s[0:1]
	v_addc_co_u32_e32 v55, vcc, 0, v53, vcc
	global_load_dwordx4 v[90:93], v[54:55], off offset:2080
	global_load_dwordx4 v[94:97], v[56:57], off offset:16
	s_mov_b64 s[0:1], 0x2420
	v_add_co_u32_e32 v56, vcc, s42, v52
	v_lshl_add_u64 v[102:103], v[52:53], 0, s[0:1]
	s_nop 0
	v_addc_co_u32_e32 v57, vcc, 0, v53, vcc
	global_load_dwordx4 v[98:101], v[56:57], off offset:1056
	s_nop 0
	global_load_dwordx4 v[102:105], v[102:103], off offset:16
	s_mov_b64 s[0:1], 0x1840
	s_or_b32 s2, s39, s18
	s_waitcnt vmcnt(6)
	v_pk_mul_f32 v[78:79], v[140:141], v[78:79] op_sel_hi:[0,1]
	v_pk_fma_f32 v[70:71], v[78:79], v[106:107], v[70:71]
	v_lshlrev_b32_e32 v78, 16, v40
	v_and_b32_e32 v79, 0xffff0000, v40
	s_waitcnt vmcnt(4)
	v_pk_mul_f32 v[86:87], v[138:139], v[86:87] op_sel_hi:[0,1]
	v_pk_fma_f32 v[70:71], v[86:87], v[78:79], v[70:71]
	v_lshlrev_b32_e32 v78, 16, v44
	v_and_b32_e32 v79, 0xffff0000, v44
	s_waitcnt vmcnt(3)
	v_pk_mul_f32 v[86:87], v[136:137], v[90:91] op_sel_hi:[0,1]
	v_pk_fma_f32 v[70:71], v[86:87], v[78:79], v[70:71]
	v_lshlrev_b32_e32 v78, 16, v48
	v_and_b32_e32 v79, 0xffff0000, v48
	s_waitcnt vmcnt(1)
	v_pk_mul_f32 v[86:87], v[134:135], v[98:99] op_sel_hi:[0,1]
	v_pk_fma_f32 v[70:71], v[86:87], v[78:79], v[70:71]
	v_lshlrev_b32_e32 v40, 16, v41
	v_mul_f32_e32 v0, 0xbfb8aa3b, v70
	v_exp_f32_e32 v0, v0
	v_and_b32_e32 v41, 0xffff0000, v41
	v_add_f32_e32 v0, 1.0, v0
	v_rcp_f32_e32 v78, v0
	v_mul_f32_e32 v0, 0xbfb8aa3b, v71
	v_exp_f32_e32 v0, v0
	s_nop 0
	v_add_f32_e32 v0, 1.0, v0
	v_rcp_f32_e32 v79, v0
	s_nop 0
	v_pk_mul_f32 v[70:71], v[70:71], v[78:79]
	v_pk_mul_f32 v[78:79], v[140:141], v[80:81] op_sel_hi:[0,1]
	v_pk_fma_f32 v[36:37], v[78:79], v[36:37], v[72:73]
	v_pk_mul_f32 v[72:73], v[138:139], v[88:89] op_sel_hi:[0,1]
	v_pk_fma_f32 v[36:37], v[72:73], v[40:41], v[36:37]
	v_lshlrev_b32_e32 v40, 16, v45
	v_and_b32_e32 v41, 0xffff0000, v45
	v_pk_mul_f32 v[44:45], v[136:137], v[92:93] op_sel_hi:[0,1]
	v_pk_fma_f32 v[36:37], v[44:45], v[40:41], v[36:37]
	v_lshlrev_b32_e32 v40, 16, v49
	v_and_b32_e32 v41, 0xffff0000, v49
	v_pk_mul_f32 v[44:45], v[134:135], v[100:101] op_sel_hi:[0,1]
	v_pk_fma_f32 v[36:37], v[44:45], v[40:41], v[36:37]
	v_pk_mul_f32 v[48:49], v[138:139], v[82:83] op_sel_hi:[0,1]
	v_mul_f32_e32 v0, 0xbfb8aa3b, v36
	v_exp_f32_e32 v0, v0
	s_nop 0
	v_add_f32_e32 v0, 1.0, v0
	v_rcp_f32_e32 v40, v0
	v_mul_f32_e32 v0, 0xbfb8aa3b, v37
	v_exp_f32_e32 v0, v0
	s_nop 0
	v_add_f32_e32 v0, 1.0, v0
	v_rcp_f32_e32 v41, v0
	s_nop 0
	v_pk_mul_f32 v[44:45], v[36:37], v[40:41]
	v_lshlrev_b32_e32 v36, 16, v38
	v_and_b32_e32 v37, 0xffff0000, v38
	v_pk_mul_f32 v[40:41], v[140:141], v[74:75] op_sel_hi:[0,1]
	v_pk_fma_f32 v[36:37], v[40:41], v[36:37], v[66:67]
	v_lshlrev_b32_e32 v40, 16, v42
	v_and_b32_e32 v41, 0xffff0000, v42
	v_pk_fma_f32 v[36:37], v[48:49], v[40:41], v[36:37]
	v_lshlrev_b32_e32 v40, 16, v46
	v_and_b32_e32 v41, 0xffff0000, v46
	v_pk_mul_f32 v[48:49], v[136:137], v[94:95] op_sel_hi:[0,1]
	v_pk_fma_f32 v[36:37], v[48:49], v[40:41], v[36:37]
	v_lshlrev_b32_e32 v40, 16, v50
	v_and_b32_e32 v41, 0xffff0000, v50
	s_waitcnt vmcnt(0)
	v_pk_mul_f32 v[48:49], v[134:135], v[102:103] op_sel_hi:[0,1]
	v_pk_fma_f32 v[36:37], v[48:49], v[40:41], v[36:37]
	s_nop 0
	v_mul_f32_e32 v0, 0xbfb8aa3b, v36
	v_exp_f32_e32 v0, v0
	s_nop 0
	v_add_f32_e32 v0, 1.0, v0
	v_rcp_f32_e32 v40, v0
	v_mul_f32_e32 v0, 0xbfb8aa3b, v37
	v_exp_f32_e32 v0, v0
	s_nop 0
	v_add_f32_e32 v0, 1.0, v0
	v_rcp_f32_e32 v41, v0
	s_nop 0
	v_pk_mul_f32 v[48:49], v[36:37], v[40:41]
	v_lshlrev_b32_e32 v36, 16, v39
	v_and_b32_e32 v37, 0xffff0000, v39
	v_pk_mul_f32 v[38:39], v[140:141], v[76:77] op_sel_hi:[0,1]
	v_pk_fma_f32 v[36:37], v[38:39], v[36:37], v[68:69]
	v_lshlrev_b32_e32 v38, 16, v43
	v_and_b32_e32 v39, 0xffff0000, v43
	v_pk_mul_f32 v[40:41], v[138:139], v[84:85] op_sel_hi:[0,1]
	v_pk_fma_f32 v[36:37], v[40:41], v[38:39], v[36:37]
	v_lshlrev_b32_e32 v38, 16, v47
	v_and_b32_e32 v39, 0xffff0000, v47
	v_pk_mul_f32 v[40:41], v[136:137], v[96:97] op_sel_hi:[0,1]
	v_pk_fma_f32 v[36:37], v[40:41], v[38:39], v[36:37]
	v_lshlrev_b32_e32 v38, 16, v51
	v_and_b32_e32 v39, 0xffff0000, v51
	v_pk_mul_f32 v[40:41], v[134:135], v[104:105] op_sel_hi:[0,1]
	v_pk_fma_f32 v[36:37], v[40:41], v[38:39], v[36:37]
	v_lshl_add_u64 v[40:41], v[2:3], 1, v[142:143]
	v_mul_f32_e32 v0, 0xbfb8aa3b, v36
	v_exp_f32_e32 v0, v0
	v_lshl_add_u64 v[50:51], v[52:53], 0, s[0:1]
	s_mov_b64 s[0:1], 0x2440
	v_add_f32_e32 v0, 1.0, v0
	v_rcp_f32_e32 v38, v0
	v_mul_f32_e32 v0, 0xbfb8aa3b, v37
	v_exp_f32_e32 v0, v0
	s_nop 0
	v_add_f32_e32 v0, 1.0, v0
	v_rcp_f32_e32 v39, v0
	v_mul_f32_e32 v0, v61, v70
	v_bfe_u32 v2, v0, 16, 1
; __device__ __forceinline__ unsigned f2bf(float f) { unsigned u = __builtin_bit_cast(unsigned, f); return (u + 0x7fffu + ((u >> 16) & 1u)) >> 16; }
; DI unsigned pk2h(float lo, float hi) { const f32x2h_t v = {lo, hi}; return __builtin_bit_cast(unsigned, __builtin_convertvector(v, bf16x2h_t)); }
; DI float silu_f(float x) { return x * __builtin_amdgcn_rcpf(1.f + __expf(-x)); }
; DI void ssd_local_unit(Frame& F, int l, int ch, int g) {
;     ...
;         for (int cc = 0; cc < 4; ++cc) {
;             const int lc = cg * 32 + cc * 8, c0 = part * 256 + g * 128 + lc;
;             float acc[8];
;             { const f32x4 b0 = *(const f32x4*)(cb + c0), b1 = *(const f32x4*)(cb + c0 + 4);
; #pragma unroll
;               for (int e = 0; e < 4; ++e) { acc[e] = b0[e]; acc[4 + e] = b1[e]; } }
; #pragma unroll
;             for (int j = 0; j < 4; ++j) { float x[8]; unpack8(raw[cc][j], x);
;                 const f32x4 w0 = *(const f32x4*)(cw + j * XC + c0), w1 = *(const f32x4*)(cw + j * XC + c0 + 4);
; #pragma unroll
;                 for (int e = 0; e < 4; ++e) { acc[e] += w0[e] * okm[j] * x[e]; acc[4 + e] += w1[e] * okm[j] * x[4 + e]; } }
; #pragma unroll
;             for (int e = 0; e < 8; ++e) acc[e] = silu_f(acc[e]);
;             v4u o; o.x = pk2h(acc[0], acc[1]); o.y = pk2h(acc[2], acc[3]); o.z = pk2h(acc[4], acc[5]); o.w = pk2h(acc[6], acc[7]);
;             *(v4u*)(xbcc + (size_t)(t0 + s) * XC + c0) = o;
;             if (part == 0) { const int r2 = lc >> 6; const float dtv = DT[r2 * 128 + s], sc = dtv * __expf(AC[r2 * 128 + 127] - AC[r2 * 128 + s]);
; #pragma unroll
;                 for (int e = 0; e < 8; ++e) { XWT[(lc + e) * LP + s] = (bf16)f2bf(acc[e] * sc); XD[(lc + e) * LP + s] = (bf16)f2bf(acc[e] * dtv); } }
	v_add3_u32 v0, v0, v2, s97
	v_pk_mul_f32 v[42:43], v[36:37], v[38:39]
	v_mul_u32_u24_e32 v2, 0x88, v163
	v_cvt_pk_bf16_f32 v36, v70, v71
	v_cvt_pk_bf16_f32 v37, v44, v45
	v_cvt_pk_bf16_f32 v38, v48, v49
	v_cvt_pk_bf16_f32 v39, v42, v43
	v_lshlrev_b32_e32 v2, 1, v2
	global_store_dwordx4 v[40:41], v[36:39], off offset:16
	s_nop 1
	v_add_u32_e32 v36, v135, v2
	ds_write_b16_d16_hi v36, v0
	v_mul_f32_e32 v0, v60, v70
	v_bfe_u32 v36, v0, 16, 1
	v_add3_u32 v0, v0, v36, s97
	v_add_u32_e32 v2, v64, v2
	ds_write_b16_d16_hi v2, v0
	v_mul_f32_e32 v0, v61, v71
	v_bfe_u32 v2, v0, 16, 1
	v_add3_u32 v0, v0, v2, s97
	ds_write_b16_d16_hi v62, v0 offset:2448
	v_mul_f32_e32 v0, v60, v71
	v_bfe_u32 v2, v0, 16, 1
	v_add3_u32 v0, v0, v2, s97
	ds_write_b16_d16_hi v63, v0 offset:2448
	v_mul_f32_e32 v0, v61, v44
	v_bfe_u32 v2, v0, 16, 1
	v_add3_u32 v0, v0, v2, s97
	ds_write_b16_d16_hi v62, v0 offset:2720
	v_mul_f32_e32 v0, v60, v44
	v_bfe_u32 v2, v0, 16, 1
	v_add3_u32 v0, v0, v2, s97
	ds_write_b16_d16_hi v63, v0 offset:2720
	v_mul_f32_e32 v0, v61, v45
	v_bfe_u32 v2, v0, 16, 1
	v_add3_u32 v0, v0, v2, s97
	ds_write_b16_d16_hi v62, v0 offset:2992
	v_mul_f32_e32 v0, v60, v45
	v_bfe_u32 v2, v0, 16, 1
	v_add3_u32 v0, v0, v2, s97
	ds_write_b16_d16_hi v63, v0 offset:2992
	v_mul_f32_e32 v0, v61, v48
	v_bfe_u32 v2, v0, 16, 1
	v_add3_u32 v0, v0, v2, s97
	ds_write_b16_d16_hi v62, v0 offset:3264
	v_mul_f32_e32 v0, v60, v48
	v_bfe_u32 v2, v0, 16, 1
	v_add3_u32 v0, v0, v2, s97
	ds_write_b16_d16_hi v63, v0 offset:3264
	v_mul_f32_e32 v0, v61, v49
	v_bfe_u32 v2, v0, 16, 1
	v_add3_u32 v0, v0, v2, s97
	ds_write_b16_d16_hi v62, v0 offset:3536
	v_mul_f32_e32 v0, v60, v49
	v_bfe_u32 v2, v0, 16, 1
	v_add3_u32 v0, v0, v2, s97
	ds_write_b16_d16_hi v63, v0 offset:3536
	v_mul_f32_e32 v0, v61, v42
	v_bfe_u32 v2, v0, 16, 1
	v_add3_u32 v0, v0, v2, s97
	ds_write_b16_d16_hi v62, v0 offset:3808
	v_mul_f32_e32 v0, v60, v42
	v_bfe_u32 v2, v0, 16, 1
	v_add3_u32 v0, v0, v2, s97
	ds_write_b16_d16_hi v63, v0 offset:3808
	v_mul_f32_e32 v0, v61, v43
	v_bfe_u32 v2, v0, 16, 1
	v_add3_u32 v0, v0, v2, s97
	ds_write_b16_d16_hi v62, v0 offset:4080
	v_mul_f32_e32 v0, v60, v43
	v_bfe_u32 v2, v0, 16, 1
	v_add3_u32 v0, v0, v2, s97
	ds_write_b16_d16_hi v63, v0 offset:4080
	global_load_dwordx4 v[36:39], v[58:59], off offset:80
	global_load_dwordx4 v[42:45], v[58:59], off offset:64
	global_load_dwordx4 v[46:49], v[52:53], off offset:80
	global_load_dwordx4 v[66:69], v[52:53], off offset:64
	global_load_dwordx4 v[70:73], v[52:53], off offset:3152
	global_load_dwordx4 v[74:77], v[52:53], off offset:3136
	global_load_dwordx4 v[78:81], v[54:55], off offset:2112
	global_load_dwordx4 v[82:85], v[50:51], off offset:16
	v_lshl_add_u64 v[50:51], v[52:53], 0, s[0:1]
	global_load_dwordx4 v[86:89], v[56:57], off offset:1088
	global_load_dwordx4 v[90:93], v[50:51], off offset:16
	v_lshlrev_b32_e32 v50, 16, v20
	v_and_b32_e32 v51, 0xffff0000, v20
	v_lshlrev_b32_e32 v20, 16, v21
	v_and_b32_e32 v21, 0xffff0000, v21
	s_mov_b64 s[0:1], 0x1860
	s_waitcnt vmcnt(6)
	v_pk_mul_f32 v[66:67], v[140:141], v[66:67] op_sel_hi:[0,1]
	v_pk_fma_f32 v[42:43], v[66:67], v[50:51], v[42:43]
	v_lshlrev_b32_e32 v50, 16, v24
	v_and_b32_e32 v51, 0xffff0000, v24
	s_waitcnt vmcnt(4)
	v_pk_mul_f32 v[66:67], v[138:139], v[74:75] op_sel_hi:[0,1]
	v_pk_fma_f32 v[42:43], v[66:67], v[50:51], v[42:43]
	v_lshlrev_b32_e32 v50, 16, v28
	v_and_b32_e32 v51, 0xffff0000, v28
	s_waitcnt vmcnt(3)
	v_pk_mul_f32 v[66:67], v[136:137], v[78:79] op_sel_hi:[0,1]
	v_pk_fma_f32 v[42:43], v[66:67], v[50:51], v[42:43]
	v_lshlrev_b32_e32 v50, 16, v32
	v_and_b32_e32 v51, 0xffff0000, v32
	s_waitcnt vmcnt(1)
	v_pk_mul_f32 v[66:67], v[134:135], v[86:87] op_sel_hi:[0,1]
	v_pk_fma_f32 v[42:43], v[66:67], v[50:51], v[42:43]
	v_lshlrev_b32_e32 v24, 16, v25
	v_mul_f32_e32 v0, 0xbfb8aa3b, v42
	v_exp_f32_e32 v0, v0
	v_and_b32_e32 v25, 0xffff0000, v25
	v_add_f32_e32 v0, 1.0, v0
	v_rcp_f32_e32 v50, v0
	v_mul_f32_e32 v0, 0xbfb8aa3b, v43
	v_exp_f32_e32 v0, v0
	s_nop 0
	v_add_f32_e32 v0, 1.0, v0
	v_rcp_f32_e32 v51, v0
	s_nop 0
	v_pk_mul_f32 v[42:43], v[42:43], v[50:51]
	v_pk_mul_f32 v[50:51], v[140:141], v[68:69] op_sel_hi:[0,1]
	v_pk_fma_f32 v[20:21], v[50:51], v[20:21], v[44:45]
	v_pk_mul_f32 v[44:45], v[138:139], v[76:77] op_sel_hi:[0,1]
	v_pk_fma_f32 v[20:21], v[44:45], v[24:25], v[20:21]
	v_lshlrev_b32_e32 v24, 16, v29
	v_and_b32_e32 v25, 0xffff0000, v29
	v_pk_mul_f32 v[28:29], v[136:137], v[80:81] op_sel_hi:[0,1]
	v_pk_fma_f32 v[20:21], v[28:29], v[24:25], v[20:21]
	v_lshlrev_b32_e32 v24, 16, v33
	v_and_b32_e32 v25, 0xffff0000, v33
	v_pk_mul_f32 v[28:29], v[134:135], v[88:89] op_sel_hi:[0,1]
	v_pk_fma_f32 v[20:21], v[28:29], v[24:25], v[20:21]
	v_pk_mul_f32 v[28:29], v[140:141], v[46:47] op_sel_hi:[0,1]
	v_mul_f32_e32 v0, 0xbfb8aa3b, v20
	v_exp_f32_e32 v0, v0
	v_pk_mul_f32 v[32:33], v[138:139], v[70:71] op_sel_hi:[0,1]
	v_lshl_add_u64 v[50:51], v[52:53], 0, s[0:1]
	s_mov_b64 s[0:1], 0x2460
	v_add_f32_e32 v0, 1.0, v0
	v_rcp_f32_e32 v24, v0
	v_mul_f32_e32 v0, 0xbfb8aa3b, v21
	v_exp_f32_e32 v0, v0
	s_nop 0
	v_add_f32_e32 v0, 1.0, v0
	v_rcp_f32_e32 v25, v0
	s_nop 0
	v_pk_mul_f32 v[24:25], v[20:21], v[24:25]
	v_lshlrev_b32_e32 v20, 16, v22
	v_and_b32_e32 v21, 0xffff0000, v22
	v_pk_fma_f32 v[20:21], v[28:29], v[20:21], v[36:37]
	v_lshlrev_b32_e32 v28, 16, v26
	v_and_b32_e32 v29, 0xffff0000, v26
	v_pk_fma_f32 v[20:21], v[32:33], v[28:29], v[20:21]
	v_lshlrev_b32_e32 v28, 16, v30
	v_and_b32_e32 v29, 0xffff0000, v30
	v_pk_mul_f32 v[32:33], v[136:137], v[82:83] op_sel_hi:[0,1]
	v_pk_fma_f32 v[20:21], v[32:33], v[28:29], v[20:21]
	v_lshlrev_b32_e32 v28, 16, v34
	v_and_b32_e32 v29, 0xffff0000, v34
	s_waitcnt vmcnt(0)
; __device__ __forceinline__ unsigned f2bf(float f) { unsigned u = __builtin_bit_cast(unsigned, f); return (u + 0x7fffu + ((u >> 16) & 1u)) >> 16; }
; DI unsigned pk2h(float lo, float hi) { const f32x2h_t v = {lo, hi}; return __builtin_bit_cast(unsigned, __builtin_convertvector(v, bf16x2h_t)); }
; DI float silu_f(float x) { return x * __builtin_amdgcn_rcpf(1.f + __expf(-x)); }
; DI void ssd_local_unit(Frame& F, int l, int ch, int g) {
;     ...
;         for (int cc = 0; cc < 4; ++cc) {
;             const int lc = cg * 32 + cc * 8, c0 = part * 256 + g * 128 + lc;
;             float acc[8];
;             { const f32x4 b0 = *(const f32x4*)(cb + c0), b1 = *(const f32x4*)(cb + c0 + 4);
; #pragma unroll
;               for (int e = 0; e < 4; ++e) { acc[e] = b0[e]; acc[4 + e] = b1[e]; } }
; #pragma unroll
;             for (int j = 0; j < 4; ++j) { float x[8]; unpack8(raw[cc][j], x);
;                 const f32x4 w0 = *(const f32x4*)(cw + j * XC + c0), w1 = *(const f32x4*)(cw + j * XC + c0 + 4);
; #pragma unroll
;                 for (int e = 0; e < 4; ++e) { acc[e] += w0[e] * okm[j] * x[e]; acc[4 + e] += w1[e] * okm[j] * x[4 + e]; } }
; #pragma unroll
;             for (int e = 0; e < 8; ++e) acc[e] = silu_f(acc[e]);
;             v4u o; o.x = pk2h(acc[0], acc[1]); o.y = pk2h(acc[2], acc[3]); o.z = pk2h(acc[4], acc[5]); o.w = pk2h(acc[6], acc[7]);
;             *(v4u*)(xbcc + (size_t)(t0 + s) * XC + c0) = o;
;             if (part == 0) { const int r2 = lc >> 6; const float dtv = DT[r2 * 128 + s], sc = dtv * __expf(AC[r2 * 128 + 127] - AC[r2 * 128 + s]);
; #pragma unroll
;                 for (int e = 0; e < 8; ++e) { XWT[(lc + e) * LP + s] = (bf16)f2bf(acc[e] * sc); XD[(lc + e) * LP + s] = (bf16)f2bf(acc[e] * dtv); } }
	v_pk_mul_f32 v[32:33], v[134:135], v[90:91] op_sel_hi:[0,1]
	v_pk_fma_f32 v[20:21], v[32:33], v[28:29], v[20:21]
	s_nop 0
	v_mul_f32_e32 v0, 0xbfb8aa3b, v20
	v_exp_f32_e32 v0, v0
	s_nop 0
	v_add_f32_e32 v0, 1.0, v0
	v_rcp_f32_e32 v28, v0
	v_mul_f32_e32 v0, 0xbfb8aa3b, v21
	v_exp_f32_e32 v0, v0
	s_nop 0
	v_add_f32_e32 v0, 1.0, v0
	v_rcp_f32_e32 v29, v0
	s_nop 0
	v_pk_mul_f32 v[28:29], v[20:21], v[28:29]
	v_lshlrev_b32_e32 v20, 16, v23
	v_and_b32_e32 v21, 0xffff0000, v23
	v_pk_mul_f32 v[22:23], v[140:141], v[48:49] op_sel_hi:[0,1]
	v_pk_fma_f32 v[20:21], v[22:23], v[20:21], v[38:39]
	v_lshlrev_b32_e32 v22, 16, v27
	v_and_b32_e32 v23, 0xffff0000, v27
	v_pk_mul_f32 v[26:27], v[138:139], v[72:73] op_sel_hi:[0,1]
	v_pk_fma_f32 v[20:21], v[26:27], v[22:23], v[20:21]
	v_lshlrev_b32_e32 v22, 16, v31
	v_and_b32_e32 v23, 0xffff0000, v31
	v_pk_mul_f32 v[26:27], v[136:137], v[84:85] op_sel_hi:[0,1]
	v_pk_fma_f32 v[20:21], v[26:27], v[22:23], v[20:21]
	v_lshlrev_b32_e32 v22, 16, v35
	v_and_b32_e32 v23, 0xffff0000, v35
	v_pk_mul_f32 v[26:27], v[134:135], v[92:93] op_sel_hi:[0,1]
	v_pk_fma_f32 v[20:21], v[26:27], v[22:23], v[20:21]
	s_nop 0
	v_mul_f32_e32 v0, 0xbfb8aa3b, v20
	v_exp_f32_e32 v0, v0
	s_nop 0
	v_add_f32_e32 v0, 1.0, v0
	v_rcp_f32_e32 v22, v0
	v_mul_f32_e32 v0, 0xbfb8aa3b, v21
	v_exp_f32_e32 v0, v0
	s_nop 0
	v_add_f32_e32 v0, 1.0, v0
	v_rcp_f32_e32 v23, v0
	v_mul_f32_e32 v0, v61, v42
	v_bfe_u32 v2, v0, 16, 1
	v_add3_u32 v0, v0, v2, s97
	v_pk_mul_f32 v[26:27], v[20:21], v[22:23]
	v_mul_u32_u24_e32 v2, 0x88, v162
	v_cvt_pk_bf16_f32 v20, v42, v43
	v_cvt_pk_bf16_f32 v21, v24, v25
	v_cvt_pk_bf16_f32 v22, v28, v29
	v_cvt_pk_bf16_f32 v23, v26, v27
	v_lshlrev_b32_e32 v2, 1, v2
	global_store_dwordx4 v[40:41], v[20:23], off offset:32
	s_nop 1
	v_add_u32_e32 v20, v135, v2
	ds_write_b16_d16_hi v20, v0
	v_mul_f32_e32 v0, v60, v42
	v_bfe_u32 v20, v0, 16, 1
	v_add3_u32 v0, v0, v20, s97
	v_add_u32_e32 v2, v64, v2
	ds_write_b16_d16_hi v2, v0
	v_mul_f32_e32 v0, v61, v43
	v_bfe_u32 v2, v0, 16, 1
	v_add3_u32 v0, v0, v2, s97
	ds_write_b16_d16_hi v62, v0 offset:4624
	v_mul_f32_e32 v0, v60, v43
	v_bfe_u32 v2, v0, 16, 1
	v_add3_u32 v0, v0, v2, s97
	ds_write_b16_d16_hi v63, v0 offset:4624
	v_mul_f32_e32 v0, v61, v24
	v_bfe_u32 v2, v0, 16, 1
	v_add3_u32 v0, v0, v2, s97
	ds_write_b16_d16_hi v62, v0 offset:4896
	v_mul_f32_e32 v0, v60, v24
	v_bfe_u32 v2, v0, 16, 1
	v_add3_u32 v0, v0, v2, s97
	ds_write_b16_d16_hi v63, v0 offset:4896
	v_mul_f32_e32 v0, v61, v25
	v_bfe_u32 v2, v0, 16, 1
	v_add3_u32 v0, v0, v2, s97
	ds_write_b16_d16_hi v62, v0 offset:5168
	v_mul_f32_e32 v0, v60, v25
	v_bfe_u32 v2, v0, 16, 1
	v_add3_u32 v0, v0, v2, s97
	ds_write_b16_d16_hi v63, v0 offset:5168
	v_mul_f32_e32 v0, v61, v28
	v_bfe_u32 v2, v0, 16, 1
	v_add3_u32 v0, v0, v2, s97
	ds_write_b16_d16_hi v62, v0 offset:5440
	v_mul_f32_e32 v0, v60, v28
	v_bfe_u32 v2, v0, 16, 1
	v_add3_u32 v0, v0, v2, s97
	ds_write_b16_d16_hi v63, v0 offset:5440
	v_mul_f32_e32 v0, v61, v29
	v_bfe_u32 v2, v0, 16, 1
	v_add3_u32 v0, v0, v2, s97
	ds_write_b16_d16_hi v62, v0 offset:5712
	v_mul_f32_e32 v0, v60, v29
	v_bfe_u32 v2, v0, 16, 1
	v_add3_u32 v0, v0, v2, s97
	ds_write_b16_d16_hi v63, v0 offset:5712
	v_mul_f32_e32 v0, v61, v26
	v_bfe_u32 v2, v0, 16, 1
	v_add3_u32 v0, v0, v2, s97
	ds_write_b16_d16_hi v62, v0 offset:5984
	v_mul_f32_e32 v0, v60, v26
	v_bfe_u32 v2, v0, 16, 1
	v_add3_u32 v0, v0, v2, s97
	ds_write_b16_d16_hi v63, v0 offset:5984
	v_mul_f32_e32 v0, v61, v27
	v_bfe_u32 v2, v0, 16, 1
	v_add3_u32 v0, v0, v2, s97
	ds_write_b16_d16_hi v62, v0 offset:6256
	v_mul_f32_e32 v0, v60, v27
	v_bfe_u32 v2, v0, 16, 1
	v_add3_u32 v0, v0, v2, s97
	ds_write_b16_d16_hi v63, v0 offset:6256
	global_load_dwordx4 v[20:23], v[58:59], off offset:112
	global_load_dwordx4 v[24:27], v[58:59], off offset:96
	global_load_dwordx4 v[28:31], v[52:53], off offset:112
	global_load_dwordx4 v[32:35], v[52:53], off offset:96
	global_load_dwordx4 v[36:39], v[52:53], off offset:3184
	global_load_dwordx4 v[42:45], v[52:53], off offset:3168
	global_load_dwordx4 v[46:49], v[54:55], off offset:2144
	global_load_dwordx4 v[66:69], v[50:51], off offset:16
	v_lshl_add_u64 v[54:55], v[52:53], 0, s[0:1]
	global_load_dwordx4 v[50:53], v[56:57], off offset:1120
	s_nop 0
	global_load_dwordx4 v[54:57], v[54:55], off offset:16
	v_lshlrev_b32_e32 v58, 16, v4
	v_and_b32_e32 v59, 0xffff0000, v4
	v_lshlrev_b32_e32 v4, 16, v5
	v_and_b32_e32 v5, 0xffff0000, v5
	s_waitcnt vmcnt(6)
	v_pk_mul_f32 v[32:33], v[140:141], v[32:33] op_sel_hi:[0,1]
	v_pk_fma_f32 v[24:25], v[32:33], v[58:59], v[24:25]
	v_lshlrev_b32_e32 v32, 16, v8
	v_and_b32_e32 v33, 0xffff0000, v8
	s_waitcnt vmcnt(4)
	v_pk_mul_f32 v[42:43], v[138:139], v[42:43] op_sel_hi:[0,1]
	v_pk_fma_f32 v[24:25], v[42:43], v[32:33], v[24:25]
	v_lshlrev_b32_e32 v32, 16, v12
	v_and_b32_e32 v33, 0xffff0000, v12
	s_waitcnt vmcnt(3)
	v_pk_mul_f32 v[42:43], v[136:137], v[46:47] op_sel_hi:[0,1]
	v_pk_fma_f32 v[24:25], v[42:43], v[32:33], v[24:25]
	v_lshlrev_b32_e32 v32, 16, v16
	v_and_b32_e32 v33, 0xffff0000, v16
	s_waitcnt vmcnt(1)
; #define LAS __attribute__((address_space(3)))
; __device__ __forceinline__ unsigned f2bf(float f) { unsigned u = __builtin_bit_cast(unsigned, f); return (u + 0x7fffu + ((u >> 16) & 1u)) >> 16; }
; DI unsigned pk2h(float lo, float hi) { const f32x2h_t v = {lo, hi}; return __builtin_bit_cast(unsigned, __builtin_convertvector(v, bf16x2h_t)); }
; DI float silu_f(float x) { return x * __builtin_amdgcn_rcpf(1.f + __expf(-x)); }
; DI void ssd_local_unit(Frame& F, int l, int ch, int g) {
;     ...
;         for (int cc = 0; cc < 4; ++cc) {
;             const int lc = cg * 32 + cc * 8, c0 = part * 256 + g * 128 + lc;
;             float acc[8];
;             { const f32x4 b0 = *(const f32x4*)(cb + c0), b1 = *(const f32x4*)(cb + c0 + 4);
; #pragma unroll
;               for (int e = 0; e < 4; ++e) { acc[e] = b0[e]; acc[4 + e] = b1[e]; } }
; #pragma unroll
;             for (int j = 0; j < 4; ++j) { float x[8]; unpack8(raw[cc][j], x);
;                 const f32x4 w0 = *(const f32x4*)(cw + j * XC + c0), w1 = *(const f32x4*)(cw + j * XC + c0 + 4);
; #pragma unroll
;                 for (int e = 0; e < 4; ++e) { acc[e] += w0[e] * okm[j] * x[e]; acc[4 + e] += w1[e] * okm[j] * x[4 + e]; } }
; #pragma unroll
;             for (int e = 0; e < 8; ++e) acc[e] = silu_f(acc[e]);
;             v4u o; o.x = pk2h(acc[0], acc[1]); o.y = pk2h(acc[2], acc[3]); o.z = pk2h(acc[4], acc[5]); o.w = pk2h(acc[6], acc[7]);
;             *(v4u*)(xbcc + (size_t)(t0 + s) * XC + c0) = o;
;             if (part == 0) { const int r2 = lc >> 6; const float dtv = DT[r2 * 128 + s], sc = dtv * __expf(AC[r2 * 128 + 127] - AC[r2 * 128 + s]);
; #pragma unroll
;                 for (int e = 0; e < 8; ++e) { XWT[(lc + e) * LP + s] = (bf16)f2bf(acc[e] * sc); XD[(lc + e) * LP + s] = (bf16)f2bf(acc[e] * dtv); } }
;     ...
;     __syncthreads();
;     const int w = F.wave, r = F.lane & 15, q = F.lane >> 4;
;     f32x4 acc[8];
; #pragma unroll
;     for (int nt = 0; nt < 8; ++nt) acc[nt] = (f32x4){0.f, 0.f, 0.f, 0.f};
; #pragma unroll
;     for (int ks = 0; ks < 4; ++ks) { const bf16x8 a = *(const LAS bf16x8*)(XWT + (16 * w + r) * LP + 32 * ks + 8 * q);
	v_pk_mul_f32 v[42:43], v[134:135], v[50:51] op_sel_hi:[0,1]
	v_pk_fma_f32 v[24:25], v[42:43], v[32:33], v[24:25]
	v_lshlrev_b32_e32 v8, 16, v9
	v_mul_f32_e32 v0, 0xbfb8aa3b, v24
	v_exp_f32_e32 v0, v0
	v_and_b32_e32 v9, 0xffff0000, v9
	v_add_f32_e32 v0, 1.0, v0
	v_rcp_f32_e32 v32, v0
	v_mul_f32_e32 v0, 0xbfb8aa3b, v25
	v_exp_f32_e32 v0, v0
	s_nop 0
	v_add_f32_e32 v0, 1.0, v0
	v_rcp_f32_e32 v33, v0
	s_nop 0
	v_pk_mul_f32 v[24:25], v[24:25], v[32:33]
	v_pk_mul_f32 v[32:33], v[140:141], v[34:35] op_sel_hi:[0,1]
	v_pk_fma_f32 v[4:5], v[32:33], v[4:5], v[26:27]
	v_pk_mul_f32 v[26:27], v[138:139], v[44:45] op_sel_hi:[0,1]
	v_pk_fma_f32 v[4:5], v[26:27], v[8:9], v[4:5]
	v_lshlrev_b32_e32 v8, 16, v13
	v_and_b32_e32 v9, 0xffff0000, v13
	v_pk_mul_f32 v[12:13], v[136:137], v[48:49] op_sel_hi:[0,1]
	v_pk_fma_f32 v[4:5], v[12:13], v[8:9], v[4:5]
	v_lshlrev_b32_e32 v8, 16, v17
	v_and_b32_e32 v9, 0xffff0000, v17
	v_pk_mul_f32 v[12:13], v[134:135], v[52:53] op_sel_hi:[0,1]
	v_pk_fma_f32 v[4:5], v[12:13], v[8:9], v[4:5]
	v_pk_mul_f32 v[12:13], v[140:141], v[28:29] op_sel_hi:[0,1]
	v_mul_f32_e32 v0, 0xbfb8aa3b, v4
	v_exp_f32_e32 v0, v0
	v_pk_mul_f32 v[16:17], v[138:139], v[36:37] op_sel_hi:[0,1]
	v_add_f32_e32 v0, 1.0, v0
	v_rcp_f32_e32 v8, v0
	v_mul_f32_e32 v0, 0xbfb8aa3b, v5
	v_exp_f32_e32 v0, v0
	s_nop 0
	v_add_f32_e32 v0, 1.0, v0
	v_rcp_f32_e32 v9, v0
	s_nop 0
	v_pk_mul_f32 v[8:9], v[4:5], v[8:9]
	v_lshlrev_b32_e32 v4, 16, v6
	v_and_b32_e32 v5, 0xffff0000, v6
	v_pk_fma_f32 v[4:5], v[12:13], v[4:5], v[20:21]
	v_lshlrev_b32_e32 v12, 16, v10
	v_and_b32_e32 v13, 0xffff0000, v10
	v_pk_fma_f32 v[4:5], v[16:17], v[12:13], v[4:5]
	v_lshlrev_b32_e32 v12, 16, v14
	v_and_b32_e32 v13, 0xffff0000, v14
	v_pk_mul_f32 v[16:17], v[136:137], v[66:67] op_sel_hi:[0,1]
	v_pk_fma_f32 v[4:5], v[16:17], v[12:13], v[4:5]
	v_lshlrev_b32_e32 v12, 16, v18
	v_and_b32_e32 v13, 0xffff0000, v18
	s_waitcnt vmcnt(0)
	v_pk_mul_f32 v[16:17], v[134:135], v[54:55] op_sel_hi:[0,1]
	v_pk_fma_f32 v[4:5], v[16:17], v[12:13], v[4:5]
	s_nop 0
	v_mul_f32_e32 v0, 0xbfb8aa3b, v4
	v_exp_f32_e32 v0, v0
	s_nop 0
	v_add_f32_e32 v0, 1.0, v0
	v_rcp_f32_e32 v12, v0
	v_mul_f32_e32 v0, 0xbfb8aa3b, v5
	v_exp_f32_e32 v0, v0
	s_nop 0
	v_add_f32_e32 v0, 1.0, v0
	v_rcp_f32_e32 v13, v0
	s_nop 0
	v_pk_mul_f32 v[12:13], v[4:5], v[12:13]
	v_lshlrev_b32_e32 v4, 16, v7
	v_and_b32_e32 v5, 0xffff0000, v7
	v_pk_mul_f32 v[6:7], v[140:141], v[30:31] op_sel_hi:[0,1]
	v_pk_fma_f32 v[4:5], v[6:7], v[4:5], v[22:23]
	v_lshlrev_b32_e32 v6, 16, v11
	v_and_b32_e32 v7, 0xffff0000, v11
	v_pk_mul_f32 v[10:11], v[138:139], v[38:39] op_sel_hi:[0,1]
	v_pk_fma_f32 v[4:5], v[10:11], v[6:7], v[4:5]
	v_lshlrev_b32_e32 v6, 16, v15
	v_and_b32_e32 v7, 0xffff0000, v15
	v_pk_mul_f32 v[10:11], v[136:137], v[68:69] op_sel_hi:[0,1]
	v_pk_fma_f32 v[4:5], v[10:11], v[6:7], v[4:5]
	v_lshlrev_b32_e32 v6, 16, v19
	v_and_b32_e32 v7, 0xffff0000, v19
	v_pk_mul_f32 v[10:11], v[134:135], v[56:57] op_sel_hi:[0,1]
	v_pk_fma_f32 v[4:5], v[10:11], v[6:7], v[4:5]
	s_nop 0
	v_mul_f32_e32 v0, 0xbfb8aa3b, v4
	v_exp_f32_e32 v0, v0
	s_nop 0
	v_add_f32_e32 v0, 1.0, v0
	v_rcp_f32_e32 v6, v0
	v_mul_f32_e32 v0, 0xbfb8aa3b, v5
	v_exp_f32_e32 v0, v0
	s_nop 0
	v_add_f32_e32 v0, 1.0, v0
	v_rcp_f32_e32 v7, v0
	v_mul_f32_e32 v0, v61, v24
	v_bfe_u32 v2, v0, 16, 1
	v_add3_u32 v0, v0, v2, s97
	v_pk_mul_f32 v[10:11], v[4:5], v[6:7]
	v_mul_u32_u24_e32 v2, 0x88, v139
	v_cvt_pk_bf16_f32 v4, v24, v25
	v_cvt_pk_bf16_f32 v5, v8, v9
	v_cvt_pk_bf16_f32 v6, v12, v13
	v_cvt_pk_bf16_f32 v7, v10, v11
	v_lshlrev_b32_e32 v2, 1, v2
	global_store_dwordx4 v[40:41], v[4:7], off offset:48
	s_nop 1
	v_add_u32_e32 v4, v135, v2
	ds_write_b16_d16_hi v4, v0
	v_mul_f32_e32 v0, v60, v24
	v_bfe_u32 v4, v0, 16, 1
	v_add3_u32 v0, v0, v4, s97
	v_add_u32_e32 v2, v64, v2
	ds_write_b16_d16_hi v2, v0
	v_mul_f32_e32 v0, v61, v25
	v_bfe_u32 v2, v0, 16, 1
	v_add3_u32 v0, v0, v2, s97
	ds_write_b16_d16_hi v62, v0 offset:6800
	v_mul_f32_e32 v0, v60, v25
	v_bfe_u32 v2, v0, 16, 1
	v_add3_u32 v0, v0, v2, s97
	ds_write_b16_d16_hi v63, v0 offset:6800
	v_mul_f32_e32 v0, v61, v8
	v_bfe_u32 v2, v0, 16, 1
	v_add3_u32 v0, v0, v2, s97
	ds_write_b16_d16_hi v62, v0 offset:7072
	v_mul_f32_e32 v0, v60, v8
	v_bfe_u32 v2, v0, 16, 1
	v_add3_u32 v0, v0, v2, s97
	ds_write_b16_d16_hi v63, v0 offset:7072
	v_mul_f32_e32 v0, v61, v9
	v_bfe_u32 v2, v0, 16, 1
	v_add3_u32 v0, v0, v2, s97
	ds_write_b16_d16_hi v62, v0 offset:7344
	v_mul_f32_e32 v0, v60, v9
	v_bfe_u32 v2, v0, 16, 1
	v_add3_u32 v0, v0, v2, s97
	ds_write_b16_d16_hi v63, v0 offset:7344
	v_mul_f32_e32 v0, v61, v12
	v_bfe_u32 v2, v0, 16, 1
	v_add3_u32 v0, v0, v2, s97
	ds_write_b16_d16_hi v62, v0 offset:7616
	v_mul_f32_e32 v0, v60, v12
	v_bfe_u32 v2, v0, 16, 1
	v_add3_u32 v0, v0, v2, s97
	ds_write_b16_d16_hi v63, v0 offset:7616
	v_mul_f32_e32 v0, v61, v13
	v_bfe_u32 v2, v0, 16, 1
	v_add3_u32 v0, v0, v2, s97
	ds_write_b16_d16_hi v62, v0 offset:7888
	v_mul_f32_e32 v0, v60, v13
	v_bfe_u32 v2, v0, 16, 1
	v_add3_u32 v0, v0, v2, s97
	ds_write_b16_d16_hi v63, v0 offset:7888
	v_mul_f32_e32 v0, v61, v10
	v_bfe_u32 v2, v0, 16, 1
	v_add3_u32 v0, v0, v2, s97
	ds_write_b16_d16_hi v62, v0 offset:8160
	v_mul_f32_e32 v0, v60, v10
	v_bfe_u32 v2, v0, 16, 1
	v_add3_u32 v0, v0, v2, s97
	ds_write_b16_d16_hi v63, v0 offset:8160
	v_mul_f32_e32 v0, v61, v11
	v_bfe_u32 v2, v0, 16, 1
	v_add3_u32 v0, v0, v2, s97
	ds_write_b16_d16_hi v62, v0 offset:8432
	v_mul_f32_e32 v0, v60, v11
	v_bfe_u32 v2, v0, 16, 1
	v_add3_u32 v0, v0, v2, s97
	ds_write_b16_d16_hi v63, v0 offset:8432
	v_and_b32_e32 v2, 15, v132
	v_and_b32_e32 v0, 48, v133
	v_lshl_or_b32 v4, s37, 4, v2
	v_add_u32_e32 v0, s19, v0
	v_mad_u64_u32 v[48:49], s[0:1], v4, s66, v[0:1]
	v_mad_u32_u24 v0, v2, s66, v0
	s_waitcnt lgkmcnt(0)
	s_barrier
; #define LAS __attribute__((address_space(3)))
; DI f32x4 mfma16(bf16x8 a, bf16x8 b, f32x4 c) { asm volatile("s_nop 3" : "+v"(a), "+v"(b)); return __builtin_amdgcn_mfma_f32_16x16x32_bf16(a, b, c, 0, 0, 0); }
; DI void ssd_local_unit(Frame& F, int l, int ch, int g) {
;     ...
;     const int w = F.wave, r = F.lane & 15, q = F.lane >> 4;
;     f32x4 acc[8];
; #pragma unroll
;     for (int nt = 0; nt < 8; ++nt) acc[nt] = (f32x4){0.f, 0.f, 0.f, 0.f};
; #pragma unroll
;     for (int ks = 0; ks < 4; ++ks) { const bf16x8 a = *(const LAS bf16x8*)(XWT + (16 * w + r) * LP + 32 * ks + 8 * q);
; #pragma unroll
;         for (int nt = 0; nt < 8; ++nt) { const bf16x8 b = *(const LAS bf16x8*)(BT + (16 * nt + r) * LP + 32 * ks + 8 * q); acc[nt] = mfma16(a, b, acc[nt]); } }
	ds_read_b128 v[4:7], v0 offset:34816
	ds_read_b128 v[8:11], v48
	s_ashr_i32 s0, s38, 8
	s_add_i32 s0, s0, s2
	s_ashr_i32 s1, s0, 31
	s_lshl_b64 s[0:1], s[0:1], 15
	s_waitcnt lgkmcnt(0)
	v_mov_b64_e32 v[14:15], v[10:11]
	v_mov_b64_e32 v[12:13], v[8:9]
	s_nop 3
	v_mov_b64_e32 v[18:19], v[10:11]
	v_mov_b64_e32 v[16:17], v[8:9]
	v_mfma_f32_16x16x32_bf16 v[4:7], v[4:7], v[12:15], 0
	ds_read_b128 v[12:15], v0 offset:39168
	s_waitcnt lgkmcnt(0)
	s_nop 3
	v_mov_b64_e32 v[22:23], v[10:11]
	v_mfma_f32_16x16x32_bf16 v[12:15], v[12:15], v[16:19], 0
	ds_read_b128 v[16:19], v0 offset:43520
	v_mov_b64_e32 v[20:21], v[8:9]
	s_waitcnt lgkmcnt(0)
	s_nop 3
	v_mov_b64_e32 v[26:27], v[10:11]
	v_mov_b64_e32 v[24:25], v[8:9]
	v_mfma_f32_16x16x32_bf16 v[16:19], v[16:19], v[20:23], 0
	ds_read_b128 v[20:23], v0 offset:47872
	s_waitcnt lgkmcnt(0)
	s_nop 3
	v_mov_b64_e32 v[30:31], v[10:11]
	v_mfma_f32_16x16x32_bf16 v[20:23], v[20:23], v[24:27], 0
	ds_read_b128 v[24:27], v0 offset:52224
	v_mov_b64_e32 v[28:29], v[8:9]
	s_waitcnt lgkmcnt(0)
	s_nop 3
	v_mov_b64_e32 v[34:35], v[10:11]
	v_mov_b64_e32 v[32:33], v[8:9]
	v_mfma_f32_16x16x32_bf16 v[24:27], v[24:27], v[28:31], 0
	ds_read_b128 v[28:31], v0 offset:56576
	s_waitcnt lgkmcnt(0)
	s_nop 3
	v_mov_b64_e32 v[38:39], v[10:11]
	v_mfma_f32_16x16x32_bf16 v[28:31], v[28:31], v[32:35], 0
	ds_read_b128 v[32:35], v0 offset:60928
	v_mov_b64_e32 v[36:37], v[8:9]
	s_waitcnt lgkmcnt(0)
	s_nop 3
	s_add_u32 s0, s20, s0
	s_addc_u32 s1, s21, s1
	v_mfma_f32_16x16x32_bf16 v[32:35], v[32:35], v[36:39], 0
	ds_read_b128 v[36:39], v0 offset:65280
	s_waitcnt lgkmcnt(0)
	s_nop 3
	v_lshlrev_b32_e32 v2, 2, v2
	v_mfma_f32_16x16x32_bf16 v[8:11], v[36:39], v[8:11], 0
	ds_read_b128 v[36:39], v0 offset:34880
	ds_read_b128 v[40:43], v48 offset:64
	s_waitcnt lgkmcnt(0)
	v_mov_b64_e32 v[46:47], v[42:43]
	v_mov_b64_e32 v[44:45], v[40:41]
	s_nop 3
	s_nop 1
	v_mfma_f32_16x16x32_bf16 v[4:7], v[36:39], v[44:47], v[4:7]
	v_mov_b64_e32 v[46:47], v[42:43]
	ds_read_b128 v[36:39], v0 offset:39232
	v_mov_b64_e32 v[44:45], v[40:41]
	s_waitcnt lgkmcnt(0)
	s_nop 3
	s_nop 0
	v_mfma_f32_16x16x32_bf16 v[12:15], v[36:39], v[44:47], v[12:15]
	v_mov_b64_e32 v[46:47], v[42:43]
	ds_read_b128 v[36:39], v0 offset:43584
	v_mov_b64_e32 v[44:45], v[40:41]
	s_waitcnt lgkmcnt(0)
	s_nop 3
	s_nop 0
	v_mfma_f32_16x16x32_bf16 v[16:19], v[36:39], v[44:47], v[16:19]
	v_mov_b64_e32 v[46:47], v[42:43]
	ds_read_b128 v[36:39], v0 offset:47936
	v_mov_b64_e32 v[44:45], v[40:41]
	s_waitcnt lgkmcnt(0)
	s_nop 3
	s_nop 0
	v_mfma_f32_16x16x32_bf16 v[20:23], v[36:39], v[44:47], v[20:23]
	v_mov_b64_e32 v[46:47], v[42:43]
	ds_read_b128 v[36:39], v0 offset:52288
	v_mov_b64_e32 v[44:45], v[40:41]
	s_waitcnt lgkmcnt(0)
	s_nop 3
	s_nop 0
	v_mfma_f32_16x16x32_bf16 v[24:27], v[36:39], v[44:47], v[24:27]
	v_mov_b64_e32 v[46:47], v[42:43]
	ds_read_b128 v[36:39], v0 offset:56640
	v_mov_b64_e32 v[44:45], v[40:41]
	s_waitcnt lgkmcnt(0)
	s_nop 3
	s_nop 0
	v_mfma_f32_16x16x32_bf16 v[28:31], v[36:39], v[44:47], v[28:31]
	v_mov_b64_e32 v[46:47], v[42:43]
	ds_read_b128 v[36:39], v0 offset:60992
	v_mov_b64_e32 v[44:45], v[40:41]
	s_waitcnt lgkmcnt(0)
	s_nop 3
	s_nop 0
	v_mfma_f32_16x16x32_bf16 v[32:35], v[36:39], v[44:47], v[32:35]
	ds_read_b128 v[36:39], v0 offset:65344
	s_waitcnt lgkmcnt(0)
	s_nop 3
	s_nop 0
	v_mfma_f32_16x16x32_bf16 v[8:11], v[36:39], v[40:43], v[8:11]
	ds_read_b128 v[36:39], v0 offset:34944
	ds_read_b128 v[40:43], v48 offset:128
	s_waitcnt lgkmcnt(0)
	v_mov_b64_e32 v[46:47], v[42:43]
	v_mov_b64_e32 v[44:45], v[40:41]
	s_nop 3
	s_nop 1
	v_mfma_f32_16x16x32_bf16 v[4:7], v[36:39], v[44:47], v[4:7]
	v_mov_b64_e32 v[46:47], v[42:43]
	ds_read_b128 v[36:39], v0 offset:39296
	v_mov_b64_e32 v[44:45], v[40:41]
	s_waitcnt lgkmcnt(0)
	s_nop 3
	s_nop 0
	v_mfma_f32_16x16x32_bf16 v[12:15], v[36:39], v[44:47], v[12:15]
	v_mov_b64_e32 v[46:47], v[42:43]
	ds_read_b128 v[36:39], v0 offset:43648
	v_mov_b64_e32 v[44:45], v[40:41]
	s_waitcnt lgkmcnt(0)
	s_nop 3
	s_nop 0
	v_mfma_f32_16x16x32_bf16 v[16:19], v[36:39], v[44:47], v[16:19]
	v_mov_b64_e32 v[46:47], v[42:43]
	ds_read_b128 v[36:39], v0 offset:48000
	v_mov_b64_e32 v[44:45], v[40:41]
	s_waitcnt lgkmcnt(0)
; #define LAS __attribute__((address_space(3)))
; DI f32x4 mfma16(bf16x8 a, bf16x8 b, f32x4 c) { asm volatile("s_nop 3" : "+v"(a), "+v"(b)); return __builtin_amdgcn_mfma_f32_16x16x32_bf16(a, b, c, 0, 0, 0); }
; DI void ssd_local_unit(Frame& F, int l, int ch, int g) {
;     ...
; #pragma unroll
;     for (int ks = 0; ks < 4; ++ks) { const bf16x8 a = *(const LAS bf16x8*)(XWT + (16 * w + r) * LP + 32 * ks + 8 * q);
; #pragma unroll
;         for (int nt = 0; nt < 8; ++nt) { const bf16x8 b = *(const LAS bf16x8*)(BT + (16 * nt + r) * LP + 32 * ks + 8 * q); acc[nt] = mfma16(a, b, acc[nt]); } }
;     float* sst = (float*)(F.ws + WS_SST);
; #pragma unroll
;     for (int jj = 0; jj < 4; ++jj) { const int row = 16 * w + 4 * q + jj, head = 2 * g + (row >> 6), p = row & 63;
;         float* o = sst + ((size_t)(ch * 4 + head) * 64 + p) * 128 + r;
; #pragma unroll
;         for (int nt = 0; nt < 8; ++nt) o[16 * nt] = acc[nt][jj]; }
;     if (F.tid < 2) ((float*)(F.ws + WS_SMALL))[ch * 4 + 2 * g + F.tid] = __expf(AC[F.tid * 128 + 127]);
;     tile_l2g((bf16*)(F.ws + WS_XDT) + (size_t)(ch * 2 + g) * 128 * 128, 128, XD, LP, 128, 128, F.tid);
	s_nop 3
	s_nop 0
	v_mfma_f32_16x16x32_bf16 v[20:23], v[36:39], v[44:47], v[20:23]
	v_mov_b64_e32 v[46:47], v[42:43]
	ds_read_b128 v[36:39], v0 offset:52352
	v_mov_b64_e32 v[44:45], v[40:41]
	s_waitcnt lgkmcnt(0)
	s_nop 3
	s_nop 0
	v_mfma_f32_16x16x32_bf16 v[24:27], v[36:39], v[44:47], v[24:27]
	v_mov_b64_e32 v[46:47], v[42:43]
	ds_read_b128 v[36:39], v0 offset:56704
	v_mov_b64_e32 v[44:45], v[40:41]
	s_waitcnt lgkmcnt(0)
	s_nop 3
	s_nop 0
	v_mfma_f32_16x16x32_bf16 v[28:31], v[36:39], v[44:47], v[28:31]
	v_mov_b64_e32 v[46:47], v[42:43]
	ds_read_b128 v[36:39], v0 offset:61056
	v_mov_b64_e32 v[44:45], v[40:41]
	s_waitcnt lgkmcnt(0)
	s_nop 3
	s_nop 0
	v_mfma_f32_16x16x32_bf16 v[32:35], v[36:39], v[44:47], v[32:35]
	ds_read_b128 v[36:39], v0 offset:65408
	s_waitcnt lgkmcnt(0)
	s_nop 3
	s_nop 0
	v_mfma_f32_16x16x32_bf16 v[36:39], v[36:39], v[40:43], v[8:11]
	s_nop 2
	ds_read_b128 v[8:11], v0 offset:35008
	ds_read_b128 v[40:43], v48 offset:192
	s_waitcnt lgkmcnt(0)
	v_mov_b64_e32 v[46:47], v[42:43]
	v_mov_b64_e32 v[44:45], v[40:41]
	s_nop 3
	s_nop 1
	v_mfma_f32_16x16x32_bf16 v[4:7], v[8:11], v[44:47], v[4:7]
	v_mov_b64_e32 v[46:47], v[42:43]
	ds_read_b128 v[8:11], v0 offset:39360
	v_mov_b64_e32 v[44:45], v[40:41]
	s_waitcnt lgkmcnt(0)
	s_nop 3
	s_nop 0
	v_mfma_f32_16x16x32_bf16 v[8:11], v[8:11], v[44:47], v[12:15]
	v_mov_b64_e32 v[46:47], v[42:43]
	v_mov_b64_e32 v[44:45], v[40:41]
	s_nop 0
	ds_read_b128 v[12:15], v0 offset:43712
	s_waitcnt lgkmcnt(0)
	s_nop 3
	s_nop 0
	v_mfma_f32_16x16x32_bf16 v[12:15], v[12:15], v[44:47], v[16:19]
	v_mov_b64_e32 v[46:47], v[42:43]
	v_mov_b64_e32 v[44:45], v[40:41]
	s_nop 0
	ds_read_b128 v[16:19], v0 offset:48064
	s_waitcnt lgkmcnt(0)
	s_nop 3
	s_nop 0
	v_mfma_f32_16x16x32_bf16 v[16:19], v[16:19], v[44:47], v[20:23]
	v_mov_b64_e32 v[46:47], v[42:43]
	v_mov_b64_e32 v[44:45], v[40:41]
	s_nop 0
	ds_read_b128 v[20:23], v0 offset:52416
	s_waitcnt lgkmcnt(0)
	s_nop 3
	s_nop 0
	v_mfma_f32_16x16x32_bf16 v[20:23], v[20:23], v[44:47], v[24:27]
	v_mov_b64_e32 v[46:47], v[42:43]
	v_mov_b64_e32 v[44:45], v[40:41]
	s_nop 0
	ds_read_b128 v[24:27], v0 offset:56768
	s_waitcnt lgkmcnt(0)
	s_nop 3
	s_nop 0
	v_mfma_f32_16x16x32_bf16 v[24:27], v[24:27], v[44:47], v[28:31]
	v_mov_b64_e32 v[46:47], v[42:43]
	v_mov_b64_e32 v[44:45], v[40:41]
	s_nop 0
	ds_read_b128 v[28:31], v0 offset:61120
	s_waitcnt lgkmcnt(0)
	s_nop 3
	s_nop 0
	v_mfma_f32_16x16x32_bf16 v[28:31], v[28:31], v[44:47], v[32:35]
	s_nop 2
	ds_read_b128 v[32:35], v0 offset:65472
	s_waitcnt lgkmcnt(0)
	s_nop 3
	v_lshlrev_b32_e32 v0, 7, v133
	v_mfma_f32_16x16x32_bf16 v[32:35], v[32:35], v[40:43], v[36:39]
	s_nop 2
	v_lshl_add_u64 v[36:37], s[0:1], 0, v[2:3]
	s_lshl_b32 s0, s37, 13
	v_mov_b32_e32 v2, s0
	s_movk_i32 s0, 0x7800
	v_bitop3_b32 v2, v0, s0, v2 bitop3:0xc8
	v_lshl_add_u64 v[38:39], v[36:37], 0, v[2:3]
	s_mov_b64 s[0:1], 0x1f100000
	v_lshl_add_u64 v[36:37], v[38:39], 0, s[0:1]
	s_mov_b32 s0, 0x1f100000
	v_add_co_u32_e32 v38, vcc, s0, v38
	s_nop 1
	v_addc_co_u32_e32 v39, vcc, 0, v39, vcc
	v_cmp_gt_i32_e32 vcc, 2, v132
	v_and_b32_e32 v40, 15, v133
	v_lshrrev_b32_e32 v41, 4, v133
	v_mul_u32_u24_e32 v40, 0x1fc, v40
	v_mul_u32_u24_e32 v41, 0x7f0, v41
	v_sub_u32_e32 v40, v40, v41
	v_ashrrev_i32_e32 v41, 31, v40
	v_lshl_add_u64 v[36:37], v[36:37], 0, v[40:41]
	s_nop 7
	global_store_dwordx4 v[36:37], v[4:7], off
	global_store_dwordx4 v[36:37], v[8:11], off offset:64
	global_store_dwordx4 v[36:37], v[12:15], off offset:128
	global_store_dwordx4 v[36:37], v[16:19], off offset:192
	global_store_dwordx4 v[36:37], v[20:23], off offset:256
	global_store_dwordx4 v[36:37], v[24:27], off offset:320
	global_store_dwordx4 v[36:37], v[28:31], off offset:384
	global_store_dwordx4 v[36:37], v[32:35], off offset:448
	s_and_saveexec_b64 s[0:1], vcc
	s_cbranch_execz .LBB0_840
	v_lshl_add_u32 v0, v132, 9, s36
	ds_read_b32 v0, v0 offset:508
	v_add_u32_e32 v4, s2, v132
	v_ashrrev_i32_e32 v5, 31, v4
	v_lshl_add_u64 v[4:5], v[4:5], 2, s[20:21]
	v_add_co_u32_e32 v4, vcc, 0x300000, v4
	s_waitcnt lgkmcnt(0)
	v_mul_f32_e32 v0, 0x3fb8aa3b, v0
	v_exp_f32_e32 v0, v0
	v_addc_co_u32_e32 v5, vcc, 0, v5, vcc
	global_store_dword v[4:5], v0, off

; #define LAS __attribute__((address_space(3)))
; DI unsigned pk2h(float lo, float hi) { const f32x2h_t v = {lo, hi}; return __builtin_bit_cast(unsigned, __builtin_convertvector(v, bf16x2h_t)); }
; DI void ml_local_unit(Frame& F, int l, int ch, int h, const MlLPre& P) {
;     ...
;     if (F.tid < 64) *(LAS unsigned*)(VWT + 64 * LP + 2 * F.tid) = pk2h(WG[2 * F.tid], WG[2 * F.tid + 1]);
;     {
;       const float wg0 = WG[s2], wg1 = WG[s2 + 1];
;       float x0[8], x1[8];
;       unpack8(rv0, x0); unpack8(rv1, x1);
; #pragma unroll
;       for (int e = 0; e < 8; ++e) *(LAS unsigned*)(VWT + (c0 + e) * LP + s2) = pk2h(x0[e] * wg0, x1[e] * wg1);
;       unpack8(rk0, x0); unpack8(rk1, x1);
; #pragma unroll
;       for (int e = 0; e < 8; ++e) *(LAS unsigned*)(KT + (c0 + e) * LP + s2) = pk2h(x0[e] * 0.125f, x1[e] * 0.125f); }
;     __syncthreads();
;     const int w = F.wave, r = F.lane & 15, q = F.lane >> 4;
;     float* mls = (float*)(F.ws + WS_MLS + ML_ALT(F.l) * (406 * MiB)) + (size_t)(ch * 4 + h) * 5120;
; #pragma unroll
;     for (int it = 0; it < 3; ++it) { const int mt = (it < 2) ? (w >> 1) : 4, nt = (it < 2) ? 2 * (w & 1) + it : w;
.LBB0_863:
	s_or_b64 exec, exec, s[0:1]
	v_ashrrev_i32_e32 v0, 2, v132
	v_and_b32_e32 v38, -2, v0
	v_lshl_add_u32 v0, v38, 2, s17
	v_bitop3_b32 v2, v132, -4, 4 bitop3:0xc8
	v_add_u32_e32 v2, s17, v2
	ds_read_b32 v42, v0 offset:40192
	ds_read_b32 v43, v2 offset:40192
	s_waitcnt vmcnt(5)
	v_lshlrev_b32_e32 v45, 16, v28
	v_lshlrev_b32_e32 v44, 16, v20
	v_lshlrev_b32_e32 v2, 1, v38
	v_sub_u32_e32 v0, v0, v2
	s_waitcnt lgkmcnt(0)
	v_pk_mul_f32 v[44:45], v[42:43], v[44:45]
	v_and_b32_e32 v40, 56, v39
	v_cvt_pk_bf16_f32 v2, v44, v45
	v_and_b32_e32 v45, 0xffff0000, v28
	v_and_b32_e32 v44, 0xffff0000, v20
	v_pk_mul_f32 v[44:45], v[42:43], v[44:45]
	v_mad_u32_u24 v0, v40, s66, v0
	v_cvt_pk_bf16_f32 v20, v44, v45
	v_lshlrev_b32_e32 v45, 16, v29
	v_lshlrev_b32_e32 v44, 16, v21
	v_and_b32_e32 v29, 0xffff0000, v29
	v_and_b32_e32 v28, 0xffff0000, v21
	ds_write2_b32 v0, v2, v20 offset1:68
	v_pk_mul_f32 v[44:45], v[42:43], v[44:45]
	v_pk_mul_f32 v[20:21], v[42:43], v[28:29]
	v_cvt_pk_bf16_f32 v2, v44, v45
	v_cvt_pk_bf16_f32 v20, v20, v21
	ds_write2_b32 v0, v2, v20 offset0:136 offset1:204
	v_lshlrev_b32_e32 v21, 16, v30
	v_lshlrev_b32_e32 v20, 16, v22
	v_pk_mul_f32 v[20:21], v[42:43], v[20:21]
	s_mov_b32 s0, 0x3e000000
	v_cvt_pk_bf16_f32 v2, v20, v21
	v_and_b32_e32 v21, 0xffff0000, v30
	v_and_b32_e32 v20, 0xffff0000, v22
	v_pk_mul_f32 v[20:21], v[42:43], v[20:21]
	v_add_u32_e32 v22, 0x400, v0
	v_cvt_pk_bf16_f32 v20, v20, v21
	ds_write2_b32 v22, v2, v20 offset0:16 offset1:84
	v_lshlrev_b32_e32 v21, 16, v31
	v_lshlrev_b32_e32 v20, 16, v23
	v_pk_mul_f32 v[20:21], v[42:43], v[20:21]
	s_nop 0
	v_cvt_pk_bf16_f32 v2, v20, v21
	v_and_b32_e32 v21, 0xffff0000, v31
	v_and_b32_e32 v20, 0xffff0000, v23
	v_pk_mul_f32 v[20:21], v[42:43], v[20:21]
	s_nop 0
	v_cvt_pk_bf16_f32 v20, v20, v21
	ds_write2_b32 v22, v2, v20 offset0:152 offset1:220
	s_waitcnt vmcnt(1)
	v_lshlrev_b32_e32 v21, 16, v8
	v_lshlrev_b32_e32 v20, 16, v4
	v_pk_mul_f32 v[20:21], v[20:21], s[0:1] op_sel_hi:[1,0]
	s_nop 0
	v_cvt_pk_bf16_f32 v2, v20, v21
	v_and_b32_e32 v21, 0xffff0000, v8
	v_and_b32_e32 v20, 0xffff0000, v4
	v_pk_mul_f32 v[20:21], v[20:21], s[0:1] op_sel_hi:[1,0]
	v_add_u32_e32 v8, 0x5400, v0
	v_cvt_pk_bf16_f32 v4, v20, v21
	ds_write2_b32 v8, v2, v4 offset0:64 offset1:132
	v_lshlrev_b32_e32 v21, 16, v9
	v_lshlrev_b32_e32 v20, 16, v5
	v_and_b32_e32 v9, 0xffff0000, v9
	v_and_b32_e32 v8, 0xffff0000, v5
	v_pk_mul_f32 v[20:21], v[20:21], s[0:1] op_sel_hi:[1,0]
	v_pk_mul_f32 v[4:5], v[8:9], s[0:1] op_sel_hi:[1,0]
	v_cvt_pk_bf16_f32 v2, v20, v21
	v_cvt_pk_bf16_f32 v4, v4, v5
	v_add_u32_e32 v5, 0x5600, v0
	ds_write2_b32 v5, v2, v4 offset0:72 offset1:140
	v_lshlrev_b32_e32 v5, 16, v10
	v_lshlrev_b32_e32 v4, 16, v6
	v_pk_mul_f32 v[4:5], v[4:5], s[0:1] op_sel_hi:[1,0]
	s_nop 0
	v_cvt_pk_bf16_f32 v2, v4, v5
	v_and_b32_e32 v5, 0xffff0000, v10
	v_and_b32_e32 v4, 0xffff0000, v6
	v_pk_mul_f32 v[4:5], v[4:5], s[0:1] op_sel_hi:[1,0]
	s_nop 0
	v_cvt_pk_bf16_f32 v4, v4, v5
	v_add_u32_e32 v5, 0x5800, v0
	ds_write2_b32 v5, v2, v4 offset0:80 offset1:148
	v_lshlrev_b32_e32 v5, 16, v11
	v_lshlrev_b32_e32 v4, 16, v7
	v_pk_mul_f32 v[4:5], v[4:5], s[0:1] op_sel_hi:[1,0]
	v_add_u32_e32 v0, 0x5a00, v0
	v_cvt_pk_bf16_f32 v2, v4, v5
	v_and_b32_e32 v5, 0xffff0000, v11
	v_and_b32_e32 v4, 0xffff0000, v7
	v_pk_mul_f32 v[4:5], v[4:5], s[0:1] op_sel_hi:[1,0]
	s_mul_i32 s1, s18, 0x5000
	s_mul_hi_i32 s0, s18, 0x5000
	s_add_u32 s1, s4, s1
	s_addc_u32 s6, s5, s0
	v_cvt_pk_bf16_f32 v4, v4, v5
	s_add_u32 s0, s1, 0x22100000
	ds_write2_b32 v0, v2, v4 offset0:88 offset1:156
	s_addc_u32 s1, s6, 0
	s_lshl_b32 s21, s19, 3
	v_and_b32_e32 v0, 48, v1
	v_and_b32_e32 v4, 15, v132
	s_lshl_b32 s20, s19, 5
	v_add_u32_e32 v2, s17, v0
	v_bfi_b32 v0, -16, s21, v132
	v_mad_u64_u32 v[10:11], s[6:7], v0, s66, v[2:3]
	v_and_or_b32 v0, s20, 32, v4
	v_mad_u32_u24 v5, v0, s66, v2
	s_waitcnt lgkmcnt(0)
	s_barrier
; #define LAS __attribute__((address_space(3)))
; DI f32x4 mfma16(bf16x8 a, bf16x8 b, f32x4 c) { asm volatile("s_nop 3" : "+v"(a), "+v"(b)); return __builtin_amdgcn_mfma_f32_16x16x32_bf16(a, b, c, 0, 0, 0); }
; DI void ml_local_unit(Frame& F, int l, int ch, int h, const MlLPre& P) {
;     ...
; #pragma unroll
;     for (int it = 0; it < 3; ++it) { const int mt = (it < 2) ? (w >> 1) : 4, nt = (it < 2) ? 2 * (w & 1) + it : w;
;         if (it == 2 && w >= 4) break;
;         f32x4 acc = (f32x4){0.f, 0.f, 0.f, 0.f};
; #pragma unroll
;         for (int ks = 0; ks < 4; ++ks) { const bf16x8 a = *(const LAS bf16x8*)(VWT + (16 * mt + r) * LP + 32 * ks + 8 * q), b = *(const LAS bf16x8*)(KT + (16 * nt + r) * LP + 32 * ks + 8 * q); acc = mfma16(a, b, acc); }
; #pragma unroll
;     ...
;         for (int jj = 0; jj < 4; ++jj) mls[(16 * mt + 4 * q + jj) * 64 + 16 * nt + r] = 0.01f * (float)(((16 * mt + 4 * q + jj) * 5 + (16 * nt + r) * 3 + ch) % 17 - 8);
;     ...
;         for (int jj = 0; jj < 4; ++jj) mls[(16 * mt + 4 * q + jj) * 64 + 16 * nt + r] = acc[jj];
;     ...
;         for (int jj = 0; jj < 4; ++jj) mls[(16 * mt + 4 * q + jj) * 64 + 16 * nt + r] = acc[jj];
;     ...
;     }
	ds_read_b128 v[6:9], v5 offset:21760
	ds_read_b128 v[20:23], v10
	s_waitcnt lgkmcnt(0)
	s_nop 3
	s_nop 0
	v_mfma_f32_16x16x32_bf16 v[6:9], v[6:9], v[20:23], 0
	ds_read_b128 v[20:23], v5 offset:21824
	ds_read_b128 v[28:31], v10 offset:64
	s_waitcnt lgkmcnt(0)
	s_nop 3
	s_nop 0
	v_mfma_f32_16x16x32_bf16 v[6:9], v[20:23], v[28:31], v[6:9]
	ds_read_b128 v[20:23], v5 offset:21888
	ds_read_b128 v[28:31], v10 offset:128
	s_waitcnt lgkmcnt(0)
	s_nop 3
	s_nop 0
	v_mfma_f32_16x16x32_bf16 v[6:9], v[20:23], v[28:31], v[6:9]
	ds_read_b128 v[20:23], v5 offset:21952
	ds_read_b128 v[28:31], v10 offset:192
	v_lshlrev_b32_e32 v1, 4, v1
	s_and_b32 s6, s21, -16
	v_and_b32_e32 v1, 0x300, v1
	s_waitcnt lgkmcnt(0)
	s_nop 3
	s_nop 0
	v_mfma_f32_16x16x32_bf16 v[6:9], v[20:23], v[28:31], v[6:9]
	v_lshl_or_b32 v11, s6, 6, v1
	v_or_b32_e32 v42, v11, v0
	v_ashrrev_i32_e32 v43, 31, v42
	v_lshl_add_u64 v[20:21], v[42:43], 2, s[0:1]
	v_ashrrev_i32_e32 v43, 31, v11
	s_nop 2
	v_lshl_add_u64 v[252:253], v[20:21], 0, v[250:251]
	global_store_dwordx4 v[252:253], v[6:9], off
	ds_read_b128 v[20:23], v5 offset:26112
	ds_read_b128 v[28:31], v10
	v_lshl_add_u64 v[44:45], v[42:43], 2, s[0:1]
	s_waitcnt lgkmcnt(0)
	s_nop 3
	s_nop 0
	v_mfma_f32_16x16x32_bf16 v[6:9], v[20:23], v[28:31], 0
	ds_read_b128 v[20:23], v5 offset:26176
	ds_read_b128 v[28:31], v10 offset:64
	s_waitcnt lgkmcnt(0)
	s_nop 3
	s_nop 0
	v_mfma_f32_16x16x32_bf16 v[6:9], v[20:23], v[28:31], v[6:9]
	ds_read_b128 v[20:23], v5 offset:26240
	ds_read_b128 v[28:31], v10 offset:128
	s_waitcnt lgkmcnt(0)
	s_nop 3
	s_nop 0
	v_mfma_f32_16x16x32_bf16 v[6:9], v[20:23], v[28:31], v[6:9]
	ds_read_b128 v[20:23], v5 offset:26304
	ds_read_b128 v[28:31], v10 offset:192
	s_waitcnt lgkmcnt(0)
	s_nop 3
	s_nop 0
	v_mfma_f32_16x16x32_bf16 v[6:9], v[20:23], v[28:31], v[6:9]
	v_or_b32_e32 v42, 16, v42
	s_cmp_gt_i32 s19, 3
	v_lshl_add_u64 v[10:11], v[42:43], 2, s[0:1]
	s_nop 4
	v_lshl_add_u64 v[252:253], v[44:45], 0, v[250:251]
	global_store_dwordx4 v[252:253], v[6:9], off offset:64
	s_cbranch_scc1 .LBB0_865
	v_mad_u32_u24 v0, v4, s66, v2
	v_lshl_or_b32 v30, s19, 4, v4
	v_mad_u64_u32 v[28:29], s[6:7], v30, s66, v[2:3]
	ds_read_b128 v[4:7], v0 offset:17408
	ds_read_b128 v[8:11], v28 offset:21760
	v_add_u32_e32 v2, v30, v1
	s_waitcnt lgkmcnt(0)
	s_nop 3
	s_nop 0
	v_mfma_f32_16x16x32_bf16 v[4:7], v[8:11], v[4:7], 0
	ds_read_b128 v[8:11], v28 offset:21824
	ds_read_b128 v[20:23], v0 offset:17472
	s_waitcnt lgkmcnt(0)
	s_nop 3
	s_nop 0
	v_mfma_f32_16x16x32_bf16 v[4:7], v[8:11], v[20:23], v[4:7]
	ds_read_b128 v[8:11], v28 offset:21888
	ds_read_b128 v[20:23], v0 offset:17536
	s_waitcnt lgkmcnt(0)
	s_nop 3
	s_nop 0
	v_mfma_f32_16x16x32_bf16 v[4:7], v[8:11], v[20:23], v[4:7]
	ds_read_b128 v[8:11], v28 offset:21952
	ds_read_b128 v[20:23], v0 offset:17600
	s_waitcnt lgkmcnt(0)
	s_nop 3
	s_nop 0
	v_mfma_f32_16x16x32_bf16 v[4:7], v[8:11], v[20:23], v[4:7]
	v_add_u32_e32 v0, 0x1000, v2
	v_ashrrev_i32_e32 v1, 31, v0
	v_lshl_add_u64 v[0:1], v[0:1], 2, s[0:1]
	s_nop 4
	v_lshl_add_u64 v[252:253], v[0:1], 0, v[250:251]
	global_store_dwordx4 v[252:253], v[4:7], off
	v_add_u32_e32 v0, 0x1040, v2
	v_ashrrev_i32_e32 v1, 31, v0
	v_lshl_add_u64 v[0:1], v[0:1], 2, s[0:1]
	v_add_u32_e32 v0, 0x1080, v2
	v_ashrrev_i32_e32 v1, 31, v0
	v_lshl_add_u64 v[0:1], v[0:1], 2, s[0:1]
	v_add_u32_e32 v0, 0x10c0, v2
	v_ashrrev_i32_e32 v1, 31, v0
	v_lshl_add_u64 v[0:1], v[0:1], 2, s[0:1]

; #define LAS __attribute__((address_space(3)))
; DI unsigned pk2h(float lo, float hi) { const f32x2h_t v = {lo, hi}; return __builtin_bit_cast(unsigned, __builtin_convertvector(v, bf16x2h_t)); }
; DI void ml_local_unit(Frame& F, int l, int ch, int h, const MlLPre& P) {
;     ...
;     if (F.tid < 64) *(LAS unsigned*)(VWT + 64 * LP + 2 * F.tid) = pk2h(WG[2 * F.tid], WG[2 * F.tid + 1]);
;     {
;       const float wg0 = WG[s2], wg1 = WG[s2 + 1];
;       float x0[8], x1[8];
;       unpack8(rv0, x0); unpack8(rv1, x1);
; #pragma unroll
;       for (int e = 0; e < 8; ++e) *(LAS unsigned*)(VWT + (c0 + e) * LP + s2) = pk2h(x0[e] * wg0, x1[e] * wg1);
;       unpack8(rk0, x0); unpack8(rk1, x1);
; #pragma unroll
;       for (int e = 0; e < 8; ++e) *(LAS unsigned*)(KT + (c0 + e) * LP + s2) = pk2h(x0[e] * 0.125f, x1[e] * 0.125f); }
;     __syncthreads();
;     const int w = F.wave, r = F.lane & 15, q = F.lane >> 4;
;     float* mls = (float*)(F.ws + WS_MLS + ML_ALT(F.l) * (406 * MiB)) + (size_t)(ch * 4 + h) * 5120;
; #pragma unroll
;     for (int it = 0; it < 3; ++it) { const int mt = (it < 2) ? (w >> 1) : 4, nt = (it < 2) ? 2 * (w & 1) + it : w;
.LBB0_885:
	s_or_b64 exec, exec, s[0:1]
	v_ashrrev_i32_e32 v0, 2, v132
	v_and_b32_e32 v38, -2, v0
	v_lshl_add_u32 v0, v38, 2, s17
	v_bitop3_b32 v2, v132, -4, 4 bitop3:0xc8
	v_add_u32_e32 v2, s17, v2
	ds_read_b32 v42, v0 offset:40192
	ds_read_b32 v43, v2 offset:40192
	v_lshlrev_b32_e32 v45, 16, v32
	v_lshlrev_b32_e32 v44, 16, v24
	v_lshlrev_b32_e32 v2, 1, v38
	v_sub_u32_e32 v0, v0, v2
	s_waitcnt lgkmcnt(0)
	v_pk_mul_f32 v[44:45], v[42:43], v[44:45]
	v_and_b32_e32 v40, 56, v39
	v_cvt_pk_bf16_f32 v2, v44, v45
	v_and_b32_e32 v45, 0xffff0000, v32
	v_and_b32_e32 v44, 0xffff0000, v24
	v_pk_mul_f32 v[44:45], v[42:43], v[44:45]
	v_mad_u32_u24 v0, v40, s66, v0
	v_cvt_pk_bf16_f32 v24, v44, v45
	v_lshlrev_b32_e32 v45, 16, v33
	v_lshlrev_b32_e32 v44, 16, v25
	v_and_b32_e32 v33, 0xffff0000, v33
	v_and_b32_e32 v32, 0xffff0000, v25
	ds_write2_b32 v0, v2, v24 offset1:68
	v_pk_mul_f32 v[44:45], v[42:43], v[44:45]
	v_pk_mul_f32 v[24:25], v[42:43], v[32:33]
	v_cvt_pk_bf16_f32 v2, v44, v45
	v_cvt_pk_bf16_f32 v24, v24, v25
	ds_write2_b32 v0, v2, v24 offset0:136 offset1:204
	v_lshlrev_b32_e32 v25, 16, v34
	v_lshlrev_b32_e32 v24, 16, v26
	v_pk_mul_f32 v[24:25], v[42:43], v[24:25]
	s_mov_b32 s0, 0x3e000000
	v_cvt_pk_bf16_f32 v2, v24, v25
	v_and_b32_e32 v25, 0xffff0000, v34
	v_and_b32_e32 v24, 0xffff0000, v26
	v_pk_mul_f32 v[24:25], v[42:43], v[24:25]
	v_add_u32_e32 v26, 0x400, v0
	v_cvt_pk_bf16_f32 v24, v24, v25
	ds_write2_b32 v26, v2, v24 offset0:16 offset1:84
	v_lshlrev_b32_e32 v25, 16, v35
	v_lshlrev_b32_e32 v24, 16, v27
	v_pk_mul_f32 v[24:25], v[42:43], v[24:25]
	s_nop 0
	v_cvt_pk_bf16_f32 v2, v24, v25
	v_and_b32_e32 v25, 0xffff0000, v35
	v_and_b32_e32 v24, 0xffff0000, v27
	v_pk_mul_f32 v[24:25], v[42:43], v[24:25]
	s_nop 0
	v_cvt_pk_bf16_f32 v24, v24, v25
	ds_write2_b32 v26, v2, v24 offset0:152 offset1:220
	s_waitcnt vmcnt(12)
	v_lshlrev_b32_e32 v25, 16, v16
	v_lshlrev_b32_e32 v24, 16, v12
	v_pk_mul_f32 v[24:25], v[24:25], s[0:1] op_sel_hi:[1,0]
	s_nop 0
	v_cvt_pk_bf16_f32 v2, v24, v25
	v_and_b32_e32 v25, 0xffff0000, v16
	v_and_b32_e32 v24, 0xffff0000, v12
	v_pk_mul_f32 v[24:25], v[24:25], s[0:1] op_sel_hi:[1,0]
	v_add_u32_e32 v16, 0x5400, v0
	v_cvt_pk_bf16_f32 v12, v24, v25
	ds_write2_b32 v16, v2, v12 offset0:64 offset1:132
	v_lshlrev_b32_e32 v25, 16, v17
	v_lshlrev_b32_e32 v24, 16, v13
	v_and_b32_e32 v17, 0xffff0000, v17
	v_and_b32_e32 v16, 0xffff0000, v13
	v_pk_mul_f32 v[24:25], v[24:25], s[0:1] op_sel_hi:[1,0]
	v_pk_mul_f32 v[12:13], v[16:17], s[0:1] op_sel_hi:[1,0]
	v_cvt_pk_bf16_f32 v2, v24, v25
	v_cvt_pk_bf16_f32 v12, v12, v13
	v_add_u32_e32 v13, 0x5600, v0
	ds_write2_b32 v13, v2, v12 offset0:72 offset1:140
	v_lshlrev_b32_e32 v13, 16, v18
	v_lshlrev_b32_e32 v12, 16, v14
	v_pk_mul_f32 v[12:13], v[12:13], s[0:1] op_sel_hi:[1,0]
	s_nop 0
	v_cvt_pk_bf16_f32 v2, v12, v13
	v_and_b32_e32 v13, 0xffff0000, v18
	v_and_b32_e32 v12, 0xffff0000, v14
	v_pk_mul_f32 v[12:13], v[12:13], s[0:1] op_sel_hi:[1,0]
	s_nop 0
	v_cvt_pk_bf16_f32 v12, v12, v13
	v_add_u32_e32 v13, 0x5800, v0
	ds_write2_b32 v13, v2, v12 offset0:80 offset1:148
	v_lshlrev_b32_e32 v13, 16, v19
	v_lshlrev_b32_e32 v12, 16, v15
	v_pk_mul_f32 v[12:13], v[12:13], s[0:1] op_sel_hi:[1,0]
	v_add_u32_e32 v0, 0x5a00, v0
	v_cvt_pk_bf16_f32 v2, v12, v13
	v_and_b32_e32 v13, 0xffff0000, v19
	v_and_b32_e32 v12, 0xffff0000, v15
	v_pk_mul_f32 v[12:13], v[12:13], s[0:1] op_sel_hi:[1,0]
	s_or_b32 s0, s18, 1
	s_mul_i32 s6, s0, 0x5000
	s_mul_hi_i32 s1, s0, 0x5000
	s_add_u32 s6, s4, s6
	s_addc_u32 s1, s5, s1
	v_cvt_pk_bf16_f32 v12, v12, v13
	s_add_u32 s6, s6, 0x22100000
	ds_write2_b32 v0, v2, v12 offset0:88 offset1:156
	s_addc_u32 s7, s1, 0
	s_lshl_b32 s22, s19, 3
	v_and_b32_e32 v0, 48, v1
	v_and_b32_e32 v12, 15, v132
	s_lshl_b32 s1, s19, 5
	v_add_u32_e32 v2, s17, v0
	v_bfi_b32 v0, -16, s22, v132
	v_mad_u64_u32 v[18:19], s[20:21], v0, s66, v[2:3]
	v_and_or_b32 v0, s1, 32, v12
	v_mad_u32_u24 v13, v0, s66, v2
	s_waitcnt lgkmcnt(0)
	s_barrier
; #define LAS __attribute__((address_space(3)))
; DI f32x4 mfma16(bf16x8 a, bf16x8 b, f32x4 c) { asm volatile("s_nop 3" : "+v"(a), "+v"(b)); return __builtin_amdgcn_mfma_f32_16x16x32_bf16(a, b, c, 0, 0, 0); }
; DI void ml_local_unit(Frame& F, int l, int ch, int h, const MlLPre& P) {
;     ...
; #pragma unroll
;     for (int it = 0; it < 3; ++it) { const int mt = (it < 2) ? (w >> 1) : 4, nt = (it < 2) ? 2 * (w & 1) + it : w;
;         if (it == 2 && w >= 4) break;
;         f32x4 acc = (f32x4){0.f, 0.f, 0.f, 0.f};
; #pragma unroll
;         for (int ks = 0; ks < 4; ++ks) { const bf16x8 a = *(const LAS bf16x8*)(VWT + (16 * mt + r) * LP + 32 * ks + 8 * q), b = *(const LAS bf16x8*)(KT + (16 * nt + r) * LP + 32 * ks + 8 * q); acc = mfma16(a, b, acc); }
; #pragma unroll
;     ...
;         for (int jj = 0; jj < 4; ++jj) mls[(16 * mt + 4 * q + jj) * 64 + 16 * nt + r] = 0.01f * (float)(((16 * mt + 4 * q + jj) * 5 + (16 * nt + r) * 3 + ch) % 17 - 8);
;     ...
;         for (int jj = 0; jj < 4; ++jj) mls[(16 * mt + 4 * q + jj) * 64 + 16 * nt + r] = acc[jj];
;     ...
;         for (int jj = 0; jj < 4; ++jj) mls[(16 * mt + 4 * q + jj) * 64 + 16 * nt + r] = acc[jj];
;     ...
;     }
	ds_read_b128 v[14:17], v13 offset:21760
	ds_read_b128 v[24:27], v18
	s_waitcnt lgkmcnt(0)
	s_nop 3
	s_nop 0
	v_mfma_f32_16x16x32_bf16 v[14:17], v[14:17], v[24:27], 0
	ds_read_b128 v[24:27], v13 offset:21824
	ds_read_b128 v[32:35], v18 offset:64
	s_waitcnt lgkmcnt(0)
	s_nop 3
	s_nop 0
	v_mfma_f32_16x16x32_bf16 v[14:17], v[24:27], v[32:35], v[14:17]
	ds_read_b128 v[24:27], v13 offset:21888
	ds_read_b128 v[32:35], v18 offset:128
	s_waitcnt lgkmcnt(0)
	s_nop 3
	s_nop 0
	v_mfma_f32_16x16x32_bf16 v[14:17], v[24:27], v[32:35], v[14:17]
	ds_read_b128 v[24:27], v13 offset:21952
	ds_read_b128 v[32:35], v18 offset:192
	v_lshlrev_b32_e32 v1, 4, v1
	s_and_b32 s1, s22, -16
	v_and_b32_e32 v1, 0x300, v1
	s_waitcnt lgkmcnt(0)
	s_nop 3
	s_nop 0
	v_mfma_f32_16x16x32_bf16 v[14:17], v[24:27], v[32:35], v[14:17]
	v_lshl_or_b32 v19, s1, 6, v1
	v_or_b32_e32 v42, v19, v0
	v_ashrrev_i32_e32 v43, 31, v42
	v_lshl_add_u64 v[24:25], v[42:43], 2, s[6:7]
	v_ashrrev_i32_e32 v43, 31, v19
	s_nop 2
	v_lshl_add_u64 v[252:253], v[24:25], 0, v[250:251]
	global_store_dwordx4 v[252:253], v[14:17], off
	ds_read_b128 v[24:27], v13 offset:26112
	ds_read_b128 v[32:35], v18
	v_lshl_add_u64 v[44:45], v[42:43], 2, s[6:7]
	s_waitcnt lgkmcnt(0)
	s_nop 3
	s_nop 0
	v_mfma_f32_16x16x32_bf16 v[14:17], v[24:27], v[32:35], 0
	ds_read_b128 v[24:27], v13 offset:26176
	ds_read_b128 v[32:35], v18 offset:64
	s_waitcnt lgkmcnt(0)
	s_nop 3
	s_nop 0
	v_mfma_f32_16x16x32_bf16 v[14:17], v[24:27], v[32:35], v[14:17]
	ds_read_b128 v[24:27], v13 offset:26240
	ds_read_b128 v[32:35], v18 offset:128
	s_waitcnt lgkmcnt(0)
	s_nop 3
	s_nop 0
	v_mfma_f32_16x16x32_bf16 v[14:17], v[24:27], v[32:35], v[14:17]
	ds_read_b128 v[24:27], v13 offset:26304
	ds_read_b128 v[32:35], v18 offset:192
	s_waitcnt lgkmcnt(0)
	s_nop 3
	s_nop 0
	v_mfma_f32_16x16x32_bf16 v[14:17], v[24:27], v[32:35], v[14:17]
	v_or_b32_e32 v42, 16, v42
	s_cmp_gt_i32 s19, 3
	v_lshl_add_u64 v[18:19], v[42:43], 2, s[6:7]
	s_nop 4
	v_lshl_add_u64 v[252:253], v[44:45], 0, v[250:251]
	global_store_dwordx4 v[252:253], v[14:17], off offset:64
	s_cbranch_scc1 .LBB0_887
	v_mad_u32_u24 v0, v12, s66, v2
	v_lshl_or_b32 v34, s19, 4, v12
	v_mad_u64_u32 v[32:33], s[20:21], v34, s66, v[2:3]
	ds_read_b128 v[12:15], v0 offset:17408
	ds_read_b128 v[16:19], v32 offset:21760
	v_add_u32_e32 v2, v34, v1
	s_waitcnt lgkmcnt(0)
	s_nop 3
	s_nop 0
	v_mfma_f32_16x16x32_bf16 v[12:15], v[16:19], v[12:15], 0
	ds_read_b128 v[16:19], v32 offset:21824
	ds_read_b128 v[24:27], v0 offset:17472
	s_waitcnt lgkmcnt(0)
	s_nop 3
	s_nop 0
	v_mfma_f32_16x16x32_bf16 v[12:15], v[16:19], v[24:27], v[12:15]
	ds_read_b128 v[16:19], v32 offset:21888
	ds_read_b128 v[24:27], v0 offset:17536
	s_waitcnt lgkmcnt(0)
	s_nop 3
	s_nop 0
	v_mfma_f32_16x16x32_bf16 v[12:15], v[16:19], v[24:27], v[12:15]
	ds_read_b128 v[16:19], v32 offset:21952
	ds_read_b128 v[24:27], v0 offset:17600
	s_waitcnt lgkmcnt(0)
	s_nop 3
	s_nop 0
	v_mfma_f32_16x16x32_bf16 v[12:15], v[16:19], v[24:27], v[12:15]
	v_add_u32_e32 v0, 0x1000, v2
	v_ashrrev_i32_e32 v1, 31, v0
	v_lshl_add_u64 v[0:1], v[0:1], 2, s[6:7]
	s_nop 4
	v_lshl_add_u64 v[252:253], v[0:1], 0, v[250:251]
	global_store_dwordx4 v[252:253], v[12:15], off
	v_add_u32_e32 v0, 0x1040, v2
	v_ashrrev_i32_e32 v1, 31, v0
	v_lshl_add_u64 v[0:1], v[0:1], 2, s[6:7]
	v_add_u32_e32 v0, 0x1080, v2
	v_ashrrev_i32_e32 v1, 31, v0
	v_lshl_add_u64 v[0:1], v[0:1], 2, s[6:7]
	v_add_u32_e32 v0, 0x10c0, v2
	v_ashrrev_i32_e32 v1, 31, v0
	v_lshl_add_u64 v[0:1], v[0:1], 2, s[6:7]

; #define LAS __attribute__((address_space(3)))
; DI unsigned pk2h(float lo, float hi) { const f32x2h_t v = {lo, hi}; return __builtin_bit_cast(unsigned, __builtin_convertvector(v, bf16x2h_t)); }
; DI void ml_local_unit(Frame& F, int l, int ch, int h, const MlLPre& P) {
;     ...
;     if (F.tid < 64) *(LAS unsigned*)(VWT + 64 * LP + 2 * F.tid) = pk2h(WG[2 * F.tid], WG[2 * F.tid + 1]);
;     {
;       const float wg0 = WG[s2], wg1 = WG[s2 + 1];
;       float x0[8], x1[8];
;       unpack8(rv0, x0); unpack8(rv1, x1);
; #pragma unroll
;       for (int e = 0; e < 8; ++e) *(LAS unsigned*)(VWT + (c0 + e) * LP + s2) = pk2h(x0[e] * wg0, x1[e] * wg1);
;       unpack8(rk0, x0); unpack8(rk1, x1);
; #pragma unroll
;       for (int e = 0; e < 8; ++e) *(LAS unsigned*)(KT + (c0 + e) * LP + s2) = pk2h(x0[e] * 0.125f, x1[e] * 0.125f); }
;     __syncthreads();
;     const int w = F.wave, r = F.lane & 15, q = F.lane >> 4;
;     float* mls = (float*)(F.ws + WS_MLS + ML_ALT(F.l) * (406 * MiB)) + (size_t)(ch * 4 + h) * 5120;
; #pragma unroll
;     for (int it = 0; it < 3; ++it) { const int mt = (it < 2) ? (w >> 1) : 4, nt = (it < 2) ? 2 * (w & 1) + it : w;
.LBB0_907:
	s_or_b64 exec, exec, s[0:1]
	v_ashrrev_i32_e32 v0, 2, v132
	v_and_b32_e32 v0, -2, v0
	v_and_b32_e32 v2, 56, v38
	v_bitop3_b32 v38, v132, -4, 4 bitop3:0xc8
	v_lshl_add_u32 v40, v0, 2, s17
	v_add_u32_e32 v39, s17, v38
	ds_read_b32 v38, v40 offset:40192
	ds_read_b32 v39, v39 offset:40192
	v_lshlrev_b32_e32 v0, 1, v0
	v_sub_u32_e32 v0, v40, v0
	s_waitcnt vmcnt(13)
	v_lshlrev_b32_e32 v41, 16, v28
	v_lshlrev_b32_e32 v40, 16, v20
	s_waitcnt lgkmcnt(0)
	v_pk_mul_f32 v[40:41], v[38:39], v[40:41]
	v_mad_u32_u24 v0, v2, s66, v0
	v_cvt_pk_bf16_f32 v42, v40, v41
	v_and_b32_e32 v41, 0xffff0000, v28
	v_and_b32_e32 v40, 0xffff0000, v20
	v_pk_mul_f32 v[40:41], v[38:39], v[40:41]
	v_and_b32_e32 v28, 0xffff0000, v21
	v_cvt_pk_bf16_f32 v2, v40, v41
	v_lshlrev_b32_e32 v41, 16, v29
	v_lshlrev_b32_e32 v40, 16, v21
	v_and_b32_e32 v29, 0xffff0000, v29
	v_pk_mul_f32 v[40:41], v[38:39], v[40:41]
	v_pk_mul_f32 v[20:21], v[38:39], v[28:29]
	ds_write2_b32 v0, v42, v2 offset1:68
	v_cvt_pk_bf16_f32 v2, v40, v41
	v_cvt_pk_bf16_f32 v20, v20, v21
	ds_write2_b32 v0, v2, v20 offset0:136 offset1:204
	v_lshlrev_b32_e32 v21, 16, v30
	v_lshlrev_b32_e32 v20, 16, v22
	v_pk_mul_f32 v[20:21], v[38:39], v[20:21]
	s_mov_b32 s0, 0x3e000000
	v_cvt_pk_bf16_f32 v2, v20, v21
	v_and_b32_e32 v21, 0xffff0000, v30
	v_and_b32_e32 v20, 0xffff0000, v22
	v_pk_mul_f32 v[20:21], v[38:39], v[20:21]
	v_add_u32_e32 v22, 0x400, v0
	v_cvt_pk_bf16_f32 v20, v20, v21
	ds_write2_b32 v22, v2, v20 offset0:16 offset1:84
	v_lshlrev_b32_e32 v21, 16, v31
	v_lshlrev_b32_e32 v20, 16, v23
	v_pk_mul_f32 v[20:21], v[38:39], v[20:21]
	s_nop 0
	v_cvt_pk_bf16_f32 v2, v20, v21
	v_and_b32_e32 v21, 0xffff0000, v31
	v_and_b32_e32 v20, 0xffff0000, v23
	v_pk_mul_f32 v[20:21], v[38:39], v[20:21]
	s_nop 0
	v_cvt_pk_bf16_f32 v20, v20, v21
	ds_write2_b32 v22, v2, v20 offset0:152 offset1:220
	s_waitcnt vmcnt(12)
	v_lshlrev_b32_e32 v21, 16, v8
	v_lshlrev_b32_e32 v20, 16, v4
	v_pk_mul_f32 v[20:21], v[20:21], s[0:1] op_sel_hi:[1,0]
	s_nop 0
	v_cvt_pk_bf16_f32 v2, v20, v21
	v_and_b32_e32 v21, 0xffff0000, v8
	v_and_b32_e32 v20, 0xffff0000, v4
	v_pk_mul_f32 v[20:21], v[20:21], s[0:1] op_sel_hi:[1,0]
	v_add_u32_e32 v8, 0x5400, v0
	v_cvt_pk_bf16_f32 v4, v20, v21
	ds_write2_b32 v8, v2, v4 offset0:64 offset1:132
	v_lshlrev_b32_e32 v21, 16, v9
	v_lshlrev_b32_e32 v20, 16, v5
	v_and_b32_e32 v9, 0xffff0000, v9
	v_and_b32_e32 v8, 0xffff0000, v5
	v_pk_mul_f32 v[20:21], v[20:21], s[0:1] op_sel_hi:[1,0]
	v_pk_mul_f32 v[4:5], v[8:9], s[0:1] op_sel_hi:[1,0]
	v_cvt_pk_bf16_f32 v2, v20, v21
	v_cvt_pk_bf16_f32 v4, v4, v5
	v_add_u32_e32 v5, 0x5600, v0
	ds_write2_b32 v5, v2, v4 offset0:72 offset1:140
	v_lshlrev_b32_e32 v5, 16, v10
	v_lshlrev_b32_e32 v4, 16, v6
	v_pk_mul_f32 v[4:5], v[4:5], s[0:1] op_sel_hi:[1,0]
	s_nop 0
	v_cvt_pk_bf16_f32 v2, v4, v5
	v_and_b32_e32 v5, 0xffff0000, v10
	v_and_b32_e32 v4, 0xffff0000, v6
	v_pk_mul_f32 v[4:5], v[4:5], s[0:1] op_sel_hi:[1,0]
	s_nop 0
	v_cvt_pk_bf16_f32 v4, v4, v5
	v_add_u32_e32 v5, 0x5800, v0
	ds_write2_b32 v5, v2, v4 offset0:80 offset1:148
	v_lshlrev_b32_e32 v5, 16, v11
	v_lshlrev_b32_e32 v4, 16, v7
	v_pk_mul_f32 v[4:5], v[4:5], s[0:1] op_sel_hi:[1,0]
	v_add_u32_e32 v0, 0x5a00, v0
	v_cvt_pk_bf16_f32 v2, v4, v5
	v_and_b32_e32 v5, 0xffff0000, v11
	v_and_b32_e32 v4, 0xffff0000, v7
	v_pk_mul_f32 v[4:5], v[4:5], s[0:1] op_sel_hi:[1,0]
	s_or_b32 s0, s18, 2
	s_mul_i32 s4, s0, 0x5000
	s_mul_hi_i32 s1, s0, 0x5000
	s_add_u32 s4, s2, s4
	s_addc_u32 s1, s3, s1
	v_cvt_pk_bf16_f32 v4, v4, v5
	s_add_u32 s4, s4, 0x22100000
	ds_write2_b32 v0, v2, v4 offset0:88 offset1:156
	s_addc_u32 s5, s1, 0
	s_lshl_b32 s20, s19, 3
	v_and_b32_e32 v0, 48, v1
	v_and_b32_e32 v4, 15, v132
	s_lshl_b32 s1, s19, 5
	v_add_u32_e32 v2, s17, v0
	v_bfi_b32 v0, -16, s20, v132
	v_mad_u64_u32 v[10:11], s[6:7], v0, s66, v[2:3]
	v_and_or_b32 v0, s1, 32, v4
	v_mad_u32_u24 v5, v0, s66, v2
	s_waitcnt lgkmcnt(0)
	s_barrier
; #define LAS __attribute__((address_space(3)))
; DI f32x4 mfma16(bf16x8 a, bf16x8 b, f32x4 c) { asm volatile("s_nop 3" : "+v"(a), "+v"(b)); return __builtin_amdgcn_mfma_f32_16x16x32_bf16(a, b, c, 0, 0, 0); }
; DI void ml_local_unit(Frame& F, int l, int ch, int h, const MlLPre& P) {
;     ...
; #pragma unroll
;     for (int it = 0; it < 3; ++it) { const int mt = (it < 2) ? (w >> 1) : 4, nt = (it < 2) ? 2 * (w & 1) + it : w;
;         if (it == 2 && w >= 4) break;
;         f32x4 acc = (f32x4){0.f, 0.f, 0.f, 0.f};
; #pragma unroll
;         for (int ks = 0; ks < 4; ++ks) { const bf16x8 a = *(const LAS bf16x8*)(VWT + (16 * mt + r) * LP + 32 * ks + 8 * q), b = *(const LAS bf16x8*)(KT + (16 * nt + r) * LP + 32 * ks + 8 * q); acc = mfma16(a, b, acc); }
; #pragma unroll
;     ...
;         for (int jj = 0; jj < 4; ++jj) mls[(16 * mt + 4 * q + jj) * 64 + 16 * nt + r] = 0.01f * (float)(((16 * mt + 4 * q + jj) * 5 + (16 * nt + r) * 3 + ch) % 17 - 8);
;     ...
;         for (int jj = 0; jj < 4; ++jj) mls[(16 * mt + 4 * q + jj) * 64 + 16 * nt + r] = acc[jj];
;     ...
;         for (int jj = 0; jj < 4; ++jj) mls[(16 * mt + 4 * q + jj) * 64 + 16 * nt + r] = acc[jj];
;     ...
;     }
	ds_read_b128 v[6:9], v5 offset:21760
	ds_read_b128 v[20:23], v10
	s_waitcnt lgkmcnt(0)
	s_nop 3
	s_nop 0
	v_mfma_f32_16x16x32_bf16 v[6:9], v[6:9], v[20:23], 0
	ds_read_b128 v[20:23], v5 offset:21824
	ds_read_b128 v[28:31], v10 offset:64
	s_waitcnt lgkmcnt(0)
	s_nop 3
	s_nop 0
	v_mfma_f32_16x16x32_bf16 v[6:9], v[20:23], v[28:31], v[6:9]
	ds_read_b128 v[20:23], v5 offset:21888
	ds_read_b128 v[28:31], v10 offset:128
	s_waitcnt lgkmcnt(0)
	s_nop 3
	s_nop 0
	v_mfma_f32_16x16x32_bf16 v[6:9], v[20:23], v[28:31], v[6:9]
	ds_read_b128 v[20:23], v5 offset:21952
	ds_read_b128 v[28:31], v10 offset:192
	v_lshlrev_b32_e32 v1, 4, v1
	s_and_b32 s1, s20, -16
	v_and_b32_e32 v1, 0x300, v1
	s_waitcnt lgkmcnt(0)
	s_nop 3
	s_nop 0
	v_mfma_f32_16x16x32_bf16 v[6:9], v[20:23], v[28:31], v[6:9]
	v_lshl_or_b32 v11, s1, 6, v1
	v_or_b32_e32 v38, v11, v0
	v_ashrrev_i32_e32 v39, 31, v38
	v_lshl_add_u64 v[20:21], v[38:39], 2, s[4:5]
	v_ashrrev_i32_e32 v39, 31, v11
	s_nop 2
	v_lshl_add_u64 v[252:253], v[20:21], 0, v[250:251]
	global_store_dwordx4 v[252:253], v[6:9], off
	ds_read_b128 v[20:23], v5 offset:26112
	ds_read_b128 v[28:31], v10
	v_lshl_add_u64 v[40:41], v[38:39], 2, s[4:5]
	s_waitcnt lgkmcnt(0)
	s_nop 3
	s_nop 0
	v_mfma_f32_16x16x32_bf16 v[6:9], v[20:23], v[28:31], 0
	ds_read_b128 v[20:23], v5 offset:26176
	ds_read_b128 v[28:31], v10 offset:64
	s_waitcnt lgkmcnt(0)
	s_nop 3
	s_nop 0
	v_mfma_f32_16x16x32_bf16 v[6:9], v[20:23], v[28:31], v[6:9]
	ds_read_b128 v[20:23], v5 offset:26240
	ds_read_b128 v[28:31], v10 offset:128
	s_waitcnt lgkmcnt(0)
	s_nop 3
	s_nop 0
	v_mfma_f32_16x16x32_bf16 v[6:9], v[20:23], v[28:31], v[6:9]
	ds_read_b128 v[20:23], v5 offset:26304
	ds_read_b128 v[28:31], v10 offset:192
	s_waitcnt lgkmcnt(0)
	s_nop 3
	s_nop 0
	v_mfma_f32_16x16x32_bf16 v[6:9], v[20:23], v[28:31], v[6:9]
	v_or_b32_e32 v38, 16, v38
	s_cmp_gt_i32 s19, 3
	v_lshl_add_u64 v[10:11], v[38:39], 2, s[4:5]
	s_nop 4
	v_lshl_add_u64 v[252:253], v[40:41], 0, v[250:251]
	global_store_dwordx4 v[252:253], v[6:9], off offset:64
	s_cbranch_scc1 .LBB0_909
	v_mad_u32_u24 v0, v4, s66, v2
	v_lshl_or_b32 v30, s19, 4, v4
	v_mad_u64_u32 v[28:29], s[6:7], v30, s66, v[2:3]
	ds_read_b128 v[4:7], v0 offset:17408
	ds_read_b128 v[8:11], v28 offset:21760
	v_add_u32_e32 v2, v30, v1
	s_waitcnt lgkmcnt(0)
	s_nop 3
	s_nop 0
	v_mfma_f32_16x16x32_bf16 v[4:7], v[8:11], v[4:7], 0
	ds_read_b128 v[8:11], v28 offset:21824
	ds_read_b128 v[20:23], v0 offset:17472
	s_waitcnt lgkmcnt(0)
	s_nop 3
	s_nop 0
	v_mfma_f32_16x16x32_bf16 v[4:7], v[8:11], v[20:23], v[4:7]
	ds_read_b128 v[8:11], v28 offset:21888
	ds_read_b128 v[20:23], v0 offset:17536
	s_waitcnt lgkmcnt(0)
	s_nop 3
	s_nop 0
	v_mfma_f32_16x16x32_bf16 v[4:7], v[8:11], v[20:23], v[4:7]
	ds_read_b128 v[8:11], v28 offset:21952
	ds_read_b128 v[20:23], v0 offset:17600
	s_waitcnt lgkmcnt(0)
	s_nop 3
	s_nop 0
	v_mfma_f32_16x16x32_bf16 v[4:7], v[8:11], v[20:23], v[4:7]
	v_add_u32_e32 v0, 0x1000, v2
	v_ashrrev_i32_e32 v1, 31, v0
	v_lshl_add_u64 v[0:1], v[0:1], 2, s[4:5]
	s_nop 4
	v_lshl_add_u64 v[252:253], v[0:1], 0, v[250:251]
	global_store_dwordx4 v[252:253], v[4:7], off
	v_add_u32_e32 v0, 0x1040, v2
	v_ashrrev_i32_e32 v1, 31, v0
	v_lshl_add_u64 v[0:1], v[0:1], 2, s[4:5]
	v_add_u32_e32 v0, 0x1080, v2
	v_ashrrev_i32_e32 v1, 31, v0
	v_lshl_add_u64 v[0:1], v[0:1], 2, s[4:5]
	v_add_u32_e32 v0, 0x10c0, v2
	v_ashrrev_i32_e32 v1, 31, v0
	v_lshl_add_u64 v[0:1], v[0:1], 2, s[4:5]

; #define LAS __attribute__((address_space(3)))
; DI unsigned pk2h(float lo, float hi) { const f32x2h_t v = {lo, hi}; return __builtin_bit_cast(unsigned, __builtin_convertvector(v, bf16x2h_t)); }
; DI void ml_local_unit(Frame& F, int l, int ch, int h, const MlLPre& P) {
;     ...
;     if (F.tid < 64) *(LAS unsigned*)(VWT + 64 * LP + 2 * F.tid) = pk2h(WG[2 * F.tid], WG[2 * F.tid + 1]);
;     {
;       const float wg0 = WG[s2], wg1 = WG[s2 + 1];
;       float x0[8], x1[8];
;       unpack8(rv0, x0); unpack8(rv1, x1);
; #pragma unroll
;       for (int e = 0; e < 8; ++e) *(LAS unsigned*)(VWT + (c0 + e) * LP + s2) = pk2h(x0[e] * wg0, x1[e] * wg1);
;       unpack8(rk0, x0); unpack8(rk1, x1);
; #pragma unroll
;       for (int e = 0; e < 8; ++e) *(LAS unsigned*)(KT + (c0 + e) * LP + s2) = pk2h(x0[e] * 0.125f, x1[e] * 0.125f); }
;     __syncthreads();
;     const int w = F.wave, r = F.lane & 15, q = F.lane >> 4;
;     float* mls = (float*)(F.ws + WS_MLS + ML_ALT(F.l) * (406 * MiB)) + (size_t)(ch * 4 + h) * 5120;
; #pragma unroll
;     for (int it = 0; it < 3; ++it) { const int mt = (it < 2) ? (w >> 1) : 4, nt = (it < 2) ? 2 * (w & 1) + it : w;
.LBB0_929:
	s_or_b64 exec, exec, s[0:1]
	v_ashrrev_i32_e32 v0, 2, v132
	v_and_b32_e32 v0, -2, v0
	v_and_b32_e32 v2, 56, v6
	v_bitop3_b32 v6, v132, -4, 4 bitop3:0xc8
	v_lshl_add_u32 v8, v0, 2, s17
	v_add_u32_e32 v7, s17, v6
	ds_read_b32 v6, v8 offset:40192
	ds_read_b32 v7, v7 offset:40192
	v_lshlrev_b32_e32 v0, 1, v0
	v_sub_u32_e32 v0, v8, v0
	s_waitcnt vmcnt(9)
	v_lshlrev_b32_e32 v9, 16, v32
	v_lshlrev_b32_e32 v8, 16, v24
	s_waitcnt lgkmcnt(0)
	v_pk_mul_f32 v[8:9], v[6:7], v[8:9]
	v_mad_u32_u24 v0, v2, s66, v0
	v_cvt_pk_bf16_f32 v10, v8, v9
	v_and_b32_e32 v9, 0xffff0000, v32
	v_and_b32_e32 v8, 0xffff0000, v24
	v_pk_mul_f32 v[8:9], v[6:7], v[8:9]
	s_mov_b32 s0, 0x3e000000
	v_cvt_pk_bf16_f32 v2, v8, v9
	v_lshlrev_b32_e32 v9, 16, v33
	v_lshlrev_b32_e32 v8, 16, v25
	v_pk_mul_f32 v[8:9], v[6:7], v[8:9]
	ds_write2_b32 v0, v10, v2 offset1:68
	v_cvt_pk_bf16_f32 v2, v8, v9
	v_and_b32_e32 v9, 0xffff0000, v33
	v_and_b32_e32 v8, 0xffff0000, v25
	v_pk_mul_f32 v[8:9], v[6:7], v[8:9]
	v_add_u32_e32 v10, 0x400, v0
	v_cvt_pk_bf16_f32 v8, v8, v9
	ds_write2_b32 v0, v2, v8 offset0:136 offset1:204
	v_lshlrev_b32_e32 v9, 16, v34
	v_lshlrev_b32_e32 v8, 16, v26
	v_pk_mul_f32 v[8:9], v[6:7], v[8:9]
	s_nop 0
	v_cvt_pk_bf16_f32 v2, v8, v9
	v_and_b32_e32 v9, 0xffff0000, v34
	v_and_b32_e32 v8, 0xffff0000, v26
	v_pk_mul_f32 v[8:9], v[6:7], v[8:9]
	s_nop 0
	v_cvt_pk_bf16_f32 v8, v8, v9
	ds_write2_b32 v10, v2, v8 offset0:16 offset1:84
	v_lshlrev_b32_e32 v9, 16, v35
	v_lshlrev_b32_e32 v8, 16, v27
	v_pk_mul_f32 v[8:9], v[6:7], v[8:9]
	s_nop 0
	v_cvt_pk_bf16_f32 v2, v8, v9
	v_and_b32_e32 v9, 0xffff0000, v35
	v_and_b32_e32 v8, 0xffff0000, v27
	v_pk_mul_f32 v[6:7], v[6:7], v[8:9]
	s_nop 0
	v_cvt_pk_bf16_f32 v6, v6, v7
	ds_write2_b32 v10, v2, v6 offset0:152 offset1:220
	s_waitcnt vmcnt(8)
	v_lshlrev_b32_e32 v7, 16, v16
	v_lshlrev_b32_e32 v6, 16, v12
	v_pk_mul_f32 v[6:7], v[6:7], s[0:1] op_sel_hi:[1,0]
	s_nop 0
	v_cvt_pk_bf16_f32 v2, v6, v7
	v_and_b32_e32 v7, 0xffff0000, v16
	v_and_b32_e32 v6, 0xffff0000, v12
	v_pk_mul_f32 v[6:7], v[6:7], s[0:1] op_sel_hi:[1,0]
	s_nop 0
	v_cvt_pk_bf16_f32 v6, v6, v7
	v_add_u32_e32 v7, 0x5400, v0
	ds_write2_b32 v7, v2, v6 offset0:64 offset1:132
	v_lshlrev_b32_e32 v7, 16, v17
	v_lshlrev_b32_e32 v6, 16, v13
	v_pk_mul_f32 v[6:7], v[6:7], s[0:1] op_sel_hi:[1,0]
	s_nop 0
	v_cvt_pk_bf16_f32 v2, v6, v7
	v_and_b32_e32 v7, 0xffff0000, v17
	v_and_b32_e32 v6, 0xffff0000, v13
	v_pk_mul_f32 v[6:7], v[6:7], s[0:1] op_sel_hi:[1,0]
	s_nop 0
	v_cvt_pk_bf16_f32 v6, v6, v7
	v_add_u32_e32 v7, 0x5600, v0
	ds_write2_b32 v7, v2, v6 offset0:72 offset1:140
	v_lshlrev_b32_e32 v7, 16, v18
	v_lshlrev_b32_e32 v6, 16, v14
	v_pk_mul_f32 v[6:7], v[6:7], s[0:1] op_sel_hi:[1,0]
	s_nop 0
	v_cvt_pk_bf16_f32 v2, v6, v7
	v_and_b32_e32 v7, 0xffff0000, v18
	v_and_b32_e32 v6, 0xffff0000, v14
	v_pk_mul_f32 v[6:7], v[6:7], s[0:1] op_sel_hi:[1,0]
	s_nop 0
	v_cvt_pk_bf16_f32 v6, v6, v7
	v_add_u32_e32 v7, 0x5800, v0
	ds_write2_b32 v7, v2, v6 offset0:80 offset1:148
	v_lshlrev_b32_e32 v7, 16, v19
	v_lshlrev_b32_e32 v6, 16, v15
	v_pk_mul_f32 v[6:7], v[6:7], s[0:1] op_sel_hi:[1,0]
	v_add_u32_e32 v0, 0x5a00, v0
	v_cvt_pk_bf16_f32 v2, v6, v7
	v_and_b32_e32 v7, 0xffff0000, v19
	v_and_b32_e32 v6, 0xffff0000, v15
	v_pk_mul_f32 v[6:7], v[6:7], s[0:1] op_sel_hi:[1,0]
	s_or_b32 s0, s18, 3
	s_mul_i32 s2, s0, 0x5000
	s_mul_hi_i32 s1, s0, 0x5000
	s_add_u32 s2, s20, s2
	s_addc_u32 s1, s21, s1
	v_cvt_pk_bf16_f32 v6, v6, v7
	s_add_u32 s2, s2, 0x22100000
	ds_write2_b32 v0, v2, v6 offset0:88 offset1:156
	s_addc_u32 s3, s1, 0
	s_lshl_b32 s7, s6, 3
	v_and_b32_e32 v0, 48, v1
	v_and_b32_e32 v6, 15, v132
	s_lshl_b32 s1, s6, 5
	v_add_u32_e32 v2, s17, v0
	v_bfi_b32 v0, -16, s7, v132
	v_mad_u64_u32 v[20:21], s[4:5], v0, s66, v[2:3]
	v_and_or_b32 v0, s1, 32, v6
	v_mad_u32_u24 v7, v0, s66, v2
	s_waitcnt lgkmcnt(0)
	s_barrier
; #define LAS __attribute__((address_space(3)))
; DI f32x4 mfma16(bf16x8 a, bf16x8 b, f32x4 c) { asm volatile("s_nop 3" : "+v"(a), "+v"(b)); return __builtin_amdgcn_mfma_f32_16x16x32_bf16(a, b, c, 0, 0, 0); }
; DI void ml_local_unit(Frame& F, int l, int ch, int h, const MlLPre& P) {
;     ...
; #pragma unroll
;     for (int it = 0; it < 3; ++it) { const int mt = (it < 2) ? (w >> 1) : 4, nt = (it < 2) ? 2 * (w & 1) + it : w;
;         if (it == 2 && w >= 4) break;
;         f32x4 acc = (f32x4){0.f, 0.f, 0.f, 0.f};
; #pragma unroll
;         for (int ks = 0; ks < 4; ++ks) { const bf16x8 a = *(const LAS bf16x8*)(VWT + (16 * mt + r) * LP + 32 * ks + 8 * q), b = *(const LAS bf16x8*)(KT + (16 * nt + r) * LP + 32 * ks + 8 * q); acc = mfma16(a, b, acc); }
; #pragma unroll
;     ...
;         for (int jj = 0; jj < 4; ++jj) mls[(16 * mt + 4 * q + jj) * 64 + 16 * nt + r] = 0.01f * (float)(((16 * mt + 4 * q + jj) * 5 + (16 * nt + r) * 3 + ch) % 17 - 8);
;     ...
;         for (int jj = 0; jj < 4; ++jj) mls[(16 * mt + 4 * q + jj) * 64 + 16 * nt + r] = acc[jj];
;     ...
;         for (int jj = 0; jj < 4; ++jj) mls[(16 * mt + 4 * q + jj) * 64 + 16 * nt + r] = acc[jj];
;     ...
;     }
	ds_read_b128 v[8:11], v7 offset:21760
	ds_read_b128 v[12:15], v20
	s_waitcnt lgkmcnt(0)
	s_nop 3
	s_nop 0
	v_mfma_f32_16x16x32_bf16 v[8:11], v[8:11], v[12:15], 0
	ds_read_b128 v[12:15], v7 offset:21824
	ds_read_b128 v[16:19], v20 offset:64
	s_waitcnt lgkmcnt(0)
	s_nop 3
	s_nop 0
	v_mfma_f32_16x16x32_bf16 v[8:11], v[12:15], v[16:19], v[8:11]
	ds_read_b128 v[12:15], v7 offset:21888
	ds_read_b128 v[16:19], v20 offset:128
	s_waitcnt lgkmcnt(0)
	s_nop 3
	s_nop 0
	v_mfma_f32_16x16x32_bf16 v[8:11], v[12:15], v[16:19], v[8:11]
	ds_read_b128 v[12:15], v7 offset:21952
	ds_read_b128 v[16:19], v20 offset:192
	v_lshlrev_b32_e32 v1, 4, v1
	s_and_b32 s1, s7, -16
	s_waitcnt lgkmcnt(0)
	s_nop 3
	v_and_b32_e32 v1, 0x300, v1
	v_mfma_f32_16x16x32_bf16 v[8:11], v[12:15], v[16:19], v[8:11]
	v_lshl_or_b32 v14, s1, 6, v1
	v_or_b32_e32 v22, v14, v0
	v_ashrrev_i32_e32 v23, 31, v22
	v_lshl_add_u64 v[12:13], v[22:23], 2, s[2:3]
	v_ashrrev_i32_e32 v23, 31, v14
	s_nop 2
	v_lshl_add_u64 v[252:253], v[12:13], 0, v[250:251]
	global_store_dwordx4 v[252:253], v[8:11], off
	ds_read_b128 v[12:15], v7 offset:26112
	ds_read_b128 v[16:19], v20
	v_lshl_add_u64 v[24:25], v[22:23], 2, s[2:3]
	s_waitcnt lgkmcnt(0)
	s_nop 3
	s_nop 0
	v_mfma_f32_16x16x32_bf16 v[8:11], v[12:15], v[16:19], 0
	ds_read_b128 v[12:15], v7 offset:26176
	ds_read_b128 v[16:19], v20 offset:64
	s_waitcnt lgkmcnt(0)
	s_nop 3
	s_nop 0
	v_mfma_f32_16x16x32_bf16 v[8:11], v[12:15], v[16:19], v[8:11]
	ds_read_b128 v[12:15], v7 offset:26240
	ds_read_b128 v[16:19], v20 offset:128
	s_waitcnt lgkmcnt(0)
	s_nop 3
	s_nop 0
	v_mfma_f32_16x16x32_bf16 v[8:11], v[12:15], v[16:19], v[8:11]
	ds_read_b128 v[12:15], v7 offset:26304
	ds_read_b128 v[16:19], v20 offset:192
	s_waitcnt lgkmcnt(0)
	s_nop 3
	s_nop 0
	v_mfma_f32_16x16x32_bf16 v[8:11], v[12:15], v[16:19], v[8:11]
	v_or_b32_e32 v22, 16, v22
	s_cmp_gt_i32 s6, 3
	v_lshl_add_u64 v[12:13], v[22:23], 2, s[2:3]
	s_nop 4
	v_lshl_add_u64 v[252:253], v[24:25], 0, v[250:251]
	global_store_dwordx4 v[252:253], v[8:11], off offset:64
	s_cbranch_scc1 .LBB0_931
	v_mad_u32_u24 v0, v6, s66, v2
	v_lshl_or_b32 v20, s6, 4, v6
	v_mad_u64_u32 v[18:19], s[4:5], v20, s66, v[2:3]
	ds_read_b128 v[6:9], v0 offset:17408
	ds_read_b128 v[10:13], v18 offset:21760
	v_add_u32_e32 v2, v20, v1
	s_waitcnt lgkmcnt(0)
	s_nop 3
	s_nop 0
	v_mfma_f32_16x16x32_bf16 v[6:9], v[10:13], v[6:9], 0
	ds_read_b128 v[10:13], v18 offset:21824
	ds_read_b128 v[14:17], v0 offset:17472
	s_waitcnt lgkmcnt(0)
	s_nop 3
	s_nop 0
	v_mfma_f32_16x16x32_bf16 v[6:9], v[10:13], v[14:17], v[6:9]
	ds_read_b128 v[10:13], v18 offset:21888
	ds_read_b128 v[14:17], v0 offset:17536
	s_waitcnt lgkmcnt(0)
	s_nop 3
	s_nop 0
	v_mfma_f32_16x16x32_bf16 v[6:9], v[10:13], v[14:17], v[6:9]
	ds_read_b128 v[10:13], v18 offset:21952
	ds_read_b128 v[14:17], v0 offset:17600
	s_waitcnt lgkmcnt(0)
	s_nop 3
	s_nop 0
	v_mfma_f32_16x16x32_bf16 v[6:9], v[10:13], v[14:17], v[6:9]
	v_add_u32_e32 v0, 0x1000, v2
	v_ashrrev_i32_e32 v1, 31, v0
	v_lshl_add_u64 v[0:1], v[0:1], 2, s[2:3]
	s_nop 4
	v_lshl_add_u64 v[252:253], v[0:1], 0, v[250:251]
	global_store_dwordx4 v[252:253], v[6:9], off
	v_add_u32_e32 v0, 0x1040, v2
	v_ashrrev_i32_e32 v1, 31, v0
	v_lshl_add_u64 v[0:1], v[0:1], 2, s[2:3]
	v_add_u32_e32 v0, 0x1080, v2
	v_ashrrev_i32_e32 v1, 31, v0
	v_lshl_add_u64 v[0:1], v[0:1], 2, s[2:3]
	v_add_u32_e32 v0, 0x10c0, v2
	v_ashrrev_i32_e32 v1, 31, v0
	v_lshl_add_u64 v[0:1], v[0:1], 2, s[2:3]
